# all per-phase s_setprio flips in the six GEMM K-loops deleted (attention's static raise kept)
# speedup vs baseline: 1.0042x; 1.0042x over previous
.Lpeel_inproj:
	s_add_u32 s28, s76, 0xfffc0080
	s_addc_u32 s29, s77, -1
	s_add_i32 s30, 0, 0x10000
	s_cmp_eq_u32 s71, 12
	s_cselect_b32 s83, s36, s29
	s_cselect_b32 s82, s37, s28
	v_add_u32_e32 v112, s30, v153
	s_cselect_b32 s81, s43, s65
	s_cselect_b32 s80, s50, s51
	s_add_i32 s31, 0, 0x14000
	ds_read_b128 v[130:133], v112
	ds_read_b128 v[134:137], v112 offset:1024
	ds_read_b128 v[156:159], v112 offset:2048
	ds_read_b128 v[160:163], v112 offset:3072
	v_add_u32_e32 v112, s31, v153
	ds_read_b128 v[164:167], v112
	ds_read_b128 v[168:171], v112 offset:1024
	ds_read_b128 v[172:175], v112 offset:2048
	ds_read_b128 v[176:179], v112 offset:3072
	v_lshl_add_u64 v[150:151], s[76:77], 0, v[146:147]
	s_add_i32 m0, s26, 0xc000
	ds_read_b128 v[180:183], v154
	ds_read_b128 v[184:187], v154 offset:1024
	ds_read_b128 v[188:191], v154 offset:2048
	ds_read_b128 v[192:195], v154 offset:3072
	ds_read_b128 v[206:209], v154 offset:4096
	ds_read_b128 v[210:213], v154 offset:5120
	ds_read_b128 v[216:219], v154 offset:6144
	ds_read_b128 v[220:223], v154 offset:7168
	global_load_lds_dwordx4 v[150:151], off
	v_lshl_add_u64 v[150:151], s[76:77], 0, v[148:149]
	s_add_i32 m0, s26, 0xe000
	s_nop 0
	global_load_lds_dwordx4 v[150:151], off
	s_waitcnt vmcnt(8)
	s_waitcnt lgkmcnt(0)
	s_barrier
	s_waitcnt lgkmcnt(0)
	v_mfma_f32_16x16x32_bf16 v[126:129], v[130:133], v[180:183], 0
	v_mfma_f32_16x16x32_bf16 v[122:125], v[156:159], v[180:183], 0
	v_mfma_f32_16x16x32_bf16 v[118:121], v[130:133], v[188:191], 0
	v_mfma_f32_16x16x32_bf16 v[114:117], v[156:159], v[188:191], 0
	v_mfma_f32_16x16x32_bf16 v[100:103], v[130:133], v[206:209], 0
	v_mfma_f32_16x16x32_bf16 v[96:99], v[156:159], v[206:209], 0
	v_mfma_f32_16x16x32_bf16 v[84:87], v[130:133], v[216:219], 0
	v_mfma_f32_16x16x32_bf16 v[80:83], v[156:159], v[216:219], 0
	v_mfma_f32_16x16x32_bf16 v[126:129], v[134:137], v[184:187], v[126:129]
	v_mfma_f32_16x16x32_bf16 v[122:125], v[160:163], v[184:187], v[122:125]
	v_mfma_f32_16x16x32_bf16 v[118:121], v[134:137], v[192:195], v[118:121]
	v_mfma_f32_16x16x32_bf16 v[114:117], v[160:163], v[192:195], v[114:117]
	v_mfma_f32_16x16x32_bf16 v[100:103], v[134:137], v[210:213], v[100:103]
	v_mfma_f32_16x16x32_bf16 v[96:99], v[160:163], v[210:213], v[96:99]
	v_mfma_f32_16x16x32_bf16 v[84:87], v[134:137], v[220:223], v[84:87]
	v_mfma_f32_16x16x32_bf16 v[80:83], v[160:163], v[220:223], v[80:83]
	v_mfma_f32_16x16x32_bf16 v[108:111], v[164:167], v[180:183], 0
	v_mfma_f32_16x16x32_bf16 v[104:107], v[172:175], v[180:183], 0
	v_mfma_f32_16x16x32_bf16 v[92:95], v[164:167], v[188:191], 0
	v_mfma_f32_16x16x32_bf16 v[88:91], v[172:175], v[188:191], 0
	v_mfma_f32_16x16x32_bf16 v[76:79], v[164:167], v[206:209], 0
	v_mfma_f32_16x16x32_bf16 v[72:75], v[172:175], v[206:209], 0
	v_mfma_f32_16x16x32_bf16 v[68:71], v[164:167], v[216:219], 0
	v_mfma_f32_16x16x32_bf16 v[64:67], v[172:175], v[216:219], 0
	v_mfma_f32_16x16x32_bf16 v[108:111], v[168:171], v[184:187], v[108:111]
	v_mfma_f32_16x16x32_bf16 v[104:107], v[176:179], v[184:187], v[104:107]
	v_mfma_f32_16x16x32_bf16 v[92:95], v[168:171], v[192:195], v[92:95]
	v_mfma_f32_16x16x32_bf16 v[88:91], v[176:179], v[192:195], v[88:91]
	v_mfma_f32_16x16x32_bf16 v[76:79], v[168:171], v[210:213], v[76:79]
	v_mfma_f32_16x16x32_bf16 v[72:75], v[176:179], v[210:213], v[72:75]
	v_mfma_f32_16x16x32_bf16 v[68:71], v[168:171], v[220:223], v[68:71]
	v_mfma_f32_16x16x32_bf16 v[64:67], v[176:179], v[220:223], v[64:67]
	s_barrier
	s_add_i32 s28, s30, s13
	v_lshl_add_u64 v[150:151], s[80:81], 0, v[140:141]
	s_mov_b32 m0, s28
	ds_read_b128 v[180:183], v154 offset:16384
	ds_read_b128 v[184:187], v154 offset:17408
	ds_read_b128 v[188:191], v154 offset:18432
	ds_read_b128 v[192:195], v154 offset:19456
	ds_read_b128 v[206:209], v154 offset:20480
	ds_read_b128 v[210:213], v154 offset:21504
	ds_read_b128 v[216:219], v154 offset:22528
	ds_read_b128 v[220:223], v154 offset:23552
	global_load_lds_dwordx4 v[150:151], off
	s_add_i32 m0, s28, 0x2000
	s_add_u32 s28, s80, 0x40000
	v_lshl_add_u64 v[224:225], s[80:81], 0, v[144:145]
	s_addc_u32 s29, s81, 0
	s_add_i32 s30, s31, s13
	global_load_lds_dwordx4 v[224:225], off
	v_lshl_add_u64 v[226:227], s[28:29], 0, v[140:141]
	s_mov_b32 m0, s30
	v_lshl_add_u64 v[228:229], s[82:83], 0, v[142:143]
	global_load_lds_dwordx4 v[226:227], off
	v_lshl_add_u64 v[226:227], s[28:29], 0, v[144:145]
	s_add_i32 m0, s30, 0x2000
	s_nop 0
	global_load_lds_dwordx4 v[226:227], off
	v_lshl_add_u64 v[226:227], s[82:83], 0, v[138:139]
	s_mov_b32 m0, s26
	s_nop 0
	global_load_lds_dwordx4 v[226:227], off
	s_mov_b32 m0, s27
	s_nop 0
	global_load_lds_dwordx4 v[228:229], off
	s_waitcnt vmcnt(8)
	s_waitcnt lgkmcnt(0)
	s_barrier
	s_waitcnt lgkmcnt(0)
	v_mfma_f32_16x16x32_bf16 v[60:63], v[130:133], v[180:183], 0
	v_mfma_f32_16x16x32_bf16 v[56:59], v[156:159], v[180:183], 0
	v_mfma_f32_16x16x32_bf16 v[52:55], v[130:133], v[188:191], 0
	v_mfma_f32_16x16x32_bf16 v[48:51], v[156:159], v[188:191], 0
	v_mfma_f32_16x16x32_bf16 v[36:39], v[130:133], v[206:209], 0
	v_mfma_f32_16x16x32_bf16 v[32:35], v[156:159], v[206:209], 0
	v_mfma_f32_16x16x32_bf16 v[20:23], v[130:133], v[216:219], 0
	v_mfma_f32_16x16x32_bf16 v[16:19], v[156:159], v[216:219], 0
	v_mfma_f32_16x16x32_bf16 v[60:63], v[134:137], v[184:187], v[60:63]
	v_mfma_f32_16x16x32_bf16 v[56:59], v[160:163], v[184:187], v[56:59]
	v_mfma_f32_16x16x32_bf16 v[52:55], v[134:137], v[192:195], v[52:55]
	v_mfma_f32_16x16x32_bf16 v[48:51], v[160:163], v[192:195], v[48:51]
	v_mfma_f32_16x16x32_bf16 v[36:39], v[134:137], v[210:213], v[36:39]
	v_mfma_f32_16x16x32_bf16 v[32:35], v[160:163], v[210:213], v[32:35]
	v_mfma_f32_16x16x32_bf16 v[20:23], v[134:137], v[220:223], v[20:23]
	v_mfma_f32_16x16x32_bf16 v[16:19], v[160:163], v[220:223], v[16:19]
	v_mfma_f32_16x16x32_bf16 v[44:47], v[164:167], v[180:183], 0
	v_mfma_f32_16x16x32_bf16 v[40:43], v[172:175], v[180:183], 0
	v_mfma_f32_16x16x32_bf16 v[28:31], v[164:167], v[188:191], 0
	v_mfma_f32_16x16x32_bf16 v[24:27], v[172:175], v[188:191], 0
	v_mfma_f32_16x16x32_bf16 v[12:15], v[164:167], v[206:209], 0
	v_mfma_f32_16x16x32_bf16 v[8:11], v[172:175], v[206:209], 0
	v_mfma_f32_16x16x32_bf16 v[4:7], v[164:167], v[216:219], 0
	v_mfma_f32_16x16x32_bf16 v[0:3], v[172:175], v[216:219], 0
	v_mfma_f32_16x16x32_bf16 v[44:47], v[168:171], v[184:187], v[44:47]
	v_mfma_f32_16x16x32_bf16 v[40:43], v[176:179], v[184:187], v[40:43]
	v_mfma_f32_16x16x32_bf16 v[28:31], v[168:171], v[192:195], v[28:31]
	v_mfma_f32_16x16x32_bf16 v[24:27], v[176:179], v[192:195], v[24:27]
	v_mfma_f32_16x16x32_bf16 v[12:15], v[168:171], v[210:213], v[12:15]
	v_mfma_f32_16x16x32_bf16 v[8:11], v[176:179], v[210:213], v[8:11]
	v_mfma_f32_16x16x32_bf16 v[4:7], v[168:171], v[220:223], v[4:7]
	v_mfma_f32_16x16x32_bf16 v[0:3], v[176:179], v[220:223], v[0:3]
	s_barrier
	s_add_i32 s30, 0, 0x18000
	v_add_u32_e32 v112, s30, v153
	s_add_i32 s31, 0, 0x1c000
	ds_read_b128 v[130:133], v112
	ds_read_b128 v[134:137], v112 offset:1024
	ds_read_b128 v[156:159], v112 offset:2048
	ds_read_b128 v[160:163], v112 offset:3072
	v_add_u32_e32 v112, s31, v153
	ds_read_b128 v[164:167], v112
	ds_read_b128 v[168:171], v112 offset:1024
	ds_read_b128 v[172:175], v112 offset:2048
	ds_read_b128 v[176:179], v112 offset:3072
	s_add_u32 s28, s82, 0x40000
	s_addc_u32 s29, s83, 0
	s_mov_b32 m0, s34
	v_lshl_add_u64 v[230:231], s[28:29], 0, v[138:139]
	ds_read_b128 v[180:183], v154 offset:32768
	ds_read_b128 v[184:187], v154 offset:33792
	ds_read_b128 v[188:191], v154 offset:34816
	ds_read_b128 v[192:195], v154 offset:35840
	ds_read_b128 v[206:209], v154 offset:36864
	ds_read_b128 v[210:213], v154 offset:37888
	ds_read_b128 v[216:219], v154 offset:38912
	ds_read_b128 v[220:223], v154 offset:39936
	global_load_lds_dwordx4 v[230:231], off
	v_lshl_add_u64 v[230:231], s[28:29], 0, v[142:143]
	s_mov_b32 m0, s14
	s_nop 0
	global_load_lds_dwordx4 v[230:231], off
	s_waitcnt vmcnt(8)
	s_waitcnt lgkmcnt(0)
	s_barrier
	s_waitcnt lgkmcnt(0)
	v_mfma_f32_16x16x32_bf16 v[126:129], v[130:133], v[180:183], v[126:129]
	v_mfma_f32_16x16x32_bf16 v[122:125], v[156:159], v[180:183], v[122:125]
	v_mfma_f32_16x16x32_bf16 v[118:121], v[130:133], v[188:191], v[118:121]
	v_mfma_f32_16x16x32_bf16 v[114:117], v[156:159], v[188:191], v[114:117]
	v_mfma_f32_16x16x32_bf16 v[100:103], v[130:133], v[206:209], v[100:103]
	v_mfma_f32_16x16x32_bf16 v[96:99], v[156:159], v[206:209], v[96:99]
	v_mfma_f32_16x16x32_bf16 v[84:87], v[130:133], v[216:219], v[84:87]
	v_mfma_f32_16x16x32_bf16 v[80:83], v[156:159], v[216:219], v[80:83]
	v_mfma_f32_16x16x32_bf16 v[126:129], v[134:137], v[184:187], v[126:129]
	v_mfma_f32_16x16x32_bf16 v[122:125], v[160:163], v[184:187], v[122:125]
	v_mfma_f32_16x16x32_bf16 v[118:121], v[134:137], v[192:195], v[118:121]
	v_mfma_f32_16x16x32_bf16 v[114:117], v[160:163], v[192:195], v[114:117]
	v_mfma_f32_16x16x32_bf16 v[100:103], v[134:137], v[210:213], v[100:103]
	v_mfma_f32_16x16x32_bf16 v[96:99], v[160:163], v[210:213], v[96:99]
	v_mfma_f32_16x16x32_bf16 v[84:87], v[134:137], v[220:223], v[84:87]
	v_mfma_f32_16x16x32_bf16 v[80:83], v[160:163], v[220:223], v[80:83]
	v_mfma_f32_16x16x32_bf16 v[108:111], v[164:167], v[180:183], v[108:111]
	v_mfma_f32_16x16x32_bf16 v[104:107], v[172:175], v[180:183], v[104:107]
	v_mfma_f32_16x16x32_bf16 v[92:95], v[164:167], v[188:191], v[92:95]
	v_mfma_f32_16x16x32_bf16 v[88:91], v[172:175], v[188:191], v[88:91]
	v_mfma_f32_16x16x32_bf16 v[76:79], v[164:167], v[206:209], v[76:79]
	v_mfma_f32_16x16x32_bf16 v[72:75], v[172:175], v[206:209], v[72:75]
	v_mfma_f32_16x16x32_bf16 v[68:71], v[164:167], v[216:219], v[68:71]
	v_mfma_f32_16x16x32_bf16 v[64:67], v[172:175], v[216:219], v[64:67]
	v_mfma_f32_16x16x32_bf16 v[108:111], v[168:171], v[184:187], v[108:111]
	v_mfma_f32_16x16x32_bf16 v[104:107], v[176:179], v[184:187], v[104:107]
	v_mfma_f32_16x16x32_bf16 v[92:95], v[168:171], v[192:195], v[92:95]
	v_mfma_f32_16x16x32_bf16 v[88:91], v[176:179], v[192:195], v[88:91]
	v_mfma_f32_16x16x32_bf16 v[76:79], v[168:171], v[210:213], v[76:79]
	v_mfma_f32_16x16x32_bf16 v[72:75], v[176:179], v[210:213], v[72:75]
	v_mfma_f32_16x16x32_bf16 v[68:71], v[168:171], v[220:223], v[68:71]
	v_mfma_f32_16x16x32_bf16 v[64:67], v[176:179], v[220:223], v[64:67]
	s_barrier
	s_add_i32 s28, s30, s13
	v_lshl_add_u64 v[150:151], v[150:151], 0, s[56:57]
	s_mov_b32 m0, s28
	ds_read_b128 v[180:183], v154 offset:49152
	ds_read_b128 v[184:187], v154 offset:50176
	ds_read_b128 v[188:191], v154 offset:51200
	ds_read_b128 v[192:195], v154 offset:52224
	ds_read_b128 v[206:209], v154 offset:53248
	ds_read_b128 v[210:213], v154 offset:54272
	ds_read_b128 v[216:219], v154 offset:55296
	ds_read_b128 v[220:223], v154 offset:56320
	global_load_lds_dwordx4 v[150:151], off
	s_add_i32 m0, s28, 0x2000
	s_add_u32 s28, s80, 0x40080
	v_lshl_add_u64 v[150:151], v[224:225], 0, s[56:57]
	s_addc_u32 s29, s81, 0
	s_add_i32 s30, s31, s13
	global_load_lds_dwordx4 v[150:151], off
	v_lshl_add_u64 v[150:151], s[28:29], 0, v[140:141]
	s_mov_b32 m0, s30
	s_nop 0
	global_load_lds_dwordx4 v[150:151], off
	v_lshl_add_u64 v[150:151], s[28:29], 0, v[144:145]
	s_add_i32 m0, s30, 0x2000
	s_nop 0
	global_load_lds_dwordx4 v[150:151], off
	v_lshl_add_u64 v[150:151], v[226:227], 0, s[56:57]
	s_mov_b32 m0, s33
	s_nop 0
	global_load_lds_dwordx4 v[150:151], off
	v_lshl_add_u64 v[150:151], v[228:229], 0, s[56:57]
	s_mov_b32 m0, s69
	s_nop 0
	global_load_lds_dwordx4 v[150:151], off
	s_waitcnt vmcnt(8)
	s_waitcnt lgkmcnt(0)
	s_barrier
	s_waitcnt lgkmcnt(0)
	v_mfma_f32_16x16x32_bf16 v[60:63], v[130:133], v[180:183], v[60:63]
	v_mfma_f32_16x16x32_bf16 v[56:59], v[156:159], v[180:183], v[56:59]
	v_mfma_f32_16x16x32_bf16 v[52:55], v[130:133], v[188:191], v[52:55]
	v_mfma_f32_16x16x32_bf16 v[48:51], v[156:159], v[188:191], v[48:51]
	v_mfma_f32_16x16x32_bf16 v[36:39], v[130:133], v[206:209], v[36:39]
	v_mfma_f32_16x16x32_bf16 v[32:35], v[156:159], v[206:209], v[32:35]
	v_mfma_f32_16x16x32_bf16 v[20:23], v[130:133], v[216:219], v[20:23]
	v_mfma_f32_16x16x32_bf16 v[16:19], v[156:159], v[216:219], v[16:19]
	v_mfma_f32_16x16x32_bf16 v[60:63], v[134:137], v[184:187], v[60:63]
	v_mfma_f32_16x16x32_bf16 v[56:59], v[160:163], v[184:187], v[56:59]
	v_mfma_f32_16x16x32_bf16 v[52:55], v[134:137], v[192:195], v[52:55]
	v_mfma_f32_16x16x32_bf16 v[48:51], v[160:163], v[192:195], v[48:51]
	v_mfma_f32_16x16x32_bf16 v[36:39], v[134:137], v[210:213], v[36:39]
	v_mfma_f32_16x16x32_bf16 v[32:35], v[160:163], v[210:213], v[32:35]
	v_mfma_f32_16x16x32_bf16 v[20:23], v[134:137], v[220:223], v[20:23]
	v_mfma_f32_16x16x32_bf16 v[16:19], v[160:163], v[220:223], v[16:19]
	v_mfma_f32_16x16x32_bf16 v[44:47], v[164:167], v[180:183], v[44:47]
	v_mfma_f32_16x16x32_bf16 v[40:43], v[172:175], v[180:183], v[40:43]
	v_mfma_f32_16x16x32_bf16 v[28:31], v[164:167], v[188:191], v[28:31]
	v_mfma_f32_16x16x32_bf16 v[24:27], v[172:175], v[188:191], v[24:27]
	v_mfma_f32_16x16x32_bf16 v[12:15], v[164:167], v[206:209], v[12:15]
	v_mfma_f32_16x16x32_bf16 v[8:11], v[172:175], v[206:209], v[8:11]
	v_mfma_f32_16x16x32_bf16 v[4:7], v[164:167], v[216:219], v[4:7]
	v_mfma_f32_16x16x32_bf16 v[0:3], v[172:175], v[216:219], v[0:3]
	v_mfma_f32_16x16x32_bf16 v[44:47], v[168:171], v[184:187], v[44:47]
	v_mfma_f32_16x16x32_bf16 v[40:43], v[176:179], v[184:187], v[40:43]
	v_mfma_f32_16x16x32_bf16 v[28:31], v[168:171], v[192:195], v[28:31]
	v_mfma_f32_16x16x32_bf16 v[24:27], v[176:179], v[192:195], v[24:27]
	v_mfma_f32_16x16x32_bf16 v[12:15], v[168:171], v[210:213], v[12:15]
	v_mfma_f32_16x16x32_bf16 v[8:11], v[176:179], v[210:213], v[8:11]
	v_mfma_f32_16x16x32_bf16 v[4:7], v[168:171], v[220:223], v[4:7]
	v_mfma_f32_16x16x32_bf16 v[0:3], v[176:179], v[220:223], v[0:3]
	s_barrier
	s_add_i32 s71, s71, 2
	s_add_u32 s76, s76, 0x100
	s_addc_u32 s77, s77, 0
	s_add_u32 s51, s51, 0x100
	s_addc_u32 s65, s65, 0
	s_cmp_gt_u32 s71, 13
.LBB0_264:
	s_add_u32 s28, s76, 0xfffc0080
	s_addc_u32 s29, s77, -1
	s_add_i32 s30, 0, 0x10000
	s_cmp_eq_u32 s71, 12
	s_cselect_b32 s83, s36, s29
	s_cselect_b32 s82, s37, s28
	v_add_u32_e32 v112, s30, v153
	s_cselect_b32 s81, s43, s65
	s_cselect_b32 s80, s50, s51
	s_add_i32 s31, 0, 0x14000
	ds_read_b128 v[130:133], v112
	ds_read_b128 v[134:137], v112 offset:1024
	ds_read_b128 v[156:159], v112 offset:2048
	ds_read_b128 v[160:163], v112 offset:3072
	v_add_u32_e32 v112, s31, v153
	ds_read_b128 v[164:167], v112
	ds_read_b128 v[168:171], v112 offset:1024
	ds_read_b128 v[172:175], v112 offset:2048
	ds_read_b128 v[176:179], v112 offset:3072
	v_lshl_add_u64 v[150:151], s[76:77], 0, v[146:147]
	s_add_i32 m0, s26, 0xc000
	ds_read_b128 v[180:183], v154
	ds_read_b128 v[184:187], v154 offset:1024
	ds_read_b128 v[188:191], v154 offset:2048
	ds_read_b128 v[192:195], v154 offset:3072
	ds_read_b128 v[206:209], v154 offset:4096
	ds_read_b128 v[210:213], v154 offset:5120
	ds_read_b128 v[216:219], v154 offset:6144
	ds_read_b128 v[220:223], v154 offset:7168
	global_load_lds_dwordx4 v[150:151], off
	v_lshl_add_u64 v[150:151], s[76:77], 0, v[148:149]
	s_add_i32 m0, s26, 0xe000
	s_nop 0
	global_load_lds_dwordx4 v[150:151], off
	s_waitcnt vmcnt(8)
	s_waitcnt lgkmcnt(0)
	s_barrier
	s_waitcnt lgkmcnt(0)
	v_mfma_f32_16x16x32_bf16 v[126:129], v[130:133], v[180:183], v[126:129]
	v_mfma_f32_16x16x32_bf16 v[122:125], v[156:159], v[180:183], v[122:125]
	v_mfma_f32_16x16x32_bf16 v[118:121], v[130:133], v[188:191], v[118:121]
	v_mfma_f32_16x16x32_bf16 v[114:117], v[156:159], v[188:191], v[114:117]
	v_mfma_f32_16x16x32_bf16 v[100:103], v[130:133], v[206:209], v[100:103]
	v_mfma_f32_16x16x32_bf16 v[96:99], v[156:159], v[206:209], v[96:99]
	v_mfma_f32_16x16x32_bf16 v[84:87], v[130:133], v[216:219], v[84:87]
	v_mfma_f32_16x16x32_bf16 v[80:83], v[156:159], v[216:219], v[80:83]
	v_mfma_f32_16x16x32_bf16 v[126:129], v[134:137], v[184:187], v[126:129]
	v_mfma_f32_16x16x32_bf16 v[122:125], v[160:163], v[184:187], v[122:125]
	v_mfma_f32_16x16x32_bf16 v[118:121], v[134:137], v[192:195], v[118:121]
	v_mfma_f32_16x16x32_bf16 v[114:117], v[160:163], v[192:195], v[114:117]
	v_mfma_f32_16x16x32_bf16 v[100:103], v[134:137], v[210:213], v[100:103]
	v_mfma_f32_16x16x32_bf16 v[96:99], v[160:163], v[210:213], v[96:99]
	v_mfma_f32_16x16x32_bf16 v[84:87], v[134:137], v[220:223], v[84:87]
	v_mfma_f32_16x16x32_bf16 v[80:83], v[160:163], v[220:223], v[80:83]
	v_mfma_f32_16x16x32_bf16 v[108:111], v[164:167], v[180:183], v[108:111]
	v_mfma_f32_16x16x32_bf16 v[104:107], v[172:175], v[180:183], v[104:107]
	v_mfma_f32_16x16x32_bf16 v[92:95], v[164:167], v[188:191], v[92:95]
	v_mfma_f32_16x16x32_bf16 v[88:91], v[172:175], v[188:191], v[88:91]
	v_mfma_f32_16x16x32_bf16 v[76:79], v[164:167], v[206:209], v[76:79]
	v_mfma_f32_16x16x32_bf16 v[72:75], v[172:175], v[206:209], v[72:75]
	v_mfma_f32_16x16x32_bf16 v[68:71], v[164:167], v[216:219], v[68:71]
	v_mfma_f32_16x16x32_bf16 v[64:67], v[172:175], v[216:219], v[64:67]
	v_mfma_f32_16x16x32_bf16 v[108:111], v[168:171], v[184:187], v[108:111]
	v_mfma_f32_16x16x32_bf16 v[104:107], v[176:179], v[184:187], v[104:107]
	v_mfma_f32_16x16x32_bf16 v[92:95], v[168:171], v[192:195], v[92:95]
	v_mfma_f32_16x16x32_bf16 v[88:91], v[176:179], v[192:195], v[88:91]
	v_mfma_f32_16x16x32_bf16 v[76:79], v[168:171], v[210:213], v[76:79]
	v_mfma_f32_16x16x32_bf16 v[72:75], v[176:179], v[210:213], v[72:75]
	v_mfma_f32_16x16x32_bf16 v[68:71], v[168:171], v[220:223], v[68:71]
	v_mfma_f32_16x16x32_bf16 v[64:67], v[176:179], v[220:223], v[64:67]
	s_barrier
	s_add_i32 s28, s30, s13
	v_lshl_add_u64 v[150:151], s[80:81], 0, v[140:141]
	s_mov_b32 m0, s28
	ds_read_b128 v[180:183], v154 offset:16384
	ds_read_b128 v[184:187], v154 offset:17408
	ds_read_b128 v[188:191], v154 offset:18432
	ds_read_b128 v[192:195], v154 offset:19456
	ds_read_b128 v[206:209], v154 offset:20480
	ds_read_b128 v[210:213], v154 offset:21504
	ds_read_b128 v[216:219], v154 offset:22528
	ds_read_b128 v[220:223], v154 offset:23552
	global_load_lds_dwordx4 v[150:151], off
	s_add_i32 m0, s28, 0x2000
	s_add_u32 s28, s80, 0x40000
	v_lshl_add_u64 v[224:225], s[80:81], 0, v[144:145]
	s_addc_u32 s29, s81, 0
	s_add_i32 s30, s31, s13
	global_load_lds_dwordx4 v[224:225], off
	v_lshl_add_u64 v[226:227], s[28:29], 0, v[140:141]
	s_mov_b32 m0, s30
	v_lshl_add_u64 v[228:229], s[82:83], 0, v[142:143]
	global_load_lds_dwordx4 v[226:227], off
	v_lshl_add_u64 v[226:227], s[28:29], 0, v[144:145]
	s_add_i32 m0, s30, 0x2000
	s_nop 0
	global_load_lds_dwordx4 v[226:227], off
	v_lshl_add_u64 v[226:227], s[82:83], 0, v[138:139]
	s_mov_b32 m0, s26
	s_nop 0
	global_load_lds_dwordx4 v[226:227], off
	s_mov_b32 m0, s27
	s_nop 0
	global_load_lds_dwordx4 v[228:229], off
	s_waitcnt vmcnt(8)
	s_waitcnt lgkmcnt(0)
	s_barrier
	s_waitcnt lgkmcnt(0)
	v_mfma_f32_16x16x32_bf16 v[60:63], v[130:133], v[180:183], v[60:63]
	v_mfma_f32_16x16x32_bf16 v[56:59], v[156:159], v[180:183], v[56:59]
	v_mfma_f32_16x16x32_bf16 v[52:55], v[130:133], v[188:191], v[52:55]
	v_mfma_f32_16x16x32_bf16 v[48:51], v[156:159], v[188:191], v[48:51]
	v_mfma_f32_16x16x32_bf16 v[36:39], v[130:133], v[206:209], v[36:39]
	v_mfma_f32_16x16x32_bf16 v[32:35], v[156:159], v[206:209], v[32:35]
	v_mfma_f32_16x16x32_bf16 v[20:23], v[130:133], v[216:219], v[20:23]
	v_mfma_f32_16x16x32_bf16 v[16:19], v[156:159], v[216:219], v[16:19]
	v_mfma_f32_16x16x32_bf16 v[60:63], v[134:137], v[184:187], v[60:63]
	v_mfma_f32_16x16x32_bf16 v[56:59], v[160:163], v[184:187], v[56:59]
	v_mfma_f32_16x16x32_bf16 v[52:55], v[134:137], v[192:195], v[52:55]
	v_mfma_f32_16x16x32_bf16 v[48:51], v[160:163], v[192:195], v[48:51]
	v_mfma_f32_16x16x32_bf16 v[36:39], v[134:137], v[210:213], v[36:39]
	v_mfma_f32_16x16x32_bf16 v[32:35], v[160:163], v[210:213], v[32:35]
	v_mfma_f32_16x16x32_bf16 v[20:23], v[134:137], v[220:223], v[20:23]
	v_mfma_f32_16x16x32_bf16 v[16:19], v[160:163], v[220:223], v[16:19]
	v_mfma_f32_16x16x32_bf16 v[44:47], v[164:167], v[180:183], v[44:47]
	v_mfma_f32_16x16x32_bf16 v[40:43], v[172:175], v[180:183], v[40:43]
	v_mfma_f32_16x16x32_bf16 v[28:31], v[164:167], v[188:191], v[28:31]
	v_mfma_f32_16x16x32_bf16 v[24:27], v[172:175], v[188:191], v[24:27]
	v_mfma_f32_16x16x32_bf16 v[12:15], v[164:167], v[206:209], v[12:15]
	v_mfma_f32_16x16x32_bf16 v[8:11], v[172:175], v[206:209], v[8:11]
	v_mfma_f32_16x16x32_bf16 v[4:7], v[164:167], v[216:219], v[4:7]
	v_mfma_f32_16x16x32_bf16 v[0:3], v[172:175], v[216:219], v[0:3]
	v_mfma_f32_16x16x32_bf16 v[44:47], v[168:171], v[184:187], v[44:47]
	v_mfma_f32_16x16x32_bf16 v[40:43], v[176:179], v[184:187], v[40:43]
	v_mfma_f32_16x16x32_bf16 v[28:31], v[168:171], v[192:195], v[28:31]
	v_mfma_f32_16x16x32_bf16 v[24:27], v[176:179], v[192:195], v[24:27]
	v_mfma_f32_16x16x32_bf16 v[12:15], v[168:171], v[210:213], v[12:15]
	v_mfma_f32_16x16x32_bf16 v[8:11], v[176:179], v[210:213], v[8:11]
	v_mfma_f32_16x16x32_bf16 v[4:7], v[168:171], v[220:223], v[4:7]
	v_mfma_f32_16x16x32_bf16 v[0:3], v[176:179], v[220:223], v[0:3]
	s_barrier
	s_add_i32 s30, 0, 0x18000
	v_add_u32_e32 v112, s30, v153
	s_add_i32 s31, 0, 0x1c000
	ds_read_b128 v[130:133], v112
	ds_read_b128 v[134:137], v112 offset:1024
	ds_read_b128 v[156:159], v112 offset:2048
	ds_read_b128 v[160:163], v112 offset:3072
	v_add_u32_e32 v112, s31, v153
	ds_read_b128 v[164:167], v112
	ds_read_b128 v[168:171], v112 offset:1024
	ds_read_b128 v[172:175], v112 offset:2048
	ds_read_b128 v[176:179], v112 offset:3072
	s_add_u32 s28, s82, 0x40000
	s_addc_u32 s29, s83, 0
	s_mov_b32 m0, s34
	v_lshl_add_u64 v[230:231], s[28:29], 0, v[138:139]
	ds_read_b128 v[180:183], v154 offset:32768
	ds_read_b128 v[184:187], v154 offset:33792
	ds_read_b128 v[188:191], v154 offset:34816
	ds_read_b128 v[192:195], v154 offset:35840
	ds_read_b128 v[206:209], v154 offset:36864
	ds_read_b128 v[210:213], v154 offset:37888
	ds_read_b128 v[216:219], v154 offset:38912
	ds_read_b128 v[220:223], v154 offset:39936
	global_load_lds_dwordx4 v[230:231], off
	v_lshl_add_u64 v[230:231], s[28:29], 0, v[142:143]
	s_mov_b32 m0, s14
	s_nop 0
	global_load_lds_dwordx4 v[230:231], off
	s_waitcnt vmcnt(8)
	s_waitcnt lgkmcnt(0)
	s_barrier
	s_waitcnt lgkmcnt(0)
	v_mfma_f32_16x16x32_bf16 v[126:129], v[130:133], v[180:183], v[126:129]
	v_mfma_f32_16x16x32_bf16 v[122:125], v[156:159], v[180:183], v[122:125]
	v_mfma_f32_16x16x32_bf16 v[118:121], v[130:133], v[188:191], v[118:121]
	v_mfma_f32_16x16x32_bf16 v[114:117], v[156:159], v[188:191], v[114:117]
	v_mfma_f32_16x16x32_bf16 v[100:103], v[130:133], v[206:209], v[100:103]
	v_mfma_f32_16x16x32_bf16 v[96:99], v[156:159], v[206:209], v[96:99]
	v_mfma_f32_16x16x32_bf16 v[84:87], v[130:133], v[216:219], v[84:87]
	v_mfma_f32_16x16x32_bf16 v[80:83], v[156:159], v[216:219], v[80:83]
	v_mfma_f32_16x16x32_bf16 v[126:129], v[134:137], v[184:187], v[126:129]
	v_mfma_f32_16x16x32_bf16 v[122:125], v[160:163], v[184:187], v[122:125]
	v_mfma_f32_16x16x32_bf16 v[118:121], v[134:137], v[192:195], v[118:121]
	v_mfma_f32_16x16x32_bf16 v[114:117], v[160:163], v[192:195], v[114:117]
	v_mfma_f32_16x16x32_bf16 v[100:103], v[134:137], v[210:213], v[100:103]
	v_mfma_f32_16x16x32_bf16 v[96:99], v[160:163], v[210:213], v[96:99]
	v_mfma_f32_16x16x32_bf16 v[84:87], v[134:137], v[220:223], v[84:87]
	v_mfma_f32_16x16x32_bf16 v[80:83], v[160:163], v[220:223], v[80:83]
	v_mfma_f32_16x16x32_bf16 v[108:111], v[164:167], v[180:183], v[108:111]
	v_mfma_f32_16x16x32_bf16 v[104:107], v[172:175], v[180:183], v[104:107]
	v_mfma_f32_16x16x32_bf16 v[92:95], v[164:167], v[188:191], v[92:95]
	v_mfma_f32_16x16x32_bf16 v[88:91], v[172:175], v[188:191], v[88:91]
	v_mfma_f32_16x16x32_bf16 v[76:79], v[164:167], v[206:209], v[76:79]
	v_mfma_f32_16x16x32_bf16 v[72:75], v[172:175], v[206:209], v[72:75]
	v_mfma_f32_16x16x32_bf16 v[68:71], v[164:167], v[216:219], v[68:71]
	v_mfma_f32_16x16x32_bf16 v[64:67], v[172:175], v[216:219], v[64:67]
	v_mfma_f32_16x16x32_bf16 v[108:111], v[168:171], v[184:187], v[108:111]
	v_mfma_f32_16x16x32_bf16 v[104:107], v[176:179], v[184:187], v[104:107]
	v_mfma_f32_16x16x32_bf16 v[92:95], v[168:171], v[192:195], v[92:95]
	v_mfma_f32_16x16x32_bf16 v[88:91], v[176:179], v[192:195], v[88:91]
	v_mfma_f32_16x16x32_bf16 v[76:79], v[168:171], v[210:213], v[76:79]
	v_mfma_f32_16x16x32_bf16 v[72:75], v[176:179], v[210:213], v[72:75]
	v_mfma_f32_16x16x32_bf16 v[68:71], v[168:171], v[220:223], v[68:71]
	v_mfma_f32_16x16x32_bf16 v[64:67], v[176:179], v[220:223], v[64:67]
	s_barrier
	s_add_i32 s28, s30, s13
	v_lshl_add_u64 v[150:151], v[150:151], 0, s[56:57]
	s_mov_b32 m0, s28
	ds_read_b128 v[180:183], v154 offset:49152
	ds_read_b128 v[184:187], v154 offset:50176
	ds_read_b128 v[188:191], v154 offset:51200
	ds_read_b128 v[192:195], v154 offset:52224
	ds_read_b128 v[206:209], v154 offset:53248
	ds_read_b128 v[210:213], v154 offset:54272
	ds_read_b128 v[216:219], v154 offset:55296
	ds_read_b128 v[220:223], v154 offset:56320
	global_load_lds_dwordx4 v[150:151], off
	s_add_i32 m0, s28, 0x2000
	s_add_u32 s28, s80, 0x40080
	v_lshl_add_u64 v[150:151], v[224:225], 0, s[56:57]
	s_addc_u32 s29, s81, 0
	s_add_i32 s30, s31, s13
	global_load_lds_dwordx4 v[150:151], off
	v_lshl_add_u64 v[150:151], s[28:29], 0, v[140:141]
	s_mov_b32 m0, s30
	s_nop 0
	global_load_lds_dwordx4 v[150:151], off
	v_lshl_add_u64 v[150:151], s[28:29], 0, v[144:145]
	s_add_i32 m0, s30, 0x2000
	s_nop 0
	global_load_lds_dwordx4 v[150:151], off
	v_lshl_add_u64 v[150:151], v[226:227], 0, s[56:57]
	s_mov_b32 m0, s33
	s_nop 0
	global_load_lds_dwordx4 v[150:151], off
	v_lshl_add_u64 v[150:151], v[228:229], 0, s[56:57]
	s_mov_b32 m0, s69
	s_nop 0
	global_load_lds_dwordx4 v[150:151], off
	s_waitcnt vmcnt(8)
	s_waitcnt lgkmcnt(0)
	s_barrier
	s_waitcnt lgkmcnt(0)
	v_mfma_f32_16x16x32_bf16 v[60:63], v[130:133], v[180:183], v[60:63]
	v_mfma_f32_16x16x32_bf16 v[56:59], v[156:159], v[180:183], v[56:59]
	v_mfma_f32_16x16x32_bf16 v[52:55], v[130:133], v[188:191], v[52:55]
	v_mfma_f32_16x16x32_bf16 v[48:51], v[156:159], v[188:191], v[48:51]
	v_mfma_f32_16x16x32_bf16 v[36:39], v[130:133], v[206:209], v[36:39]
	v_mfma_f32_16x16x32_bf16 v[32:35], v[156:159], v[206:209], v[32:35]
	v_mfma_f32_16x16x32_bf16 v[20:23], v[130:133], v[216:219], v[20:23]
	v_mfma_f32_16x16x32_bf16 v[16:19], v[156:159], v[216:219], v[16:19]
	v_mfma_f32_16x16x32_bf16 v[60:63], v[134:137], v[184:187], v[60:63]
	v_mfma_f32_16x16x32_bf16 v[56:59], v[160:163], v[184:187], v[56:59]
	v_mfma_f32_16x16x32_bf16 v[52:55], v[134:137], v[192:195], v[52:55]
	v_mfma_f32_16x16x32_bf16 v[48:51], v[160:163], v[192:195], v[48:51]
	v_mfma_f32_16x16x32_bf16 v[36:39], v[134:137], v[210:213], v[36:39]
	v_mfma_f32_16x16x32_bf16 v[32:35], v[160:163], v[210:213], v[32:35]
	v_mfma_f32_16x16x32_bf16 v[20:23], v[134:137], v[220:223], v[20:23]
	v_mfma_f32_16x16x32_bf16 v[16:19], v[160:163], v[220:223], v[16:19]
	v_mfma_f32_16x16x32_bf16 v[44:47], v[164:167], v[180:183], v[44:47]
	v_mfma_f32_16x16x32_bf16 v[40:43], v[172:175], v[180:183], v[40:43]
	v_mfma_f32_16x16x32_bf16 v[28:31], v[164:167], v[188:191], v[28:31]
	v_mfma_f32_16x16x32_bf16 v[24:27], v[172:175], v[188:191], v[24:27]
	v_mfma_f32_16x16x32_bf16 v[12:15], v[164:167], v[206:209], v[12:15]
	v_mfma_f32_16x16x32_bf16 v[8:11], v[172:175], v[206:209], v[8:11]
	v_mfma_f32_16x16x32_bf16 v[4:7], v[164:167], v[216:219], v[4:7]
	v_mfma_f32_16x16x32_bf16 v[0:3], v[172:175], v[216:219], v[0:3]
	v_mfma_f32_16x16x32_bf16 v[44:47], v[168:171], v[184:187], v[44:47]
	v_mfma_f32_16x16x32_bf16 v[40:43], v[176:179], v[184:187], v[40:43]
	v_mfma_f32_16x16x32_bf16 v[28:31], v[168:171], v[192:195], v[28:31]
	v_mfma_f32_16x16x32_bf16 v[24:27], v[176:179], v[192:195], v[24:27]
	v_mfma_f32_16x16x32_bf16 v[12:15], v[168:171], v[210:213], v[12:15]
	v_mfma_f32_16x16x32_bf16 v[8:11], v[176:179], v[210:213], v[8:11]
	v_mfma_f32_16x16x32_bf16 v[4:7], v[168:171], v[220:223], v[4:7]
	v_mfma_f32_16x16x32_bf16 v[0:3], v[176:179], v[220:223], v[0:3]
	s_barrier
	s_add_i32 s71, s71, 2
	s_add_u32 s76, s76, 0x100
	s_addc_u32 s77, s77, 0
	s_add_u32 s51, s51, 0x100
	s_addc_u32 s65, s65, 0
	s_cmp_gt_u32 s71, 13
	s_cbranch_scc0 .LBB0_264
	s_and_b64 vcc, exec, s[46:47]
	s_cbranch_vccz .LBB0_267
	s_barrier

.Lpeel_gate:
	s_add_u32 s28, s82, 0xfffe0080
	s_addc_u32 s29, s83, -1
	s_add_i32 s85, 0, 0x10000
	s_cmp_eq_u32 s84, 4
	s_cselect_b32 vcc_hi, s37, s29
	s_cselect_b32 vcc_lo, s50, s28
	s_cselect_b32 s97, s51, s75
	s_cselect_b32 s96, s71, s73
	s_add_i32 s28, 0, 0x14000
	v_add_u32_e32 v0, s85, v183
	v_add_u32_e32 v12, s28, v183
	ds_read_b128 v[16:19], v0
	ds_read_b128 v[20:23], v0 offset:1024
	ds_read_b128 v[24:27], v0 offset:2048
	ds_read_b128 v[28:31], v0 offset:3072
	ds_read_b128 v[0:3], v12
	ds_read_b128 v[4:7], v12 offset:1024
	ds_read_b128 v[8:11], v12 offset:2048
	ds_read_b128 v[12:15], v12 offset:3072
	v_lshl_add_u64 v[194:195], s[82:83], 0, v[170:171]
	s_add_i32 m0, s6, 0xc000
	ds_read_b128 v[174:177], v184
	ds_read_b128 v[178:181], v184 offset:1024
	ds_read_b128 v[186:189], v184 offset:2048
	ds_read_b128 v[190:193], v184 offset:3072
	ds_read_b128 v[216:219], v184 offset:4096
	ds_read_b128 v[220:223], v184 offset:5120
	ds_read_b128 v[224:227], v184 offset:6144
	ds_read_b128 v[228:231], v184 offset:7168
	global_load_lds_dwordx4 v[194:195], off
	v_lshl_add_u64 v[194:195], s[82:83], 0, v[172:173]
	s_add_i32 m0, s6, 0xe000
	s_nop 0
	global_load_lds_dwordx4 v[194:195], off
	s_waitcnt vmcnt(8)
	s_waitcnt lgkmcnt(0)
	s_barrier
	s_waitcnt lgkmcnt(0)
	v_mfma_scale_f32_16x16x128_f8f6f4 v[158:161], v[16:23], v[174:181], 0, v200, v201 op_sel_hi:[0,0,0]
	v_mfma_scale_f32_16x16x128_f8f6f4 v[154:157], v[24:31], v[174:181], 0, v200, v201 op_sel_hi:[0,0,0]
	v_mfma_scale_f32_16x16x128_f8f6f4 v[150:153], v[16:23], v[186:193], 0, v200, v201 op_sel_hi:[0,0,0]
	v_mfma_scale_f32_16x16x128_f8f6f4 v[146:149], v[24:31], v[186:193], 0, v200, v201 op_sel_hi:[0,0,0]
	v_mfma_scale_f32_16x16x128_f8f6f4 v[134:137], v[16:23], v[216:223], 0, v200, v201 op_sel_hi:[0,0,0]
	v_mfma_scale_f32_16x16x128_f8f6f4 v[130:133], v[24:31], v[216:223], 0, v200, v201 op_sel_hi:[0,0,0]
	v_mfma_scale_f32_16x16x128_f8f6f4 v[118:121], v[16:23], v[224:231], 0, v200, v201 op_sel_hi:[0,0,0]
	v_mfma_scale_f32_16x16x128_f8f6f4 v[114:117], v[24:31], v[224:231], 0, v200, v201 op_sel_hi:[0,0,0]
	v_mfma_scale_f32_16x16x128_f8f6f4 v[142:145], v[0:7], v[174:181], 0, v200, v201 op_sel_hi:[0,0,0]
	v_mfma_scale_f32_16x16x128_f8f6f4 v[138:141], v[8:15], v[174:181], 0, v200, v201 op_sel_hi:[0,0,0]
	v_mfma_scale_f32_16x16x128_f8f6f4 v[126:129], v[0:7], v[186:193], 0, v200, v201 op_sel_hi:[0,0,0]
	v_mfma_scale_f32_16x16x128_f8f6f4 v[122:125], v[8:15], v[186:193], 0, v200, v201 op_sel_hi:[0,0,0]
	v_mfma_scale_f32_16x16x128_f8f6f4 v[108:111], v[0:7], v[216:223], 0, v200, v201 op_sel_hi:[0,0,0]
	v_mfma_scale_f32_16x16x128_f8f6f4 v[104:107], v[8:15], v[216:223], 0, v200, v201 op_sel_hi:[0,0,0]
	v_mfma_scale_f32_16x16x128_f8f6f4 v[100:103], v[0:7], v[224:231], 0, v200, v201 op_sel_hi:[0,0,0]
	v_mfma_scale_f32_16x16x128_f8f6f4 v[96:99], v[8:15], v[224:231], 0, v200, v201 op_sel_hi:[0,0,0]
	s_barrier
	s_add_i32 s29, s85, s14
	v_lshl_add_u64 v[174:175], s[96:97], 0, v[164:165]
	s_mov_b32 m0, s29
	ds_read_b128 v[186:189], v184 offset:16384
	ds_read_b128 v[190:193], v184 offset:17408
	ds_read_b128 v[216:219], v184 offset:18432
	ds_read_b128 v[220:223], v184 offset:19456
	ds_read_b128 v[224:227], v184 offset:20480
	ds_read_b128 v[228:231], v184 offset:21504
	ds_read_b128 v[232:235], v184 offset:22528
	ds_read_b128 v[236:239], v184 offset:23552
	global_load_lds_dwordx4 v[174:175], off
	s_add_i32 m0, s29, 0x2000
	s_add_u32 s30, s96, 0x20000
	v_lshl_add_u64 v[176:177], s[96:97], 0, v[168:169]
	s_addc_u32 s31, s97, 0
	s_add_i32 s28, s28, s14
	global_load_lds_dwordx4 v[176:177], off
	v_lshl_add_u64 v[178:179], s[30:31], 0, v[164:165]
	s_mov_b32 m0, s28
	v_lshl_add_u64 v[180:181], vcc, 0, v[166:167]
	global_load_lds_dwordx4 v[178:179], off
	v_lshl_add_u64 v[178:179], s[30:31], 0, v[168:169]
	s_add_i32 m0, s28, 0x2000
	s_nop 0
	global_load_lds_dwordx4 v[178:179], off
	v_lshl_add_u64 v[178:179], vcc, 0, v[162:163]
	s_mov_b32 m0, s6
	s_nop 0
	global_load_lds_dwordx4 v[178:179], off
	s_mov_b32 m0, s7
	s_nop 0
	global_load_lds_dwordx4 v[180:181], off
	s_waitcnt vmcnt(8)
	s_waitcnt lgkmcnt(0)
	s_barrier
	s_waitcnt lgkmcnt(0)
	v_mfma_scale_f32_16x16x128_f8f6f4 v[92:95], v[16:23], v[186:193], 0, v200, v201 op_sel_hi:[0,0,0]
	v_mfma_scale_f32_16x16x128_f8f6f4 v[88:91], v[24:31], v[186:193], 0, v200, v201 op_sel_hi:[0,0,0]
	v_mfma_scale_f32_16x16x128_f8f6f4 v[84:87], v[16:23], v[216:223], 0, v200, v201 op_sel_hi:[0,0,0]
	v_mfma_scale_f32_16x16x128_f8f6f4 v[80:83], v[24:31], v[216:223], 0, v200, v201 op_sel_hi:[0,0,0]
	v_mfma_scale_f32_16x16x128_f8f6f4 v[68:71], v[16:23], v[224:231], 0, v200, v201 op_sel_hi:[0,0,0]
	v_mfma_scale_f32_16x16x128_f8f6f4 v[64:67], v[24:31], v[224:231], 0, v200, v201 op_sel_hi:[0,0,0]
	v_mfma_scale_f32_16x16x128_f8f6f4 v[52:55], v[16:23], v[232:239], 0, v200, v201 op_sel_hi:[0,0,0]
	v_mfma_scale_f32_16x16x128_f8f6f4 v[48:51], v[24:31], v[232:239], 0, v200, v201 op_sel_hi:[0,0,0]
	v_mfma_scale_f32_16x16x128_f8f6f4 v[76:79], v[0:7], v[186:193], 0, v200, v201 op_sel_hi:[0,0,0]
	v_mfma_scale_f32_16x16x128_f8f6f4 v[72:75], v[8:15], v[186:193], 0, v200, v201 op_sel_hi:[0,0,0]
	v_mfma_scale_f32_16x16x128_f8f6f4 v[60:63], v[0:7], v[216:223], 0, v200, v201 op_sel_hi:[0,0,0]
	v_mfma_scale_f32_16x16x128_f8f6f4 v[56:59], v[8:15], v[216:223], 0, v200, v201 op_sel_hi:[0,0,0]
	v_mfma_scale_f32_16x16x128_f8f6f4 v[44:47], v[0:7], v[224:231], 0, v200, v201 op_sel_hi:[0,0,0]
	v_mfma_scale_f32_16x16x128_f8f6f4 v[40:43], v[8:15], v[224:231], 0, v200, v201 op_sel_hi:[0,0,0]
	v_mfma_scale_f32_16x16x128_f8f6f4 v[36:39], v[0:7], v[232:239], 0, v200, v201 op_sel_hi:[0,0,0]
	v_mfma_scale_f32_16x16x128_f8f6f4 v[32:35], v[8:15], v[232:239], 0, v200, v201 op_sel_hi:[0,0,0]
	s_barrier
	s_add_i32 s30, 0, 0x18000
	s_add_i32 s31, 0, 0x1c000
	v_add_u32_e32 v12, s30, v183
	v_add_u32_e32 v28, s31, v183
	ds_read_b128 v[0:3], v12
	ds_read_b128 v[4:7], v12 offset:1024
	ds_read_b128 v[8:11], v12 offset:2048
	ds_read_b128 v[12:15], v12 offset:3072
	ds_read_b128 v[16:19], v28
	ds_read_b128 v[20:23], v28 offset:1024
	ds_read_b128 v[24:27], v28 offset:2048
	ds_read_b128 v[28:31], v28 offset:3072
	s_add_u32 s28, vcc_lo, 0x20000
	s_addc_u32 s29, vcc_hi, 0
	s_mov_b32 m0, s86
	v_lshl_add_u64 v[194:195], s[28:29], 0, v[162:163]
	ds_read_b128 v[186:189], v184 offset:32768
	ds_read_b128 v[190:193], v184 offset:33792
	ds_read_b128 v[216:219], v184 offset:34816
	ds_read_b128 v[220:223], v184 offset:35840
	ds_read_b128 v[224:227], v184 offset:36864
	ds_read_b128 v[228:231], v184 offset:37888
	ds_read_b128 v[232:235], v184 offset:38912
	ds_read_b128 v[236:239], v184 offset:39936
	global_load_lds_dwordx4 v[194:195], off
	v_lshl_add_u64 v[194:195], s[28:29], 0, v[166:167]
	s_mov_b32 m0, s33
	s_nop 0
	global_load_lds_dwordx4 v[194:195], off
	s_waitcnt vmcnt(8)
	s_waitcnt lgkmcnt(0)
	s_barrier
	s_waitcnt lgkmcnt(0)
	v_mfma_scale_f32_16x16x128_f8f6f4 v[158:161], v[0:7], v[186:193], v[158:161], v200, v201 op_sel_hi:[0,0,0]
	v_mfma_scale_f32_16x16x128_f8f6f4 v[154:157], v[8:15], v[186:193], v[154:157], v200, v201 op_sel_hi:[0,0,0]
	v_mfma_scale_f32_16x16x128_f8f6f4 v[150:153], v[0:7], v[216:223], v[150:153], v200, v201 op_sel_hi:[0,0,0]
	v_mfma_scale_f32_16x16x128_f8f6f4 v[146:149], v[8:15], v[216:223], v[146:149], v200, v201 op_sel_hi:[0,0,0]
	v_mfma_scale_f32_16x16x128_f8f6f4 v[134:137], v[0:7], v[224:231], v[134:137], v200, v201 op_sel_hi:[0,0,0]
	v_mfma_scale_f32_16x16x128_f8f6f4 v[130:133], v[8:15], v[224:231], v[130:133], v200, v201 op_sel_hi:[0,0,0]
	v_mfma_scale_f32_16x16x128_f8f6f4 v[118:121], v[0:7], v[232:239], v[118:121], v200, v201 op_sel_hi:[0,0,0]
	v_mfma_scale_f32_16x16x128_f8f6f4 v[114:117], v[8:15], v[232:239], v[114:117], v200, v201 op_sel_hi:[0,0,0]
	v_mfma_scale_f32_16x16x128_f8f6f4 v[142:145], v[16:23], v[186:193], v[142:145], v200, v201 op_sel_hi:[0,0,0]
	v_mfma_scale_f32_16x16x128_f8f6f4 v[138:141], v[24:31], v[186:193], v[138:141], v200, v201 op_sel_hi:[0,0,0]
	v_mfma_scale_f32_16x16x128_f8f6f4 v[126:129], v[16:23], v[216:223], v[126:129], v200, v201 op_sel_hi:[0,0,0]
	v_mfma_scale_f32_16x16x128_f8f6f4 v[122:125], v[24:31], v[216:223], v[122:125], v200, v201 op_sel_hi:[0,0,0]
	v_mfma_scale_f32_16x16x128_f8f6f4 v[108:111], v[16:23], v[224:231], v[108:111], v200, v201 op_sel_hi:[0,0,0]
	v_mfma_scale_f32_16x16x128_f8f6f4 v[104:107], v[24:31], v[224:231], v[104:107], v200, v201 op_sel_hi:[0,0,0]
	v_mfma_scale_f32_16x16x128_f8f6f4 v[100:103], v[16:23], v[232:239], v[100:103], v200, v201 op_sel_hi:[0,0,0]
	v_mfma_scale_f32_16x16x128_f8f6f4 v[96:99], v[24:31], v[232:239], v[96:99], v200, v201 op_sel_hi:[0,0,0]
	s_barrier
	s_add_i32 s28, s30, s14
	v_lshl_add_u64 v[174:175], v[174:175], 0, s[56:57]
	s_mov_b32 m0, s28
	ds_read_b128 v[186:189], v184 offset:49152
	ds_read_b128 v[190:193], v184 offset:50176
	ds_read_b128 v[216:219], v184 offset:51200
	ds_read_b128 v[220:223], v184 offset:52224
	ds_read_b128 v[224:227], v184 offset:53248
	ds_read_b128 v[228:231], v184 offset:54272
	ds_read_b128 v[232:235], v184 offset:55296
	ds_read_b128 v[236:239], v184 offset:56320
	global_load_lds_dwordx4 v[174:175], off
	s_add_i32 m0, s28, 0x2000
	s_add_u32 s28, s96, 0x20080
	v_lshl_add_u64 v[174:175], v[176:177], 0, s[56:57]
	s_addc_u32 s29, s97, 0
	s_add_i32 s30, s31, s14
	global_load_lds_dwordx4 v[174:175], off
	v_lshl_add_u64 v[174:175], s[28:29], 0, v[164:165]
	s_mov_b32 m0, s30
	s_nop 0
	global_load_lds_dwordx4 v[174:175], off
	v_lshl_add_u64 v[174:175], s[28:29], 0, v[168:169]
	s_add_i32 m0, s30, 0x2000
	s_nop 0
	global_load_lds_dwordx4 v[174:175], off
	v_lshl_add_u64 v[174:175], v[178:179], 0, s[56:57]
	s_mov_b32 m0, s54
	s_nop 0
	global_load_lds_dwordx4 v[174:175], off
	v_lshl_add_u64 v[174:175], v[180:181], 0, s[56:57]
	s_mov_b32 m0, s55
	s_nop 0
	global_load_lds_dwordx4 v[174:175], off
	s_waitcnt vmcnt(8)
	s_waitcnt lgkmcnt(0)
	s_barrier
	s_waitcnt lgkmcnt(0)
	v_mfma_scale_f32_16x16x128_f8f6f4 v[92:95], v[0:7], v[186:193], v[92:95], v200, v201 op_sel_hi:[0,0,0]
	v_mfma_scale_f32_16x16x128_f8f6f4 v[88:91], v[8:15], v[186:193], v[88:91], v200, v201 op_sel_hi:[0,0,0]
	v_mfma_scale_f32_16x16x128_f8f6f4 v[84:87], v[0:7], v[216:223], v[84:87], v200, v201 op_sel_hi:[0,0,0]
	v_mfma_scale_f32_16x16x128_f8f6f4 v[80:83], v[8:15], v[216:223], v[80:83], v200, v201 op_sel_hi:[0,0,0]
	v_mfma_scale_f32_16x16x128_f8f6f4 v[68:71], v[0:7], v[224:231], v[68:71], v200, v201 op_sel_hi:[0,0,0]
	v_mfma_scale_f32_16x16x128_f8f6f4 v[64:67], v[8:15], v[224:231], v[64:67], v200, v201 op_sel_hi:[0,0,0]
	v_mfma_scale_f32_16x16x128_f8f6f4 v[52:55], v[0:7], v[232:239], v[52:55], v200, v201 op_sel_hi:[0,0,0]
	v_mfma_scale_f32_16x16x128_f8f6f4 v[48:51], v[8:15], v[232:239], v[48:51], v200, v201 op_sel_hi:[0,0,0]
	v_mfma_scale_f32_16x16x128_f8f6f4 v[76:79], v[16:23], v[186:193], v[76:79], v200, v201 op_sel_hi:[0,0,0]
	v_mfma_scale_f32_16x16x128_f8f6f4 v[72:75], v[24:31], v[186:193], v[72:75], v200, v201 op_sel_hi:[0,0,0]
	v_mfma_scale_f32_16x16x128_f8f6f4 v[60:63], v[16:23], v[216:223], v[60:63], v200, v201 op_sel_hi:[0,0,0]
	v_mfma_scale_f32_16x16x128_f8f6f4 v[56:59], v[24:31], v[216:223], v[56:59], v200, v201 op_sel_hi:[0,0,0]
	v_mfma_scale_f32_16x16x128_f8f6f4 v[44:47], v[16:23], v[224:231], v[44:47], v200, v201 op_sel_hi:[0,0,0]
	v_mfma_scale_f32_16x16x128_f8f6f4 v[40:43], v[24:31], v[224:231], v[40:43], v200, v201 op_sel_hi:[0,0,0]
	v_mfma_scale_f32_16x16x128_f8f6f4 v[36:39], v[16:23], v[232:239], v[36:39], v200, v201 op_sel_hi:[0,0,0]
	v_mfma_scale_f32_16x16x128_f8f6f4 v[32:35], v[24:31], v[232:239], v[32:35], v200, v201 op_sel_hi:[0,0,0]
	s_barrier
	s_add_i32 s84, s84, 2
	s_add_u32 s82, s82, 0x100
	s_addc_u32 s83, s83, 0
	s_add_u32 s73, s73, 0x100
	s_addc_u32 s75, s75, 0
	s_cmp_gt_u32 s84, 5
.LBB0_666:
	s_add_u32 s28, s82, 0xfffe0080
	s_addc_u32 s29, s83, -1
	s_add_i32 s85, 0, 0x10000
	s_cmp_eq_u32 s84, 4
	s_cselect_b32 vcc_hi, s37, s29
	s_cselect_b32 vcc_lo, s50, s28
	s_cselect_b32 s97, s51, s75
	s_cselect_b32 s96, s71, s73
	s_add_i32 s28, 0, 0x14000
	v_add_u32_e32 v0, s85, v183
	v_add_u32_e32 v12, s28, v183
	ds_read_b128 v[16:19], v0
	ds_read_b128 v[20:23], v0 offset:1024
	ds_read_b128 v[24:27], v0 offset:2048
	ds_read_b128 v[28:31], v0 offset:3072
	ds_read_b128 v[0:3], v12
	ds_read_b128 v[4:7], v12 offset:1024
	ds_read_b128 v[8:11], v12 offset:2048
	ds_read_b128 v[12:15], v12 offset:3072
	v_lshl_add_u64 v[194:195], s[82:83], 0, v[170:171]
	s_add_i32 m0, s6, 0xc000
	ds_read_b128 v[174:177], v184
	ds_read_b128 v[178:181], v184 offset:1024
	ds_read_b128 v[186:189], v184 offset:2048
	ds_read_b128 v[190:193], v184 offset:3072
	ds_read_b128 v[216:219], v184 offset:4096
	ds_read_b128 v[220:223], v184 offset:5120
	ds_read_b128 v[224:227], v184 offset:6144
	ds_read_b128 v[228:231], v184 offset:7168
	global_load_lds_dwordx4 v[194:195], off
	v_lshl_add_u64 v[194:195], s[82:83], 0, v[172:173]
	s_add_i32 m0, s6, 0xe000
	s_nop 0
	global_load_lds_dwordx4 v[194:195], off
	s_waitcnt vmcnt(8)
	s_waitcnt lgkmcnt(0)
	s_barrier
	s_waitcnt lgkmcnt(0)
	v_mfma_scale_f32_16x16x128_f8f6f4 v[158:161], v[16:23], v[174:181], v[158:161], v200, v201 op_sel_hi:[0,0,0]
	v_mfma_scale_f32_16x16x128_f8f6f4 v[154:157], v[24:31], v[174:181], v[154:157], v200, v201 op_sel_hi:[0,0,0]
	v_mfma_scale_f32_16x16x128_f8f6f4 v[150:153], v[16:23], v[186:193], v[150:153], v200, v201 op_sel_hi:[0,0,0]
	v_mfma_scale_f32_16x16x128_f8f6f4 v[146:149], v[24:31], v[186:193], v[146:149], v200, v201 op_sel_hi:[0,0,0]
	v_mfma_scale_f32_16x16x128_f8f6f4 v[134:137], v[16:23], v[216:223], v[134:137], v200, v201 op_sel_hi:[0,0,0]
	v_mfma_scale_f32_16x16x128_f8f6f4 v[130:133], v[24:31], v[216:223], v[130:133], v200, v201 op_sel_hi:[0,0,0]
	v_mfma_scale_f32_16x16x128_f8f6f4 v[118:121], v[16:23], v[224:231], v[118:121], v200, v201 op_sel_hi:[0,0,0]
	v_mfma_scale_f32_16x16x128_f8f6f4 v[114:117], v[24:31], v[224:231], v[114:117], v200, v201 op_sel_hi:[0,0,0]
	v_mfma_scale_f32_16x16x128_f8f6f4 v[142:145], v[0:7], v[174:181], v[142:145], v200, v201 op_sel_hi:[0,0,0]
	v_mfma_scale_f32_16x16x128_f8f6f4 v[138:141], v[8:15], v[174:181], v[138:141], v200, v201 op_sel_hi:[0,0,0]
	v_mfma_scale_f32_16x16x128_f8f6f4 v[126:129], v[0:7], v[186:193], v[126:129], v200, v201 op_sel_hi:[0,0,0]
	v_mfma_scale_f32_16x16x128_f8f6f4 v[122:125], v[8:15], v[186:193], v[122:125], v200, v201 op_sel_hi:[0,0,0]
	v_mfma_scale_f32_16x16x128_f8f6f4 v[108:111], v[0:7], v[216:223], v[108:111], v200, v201 op_sel_hi:[0,0,0]
	v_mfma_scale_f32_16x16x128_f8f6f4 v[104:107], v[8:15], v[216:223], v[104:107], v200, v201 op_sel_hi:[0,0,0]
	v_mfma_scale_f32_16x16x128_f8f6f4 v[100:103], v[0:7], v[224:231], v[100:103], v200, v201 op_sel_hi:[0,0,0]
	v_mfma_scale_f32_16x16x128_f8f6f4 v[96:99], v[8:15], v[224:231], v[96:99], v200, v201 op_sel_hi:[0,0,0]
	s_barrier
	s_add_i32 s29, s85, s14
	v_lshl_add_u64 v[174:175], s[96:97], 0, v[164:165]
	s_mov_b32 m0, s29
	ds_read_b128 v[186:189], v184 offset:16384
	ds_read_b128 v[190:193], v184 offset:17408
	ds_read_b128 v[216:219], v184 offset:18432
	ds_read_b128 v[220:223], v184 offset:19456
	ds_read_b128 v[224:227], v184 offset:20480
	ds_read_b128 v[228:231], v184 offset:21504
	ds_read_b128 v[232:235], v184 offset:22528
	ds_read_b128 v[236:239], v184 offset:23552
	global_load_lds_dwordx4 v[174:175], off
	s_add_i32 m0, s29, 0x2000
	s_add_u32 s30, s96, 0x20000
	v_lshl_add_u64 v[176:177], s[96:97], 0, v[168:169]
	s_addc_u32 s31, s97, 0
	s_add_i32 s28, s28, s14
	global_load_lds_dwordx4 v[176:177], off
	v_lshl_add_u64 v[178:179], s[30:31], 0, v[164:165]
	s_mov_b32 m0, s28
	v_lshl_add_u64 v[180:181], vcc, 0, v[166:167]
	global_load_lds_dwordx4 v[178:179], off
	v_lshl_add_u64 v[178:179], s[30:31], 0, v[168:169]
	s_add_i32 m0, s28, 0x2000
	s_nop 0
	global_load_lds_dwordx4 v[178:179], off
	v_lshl_add_u64 v[178:179], vcc, 0, v[162:163]
	s_mov_b32 m0, s6
	s_nop 0
	global_load_lds_dwordx4 v[178:179], off
	s_mov_b32 m0, s7
	s_nop 0
	global_load_lds_dwordx4 v[180:181], off
	s_waitcnt vmcnt(8)
	s_waitcnt lgkmcnt(0)
	s_barrier
	s_waitcnt lgkmcnt(0)
	v_mfma_scale_f32_16x16x128_f8f6f4 v[92:95], v[16:23], v[186:193], v[92:95], v200, v201 op_sel_hi:[0,0,0]
	v_mfma_scale_f32_16x16x128_f8f6f4 v[88:91], v[24:31], v[186:193], v[88:91], v200, v201 op_sel_hi:[0,0,0]
	v_mfma_scale_f32_16x16x128_f8f6f4 v[84:87], v[16:23], v[216:223], v[84:87], v200, v201 op_sel_hi:[0,0,0]
	v_mfma_scale_f32_16x16x128_f8f6f4 v[80:83], v[24:31], v[216:223], v[80:83], v200, v201 op_sel_hi:[0,0,0]
	v_mfma_scale_f32_16x16x128_f8f6f4 v[68:71], v[16:23], v[224:231], v[68:71], v200, v201 op_sel_hi:[0,0,0]
	v_mfma_scale_f32_16x16x128_f8f6f4 v[64:67], v[24:31], v[224:231], v[64:67], v200, v201 op_sel_hi:[0,0,0]
	v_mfma_scale_f32_16x16x128_f8f6f4 v[52:55], v[16:23], v[232:239], v[52:55], v200, v201 op_sel_hi:[0,0,0]
	v_mfma_scale_f32_16x16x128_f8f6f4 v[48:51], v[24:31], v[232:239], v[48:51], v200, v201 op_sel_hi:[0,0,0]
	v_mfma_scale_f32_16x16x128_f8f6f4 v[76:79], v[0:7], v[186:193], v[76:79], v200, v201 op_sel_hi:[0,0,0]
	v_mfma_scale_f32_16x16x128_f8f6f4 v[72:75], v[8:15], v[186:193], v[72:75], v200, v201 op_sel_hi:[0,0,0]
	v_mfma_scale_f32_16x16x128_f8f6f4 v[60:63], v[0:7], v[216:223], v[60:63], v200, v201 op_sel_hi:[0,0,0]
	v_mfma_scale_f32_16x16x128_f8f6f4 v[56:59], v[8:15], v[216:223], v[56:59], v200, v201 op_sel_hi:[0,0,0]
	v_mfma_scale_f32_16x16x128_f8f6f4 v[44:47], v[0:7], v[224:231], v[44:47], v200, v201 op_sel_hi:[0,0,0]
	v_mfma_scale_f32_16x16x128_f8f6f4 v[40:43], v[8:15], v[224:231], v[40:43], v200, v201 op_sel_hi:[0,0,0]
	v_mfma_scale_f32_16x16x128_f8f6f4 v[36:39], v[0:7], v[232:239], v[36:39], v200, v201 op_sel_hi:[0,0,0]
	v_mfma_scale_f32_16x16x128_f8f6f4 v[32:35], v[8:15], v[232:239], v[32:35], v200, v201 op_sel_hi:[0,0,0]
	s_barrier
	s_add_i32 s30, 0, 0x18000
	s_add_i32 s31, 0, 0x1c000
	v_add_u32_e32 v12, s30, v183
	v_add_u32_e32 v28, s31, v183
	ds_read_b128 v[0:3], v12
	ds_read_b128 v[4:7], v12 offset:1024
	ds_read_b128 v[8:11], v12 offset:2048
	ds_read_b128 v[12:15], v12 offset:3072
	ds_read_b128 v[16:19], v28
	ds_read_b128 v[20:23], v28 offset:1024
	ds_read_b128 v[24:27], v28 offset:2048
	ds_read_b128 v[28:31], v28 offset:3072
	s_add_u32 s28, vcc_lo, 0x20000
	s_addc_u32 s29, vcc_hi, 0
	s_mov_b32 m0, s86
	v_lshl_add_u64 v[194:195], s[28:29], 0, v[162:163]
	ds_read_b128 v[186:189], v184 offset:32768
	ds_read_b128 v[190:193], v184 offset:33792
	ds_read_b128 v[216:219], v184 offset:34816
	ds_read_b128 v[220:223], v184 offset:35840
	ds_read_b128 v[224:227], v184 offset:36864
	ds_read_b128 v[228:231], v184 offset:37888
	ds_read_b128 v[232:235], v184 offset:38912
	ds_read_b128 v[236:239], v184 offset:39936
	global_load_lds_dwordx4 v[194:195], off
	v_lshl_add_u64 v[194:195], s[28:29], 0, v[166:167]
	s_mov_b32 m0, s33
	s_nop 0
	global_load_lds_dwordx4 v[194:195], off
	s_waitcnt vmcnt(8)
	s_waitcnt lgkmcnt(0)
	s_barrier
	s_waitcnt lgkmcnt(0)
	v_mfma_scale_f32_16x16x128_f8f6f4 v[158:161], v[0:7], v[186:193], v[158:161], v200, v201 op_sel_hi:[0,0,0]
	v_mfma_scale_f32_16x16x128_f8f6f4 v[154:157], v[8:15], v[186:193], v[154:157], v200, v201 op_sel_hi:[0,0,0]
	v_mfma_scale_f32_16x16x128_f8f6f4 v[150:153], v[0:7], v[216:223], v[150:153], v200, v201 op_sel_hi:[0,0,0]
	v_mfma_scale_f32_16x16x128_f8f6f4 v[146:149], v[8:15], v[216:223], v[146:149], v200, v201 op_sel_hi:[0,0,0]
	v_mfma_scale_f32_16x16x128_f8f6f4 v[134:137], v[0:7], v[224:231], v[134:137], v200, v201 op_sel_hi:[0,0,0]
	v_mfma_scale_f32_16x16x128_f8f6f4 v[130:133], v[8:15], v[224:231], v[130:133], v200, v201 op_sel_hi:[0,0,0]
	v_mfma_scale_f32_16x16x128_f8f6f4 v[118:121], v[0:7], v[232:239], v[118:121], v200, v201 op_sel_hi:[0,0,0]
	v_mfma_scale_f32_16x16x128_f8f6f4 v[114:117], v[8:15], v[232:239], v[114:117], v200, v201 op_sel_hi:[0,0,0]
	v_mfma_scale_f32_16x16x128_f8f6f4 v[142:145], v[16:23], v[186:193], v[142:145], v200, v201 op_sel_hi:[0,0,0]
	v_mfma_scale_f32_16x16x128_f8f6f4 v[138:141], v[24:31], v[186:193], v[138:141], v200, v201 op_sel_hi:[0,0,0]
	v_mfma_scale_f32_16x16x128_f8f6f4 v[126:129], v[16:23], v[216:223], v[126:129], v200, v201 op_sel_hi:[0,0,0]
	v_mfma_scale_f32_16x16x128_f8f6f4 v[122:125], v[24:31], v[216:223], v[122:125], v200, v201 op_sel_hi:[0,0,0]
	v_mfma_scale_f32_16x16x128_f8f6f4 v[108:111], v[16:23], v[224:231], v[108:111], v200, v201 op_sel_hi:[0,0,0]
	v_mfma_scale_f32_16x16x128_f8f6f4 v[104:107], v[24:31], v[224:231], v[104:107], v200, v201 op_sel_hi:[0,0,0]
	v_mfma_scale_f32_16x16x128_f8f6f4 v[100:103], v[16:23], v[232:239], v[100:103], v200, v201 op_sel_hi:[0,0,0]
	v_mfma_scale_f32_16x16x128_f8f6f4 v[96:99], v[24:31], v[232:239], v[96:99], v200, v201 op_sel_hi:[0,0,0]
	s_barrier
	s_add_i32 s28, s30, s14
	v_lshl_add_u64 v[174:175], v[174:175], 0, s[56:57]
	s_mov_b32 m0, s28
	ds_read_b128 v[186:189], v184 offset:49152
	ds_read_b128 v[190:193], v184 offset:50176
	ds_read_b128 v[216:219], v184 offset:51200
	ds_read_b128 v[220:223], v184 offset:52224
	ds_read_b128 v[224:227], v184 offset:53248
	ds_read_b128 v[228:231], v184 offset:54272
	ds_read_b128 v[232:235], v184 offset:55296
	ds_read_b128 v[236:239], v184 offset:56320
	global_load_lds_dwordx4 v[174:175], off
	s_add_i32 m0, s28, 0x2000
	s_add_u32 s28, s96, 0x20080
	v_lshl_add_u64 v[174:175], v[176:177], 0, s[56:57]
	s_addc_u32 s29, s97, 0
	s_add_i32 s30, s31, s14
	global_load_lds_dwordx4 v[174:175], off
	v_lshl_add_u64 v[174:175], s[28:29], 0, v[164:165]
	s_mov_b32 m0, s30
	s_nop 0
	global_load_lds_dwordx4 v[174:175], off
	v_lshl_add_u64 v[174:175], s[28:29], 0, v[168:169]
	s_add_i32 m0, s30, 0x2000
	s_nop 0
	global_load_lds_dwordx4 v[174:175], off
	v_lshl_add_u64 v[174:175], v[178:179], 0, s[56:57]
	s_mov_b32 m0, s54
	s_nop 0
	global_load_lds_dwordx4 v[174:175], off
	v_lshl_add_u64 v[174:175], v[180:181], 0, s[56:57]
	s_mov_b32 m0, s55
	s_nop 0
	global_load_lds_dwordx4 v[174:175], off
	s_waitcnt vmcnt(8)
	s_waitcnt lgkmcnt(0)
	s_barrier
	s_waitcnt lgkmcnt(0)
	v_mfma_scale_f32_16x16x128_f8f6f4 v[92:95], v[0:7], v[186:193], v[92:95], v200, v201 op_sel_hi:[0,0,0]
	v_mfma_scale_f32_16x16x128_f8f6f4 v[88:91], v[8:15], v[186:193], v[88:91], v200, v201 op_sel_hi:[0,0,0]
	v_mfma_scale_f32_16x16x128_f8f6f4 v[84:87], v[0:7], v[216:223], v[84:87], v200, v201 op_sel_hi:[0,0,0]
	v_mfma_scale_f32_16x16x128_f8f6f4 v[80:83], v[8:15], v[216:223], v[80:83], v200, v201 op_sel_hi:[0,0,0]
	v_mfma_scale_f32_16x16x128_f8f6f4 v[68:71], v[0:7], v[224:231], v[68:71], v200, v201 op_sel_hi:[0,0,0]
	v_mfma_scale_f32_16x16x128_f8f6f4 v[64:67], v[8:15], v[224:231], v[64:67], v200, v201 op_sel_hi:[0,0,0]
	v_mfma_scale_f32_16x16x128_f8f6f4 v[52:55], v[0:7], v[232:239], v[52:55], v200, v201 op_sel_hi:[0,0,0]
	v_mfma_scale_f32_16x16x128_f8f6f4 v[48:51], v[8:15], v[232:239], v[48:51], v200, v201 op_sel_hi:[0,0,0]
	v_mfma_scale_f32_16x16x128_f8f6f4 v[76:79], v[16:23], v[186:193], v[76:79], v200, v201 op_sel_hi:[0,0,0]
	v_mfma_scale_f32_16x16x128_f8f6f4 v[72:75], v[24:31], v[186:193], v[72:75], v200, v201 op_sel_hi:[0,0,0]
	v_mfma_scale_f32_16x16x128_f8f6f4 v[60:63], v[16:23], v[216:223], v[60:63], v200, v201 op_sel_hi:[0,0,0]
	v_mfma_scale_f32_16x16x128_f8f6f4 v[56:59], v[24:31], v[216:223], v[56:59], v200, v201 op_sel_hi:[0,0,0]
	v_mfma_scale_f32_16x16x128_f8f6f4 v[44:47], v[16:23], v[224:231], v[44:47], v200, v201 op_sel_hi:[0,0,0]
	v_mfma_scale_f32_16x16x128_f8f6f4 v[40:43], v[24:31], v[224:231], v[40:43], v200, v201 op_sel_hi:[0,0,0]
	v_mfma_scale_f32_16x16x128_f8f6f4 v[36:39], v[16:23], v[232:239], v[36:39], v200, v201 op_sel_hi:[0,0,0]
	v_mfma_scale_f32_16x16x128_f8f6f4 v[32:35], v[24:31], v[232:239], v[32:35], v200, v201 op_sel_hi:[0,0,0]
	s_barrier
	s_add_i32 s84, s84, 2
	s_add_u32 s82, s82, 0x100
	s_addc_u32 s83, s83, 0
	s_add_u32 s73, s73, 0x100
	s_addc_u32 s75, s75, 0
	s_cmp_gt_u32 s84, 5
	s_cbranch_scc0 .LBB0_666
	s_and_b64 vcc, exec, s[64:65]
	s_cbranch_vccz .LBB0_669
	s_barrier

.LBB0_758:
	s_add_u32 s30, s76, s80
	s_addc_u32 s31, s77, s81
	s_add_u32 s49, s30, 0x100
	s_addc_u32 s60, s31, 0
	s_and_b64 s[28:29], s[50:51], exec
	s_cselect_b32 s97, s65, s60
	s_cselect_b32 s96, s64, s49
	s_add_u32 s28, s72, s80
	s_addc_u32 s29, s73, s81
	s_add_u32 s49, s28, 0x100
	s_addc_u32 s60, s29, 0
	s_add_i32 s69, 0, 0x10000
	s_and_b64 s[28:29], s[50:51], exec
	s_cselect_b32 vcc_hi, s7, s60
	s_cselect_b32 vcc_lo, s37, s49
	s_add_i32 s49, 0, 0x14000
	s_add_u32 s30, s30, 0x10080
	s_addc_u32 s31, s31, 0
	s_add_i32 s84, s69, s25
	s_add_i32 m0, s26, 0xc000
	s_add_i32 s75, s26, 0xe000
	s_add_i32 s85, s84, 0x2000
	v_add_u32_e32 v112, s69, v175
	s_add_u32 s50, vcc_lo, 0x10000
	ds_read_b128 v[132:135], v112
	ds_read_b128 v[136:139], v112 offset:1024
	ds_read_b128 v[140:143], v112 offset:2048
	ds_read_b128 v[144:147], v112 offset:3072
	v_add_u32_e32 v112, s49, v175
	s_addc_u32 s51, vcc_hi, 0
	s_add_i32 s86, s49, s25
	ds_read_b128 v[148:151], v112
	ds_read_b128 v[152:155], v112 offset:1024
	ds_read_b128 v[156:159], v112 offset:2048
	ds_read_b128 v[160:163], v112 offset:3072
	s_add_i32 s63, s86, 0x2000
	s_add_i32 s29, 0, 0x18000
	s_add_i32 s60, 0, 0x1c000
	s_add_u32 s82, s96, 0x10000
	s_addc_u32 s83, s97, 0
	s_add_i32 s28, s29, s25
	s_add_i32 s45, s28, 0x2000
	s_add_u32 s80, vcc_lo, 0x10080
	s_addc_u32 s81, vcc_hi, 0
	s_add_i32 s69, s60, s25
	s_add_i32 s49, s69, 0x2000
	v_lshl_add_u64 v[114:115], s[30:31], 0, v[164:165]
	ds_read_b128 v[178:181], v176
	ds_read_b128 v[182:185], v176 offset:1024
	ds_read_b128 v[186:189], v176 offset:2048
	ds_read_b128 v[190:193], v176 offset:3072
	ds_read_b128 v[206:209], v176 offset:4096
	ds_read_b128 v[210:213], v176 offset:5120
	ds_read_b128 v[216:219], v176 offset:6144
	ds_read_b128 v[220:223], v176 offset:7168
	global_load_lds_dwordx4 v[114:115], off
	v_lshl_add_u64 v[114:115], s[30:31], 0, v[168:169]
	s_mov_b32 m0, s75
	s_nop 0
	global_load_lds_dwordx4 v[114:115], off
	s_waitcnt vmcnt(8)
	s_waitcnt lgkmcnt(0)
	s_barrier
	s_waitcnt lgkmcnt(0)
	v_mfma_f32_16x16x32_bf16 v[128:131], v[132:135], v[178:181], v[128:131]
	v_mfma_f32_16x16x32_bf16 v[124:127], v[140:143], v[178:181], v[124:127]
	v_mfma_f32_16x16x32_bf16 v[120:123], v[132:135], v[186:189], v[120:123]
	v_mfma_f32_16x16x32_bf16 v[114:117], v[140:143], v[186:189], v[116:119]
	v_mfma_f32_16x16x32_bf16 v[108:111], v[132:135], v[206:209], v[108:111]
	v_mfma_f32_16x16x32_bf16 v[104:107], v[140:143], v[206:209], v[104:107]
	v_mfma_f32_16x16x32_bf16 v[100:103], v[132:135], v[216:219], v[100:103]
	v_mfma_f32_16x16x32_bf16 v[96:99], v[140:143], v[216:219], v[96:99]
	v_mfma_f32_16x16x32_bf16 v[128:131], v[136:139], v[182:185], v[128:131]
	v_mfma_f32_16x16x32_bf16 v[124:127], v[144:147], v[182:185], v[124:127]
	v_mfma_f32_16x16x32_bf16 v[120:123], v[136:139], v[190:193], v[120:123]
	v_mfma_f32_16x16x32_bf16 v[114:117], v[144:147], v[190:193], v[114:117]
	v_mfma_f32_16x16x32_bf16 v[108:111], v[136:139], v[210:213], v[108:111]
	v_mfma_f32_16x16x32_bf16 v[104:107], v[144:147], v[210:213], v[104:107]
	v_mfma_f32_16x16x32_bf16 v[100:103], v[136:139], v[220:223], v[100:103]
	v_mfma_f32_16x16x32_bf16 v[96:99], v[144:147], v[220:223], v[96:99]
	v_mfma_f32_16x16x32_bf16 v[92:95], v[148:151], v[178:181], v[92:95]
	v_mfma_f32_16x16x32_bf16 v[88:91], v[156:159], v[178:181], v[88:91]
	v_mfma_f32_16x16x32_bf16 v[84:87], v[148:151], v[186:189], v[84:87]
	v_mfma_f32_16x16x32_bf16 v[80:83], v[156:159], v[186:189], v[80:83]
	v_mfma_f32_16x16x32_bf16 v[76:79], v[148:151], v[206:209], v[76:79]
	v_mfma_f32_16x16x32_bf16 v[72:75], v[156:159], v[206:209], v[72:75]
	v_mfma_f32_16x16x32_bf16 v[68:71], v[148:151], v[216:219], v[68:71]
	v_mfma_f32_16x16x32_bf16 v[64:67], v[156:159], v[216:219], v[64:67]
	v_mfma_f32_16x16x32_bf16 v[92:95], v[152:155], v[182:185], v[92:95]
	v_mfma_f32_16x16x32_bf16 v[88:91], v[160:163], v[182:185], v[88:91]
	v_mfma_f32_16x16x32_bf16 v[84:87], v[152:155], v[190:193], v[84:87]
	v_mfma_f32_16x16x32_bf16 v[80:83], v[160:163], v[190:193], v[80:83]
	v_mfma_f32_16x16x32_bf16 v[76:79], v[152:155], v[210:213], v[76:79]
	v_mfma_f32_16x16x32_bf16 v[72:75], v[160:163], v[210:213], v[72:75]
	v_mfma_f32_16x16x32_bf16 v[68:71], v[152:155], v[220:223], v[68:71]
	v_mfma_f32_16x16x32_bf16 v[64:67], v[160:163], v[220:223], v[64:67]
	s_barrier
	s_mov_b32 m0, s84
	v_lshl_add_u64 v[172:173], vcc, 0, v[166:167]
	ds_read_b128 v[178:181], v176 offset:16384
	ds_read_b128 v[182:185], v176 offset:17408
	ds_read_b128 v[186:189], v176 offset:18432
	ds_read_b128 v[190:193], v176 offset:19456
	ds_read_b128 v[206:209], v176 offset:20480
	ds_read_b128 v[210:213], v176 offset:21504
	ds_read_b128 v[216:219], v176 offset:22528
	ds_read_b128 v[220:223], v176 offset:23552
	global_load_lds_dwordx4 v[172:173], off
	v_lshl_add_u64 v[194:195], vcc, 0, v[170:171]
	s_mov_b32 m0, s85
	v_lshl_add_u64 v[118:119], s[50:51], 0, v[166:167]
	global_load_lds_dwordx4 v[194:195], off
	s_mov_b32 m0, s86
	v_lshl_add_u64 v[224:225], s[96:97], 0, v[164:165]
	global_load_lds_dwordx4 v[118:119], off
	v_lshl_add_u64 v[118:119], s[50:51], 0, v[170:171]
	s_mov_b32 m0, s63
	v_lshl_add_u64 v[226:227], s[96:97], 0, v[168:169]
	global_load_lds_dwordx4 v[118:119], off
	s_mov_b32 m0, s26
	s_nop 0
	global_load_lds_dwordx4 v[224:225], off
	s_mov_b32 m0, s27
	s_nop 0
	global_load_lds_dwordx4 v[226:227], off
	s_waitcnt vmcnt(8)
	s_waitcnt lgkmcnt(0)
	s_barrier
	s_waitcnt lgkmcnt(0)
	v_mfma_f32_16x16x32_bf16 v[60:63], v[132:135], v[178:181], v[60:63]
	v_mfma_f32_16x16x32_bf16 v[56:59], v[140:143], v[178:181], v[56:59]
	v_mfma_f32_16x16x32_bf16 v[52:55], v[132:135], v[186:189], v[52:55]
	v_mfma_f32_16x16x32_bf16 v[48:51], v[140:143], v[186:189], v[48:51]
	v_mfma_f32_16x16x32_bf16 v[44:47], v[132:135], v[206:209], v[44:47]
	v_mfma_f32_16x16x32_bf16 v[40:43], v[140:143], v[206:209], v[40:43]
	v_mfma_f32_16x16x32_bf16 v[36:39], v[132:135], v[216:219], v[36:39]
	v_mfma_f32_16x16x32_bf16 v[32:35], v[140:143], v[216:219], v[32:35]
	v_mfma_f32_16x16x32_bf16 v[60:63], v[136:139], v[182:185], v[60:63]
	v_mfma_f32_16x16x32_bf16 v[56:59], v[144:147], v[182:185], v[56:59]
	v_mfma_f32_16x16x32_bf16 v[52:55], v[136:139], v[190:193], v[52:55]
	v_mfma_f32_16x16x32_bf16 v[48:51], v[144:147], v[190:193], v[48:51]
	v_mfma_f32_16x16x32_bf16 v[44:47], v[136:139], v[210:213], v[44:47]
	v_mfma_f32_16x16x32_bf16 v[40:43], v[144:147], v[210:213], v[40:43]
	v_mfma_f32_16x16x32_bf16 v[36:39], v[136:139], v[220:223], v[36:39]
	v_mfma_f32_16x16x32_bf16 v[32:35], v[144:147], v[220:223], v[32:35]
	v_mfma_f32_16x16x32_bf16 v[28:31], v[148:151], v[178:181], v[28:31]
	v_mfma_f32_16x16x32_bf16 v[24:27], v[156:159], v[178:181], v[24:27]
	v_mfma_f32_16x16x32_bf16 v[20:23], v[148:151], v[186:189], v[20:23]
	v_mfma_f32_16x16x32_bf16 v[16:19], v[156:159], v[186:189], v[16:19]
	v_mfma_f32_16x16x32_bf16 v[12:15], v[148:151], v[206:209], v[12:15]
	v_mfma_f32_16x16x32_bf16 v[8:11], v[156:159], v[206:209], v[8:11]
	v_mfma_f32_16x16x32_bf16 v[4:7], v[148:151], v[216:219], v[4:7]
	v_mfma_f32_16x16x32_bf16 v[0:3], v[156:159], v[216:219], v[0:3]
	v_mfma_f32_16x16x32_bf16 v[28:31], v[152:155], v[182:185], v[28:31]
	v_mfma_f32_16x16x32_bf16 v[24:27], v[160:163], v[182:185], v[24:27]
	v_mfma_f32_16x16x32_bf16 v[20:23], v[152:155], v[190:193], v[20:23]
	v_mfma_f32_16x16x32_bf16 v[16:19], v[160:163], v[190:193], v[16:19]
	v_mfma_f32_16x16x32_bf16 v[12:15], v[152:155], v[210:213], v[12:15]
	v_mfma_f32_16x16x32_bf16 v[8:11], v[160:163], v[210:213], v[8:11]
	v_mfma_f32_16x16x32_bf16 v[4:7], v[152:155], v[220:223], v[4:7]
	v_mfma_f32_16x16x32_bf16 v[0:3], v[160:163], v[220:223], v[0:3]
	s_barrier
	v_add_u32_e32 v112, s29, v175
	ds_read_b128 v[132:135], v112
	ds_read_b128 v[136:139], v112 offset:1024
	ds_read_b128 v[140:143], v112 offset:2048
	ds_read_b128 v[144:147], v112 offset:3072
	v_add_u32_e32 v112, s60, v175
	ds_read_b128 v[148:151], v112
	ds_read_b128 v[152:155], v112 offset:1024
	ds_read_b128 v[156:159], v112 offset:2048
	ds_read_b128 v[160:163], v112 offset:3072
	s_mov_b32 m0, s33
	v_lshl_add_u64 v[118:119], s[82:83], 0, v[164:165]
	ds_read_b128 v[178:181], v176 offset:32768
	ds_read_b128 v[182:185], v176 offset:33792
	ds_read_b128 v[186:189], v176 offset:34816
	ds_read_b128 v[190:193], v176 offset:35840
	ds_read_b128 v[206:209], v176 offset:36864
	ds_read_b128 v[210:213], v176 offset:37888
	ds_read_b128 v[216:219], v176 offset:38912
	ds_read_b128 v[220:223], v176 offset:39936
	global_load_lds_dwordx4 v[118:119], off
	v_lshl_add_u64 v[118:119], s[82:83], 0, v[168:169]
	s_mov_b32 m0, s34
	s_nop 0
	global_load_lds_dwordx4 v[118:119], off
	s_waitcnt vmcnt(8)
	s_waitcnt lgkmcnt(0)
	s_barrier
	s_waitcnt lgkmcnt(0)
	v_mfma_f32_16x16x32_bf16 v[128:131], v[132:135], v[178:181], v[128:131]
	v_mfma_f32_16x16x32_bf16 v[124:127], v[140:143], v[178:181], v[124:127]
	v_mfma_f32_16x16x32_bf16 v[118:121], v[132:135], v[186:189], v[120:123]
	v_mfma_f32_16x16x32_bf16 v[114:117], v[140:143], v[186:189], v[114:117]
	v_mfma_f32_16x16x32_bf16 v[108:111], v[132:135], v[206:209], v[108:111]
	v_mfma_f32_16x16x32_bf16 v[104:107], v[140:143], v[206:209], v[104:107]
	v_mfma_f32_16x16x32_bf16 v[100:103], v[132:135], v[216:219], v[100:103]
	v_mfma_f32_16x16x32_bf16 v[96:99], v[140:143], v[216:219], v[96:99]
	v_mfma_f32_16x16x32_bf16 v[128:131], v[136:139], v[182:185], v[128:131]
	v_mfma_f32_16x16x32_bf16 v[124:127], v[144:147], v[182:185], v[124:127]
	v_mfma_f32_16x16x32_bf16 v[120:123], v[136:139], v[190:193], v[118:121]
	v_mfma_f32_16x16x32_bf16 v[116:119], v[144:147], v[190:193], v[114:117]
	v_mfma_f32_16x16x32_bf16 v[108:111], v[136:139], v[210:213], v[108:111]
	v_mfma_f32_16x16x32_bf16 v[104:107], v[144:147], v[210:213], v[104:107]
	v_mfma_f32_16x16x32_bf16 v[100:103], v[136:139], v[220:223], v[100:103]
	v_mfma_f32_16x16x32_bf16 v[96:99], v[144:147], v[220:223], v[96:99]
	v_mfma_f32_16x16x32_bf16 v[92:95], v[148:151], v[178:181], v[92:95]
	v_mfma_f32_16x16x32_bf16 v[88:91], v[156:159], v[178:181], v[88:91]
	v_mfma_f32_16x16x32_bf16 v[84:87], v[148:151], v[186:189], v[84:87]
	v_mfma_f32_16x16x32_bf16 v[80:83], v[156:159], v[186:189], v[80:83]
	v_mfma_f32_16x16x32_bf16 v[76:79], v[148:151], v[206:209], v[76:79]
	v_mfma_f32_16x16x32_bf16 v[72:75], v[156:159], v[206:209], v[72:75]
	v_mfma_f32_16x16x32_bf16 v[68:71], v[148:151], v[216:219], v[68:71]
	v_mfma_f32_16x16x32_bf16 v[64:67], v[156:159], v[216:219], v[64:67]
	v_mfma_f32_16x16x32_bf16 v[92:95], v[152:155], v[182:185], v[92:95]
	v_mfma_f32_16x16x32_bf16 v[88:91], v[160:163], v[182:185], v[88:91]
	v_mfma_f32_16x16x32_bf16 v[84:87], v[152:155], v[190:193], v[84:87]
	v_mfma_f32_16x16x32_bf16 v[80:83], v[160:163], v[190:193], v[80:83]
	v_mfma_f32_16x16x32_bf16 v[76:79], v[152:155], v[210:213], v[76:79]
	v_mfma_f32_16x16x32_bf16 v[72:75], v[160:163], v[210:213], v[72:75]
	v_mfma_f32_16x16x32_bf16 v[68:71], v[152:155], v[220:223], v[68:71]
	v_mfma_f32_16x16x32_bf16 v[64:67], v[160:163], v[220:223], v[64:67]
	s_barrier
	s_mov_b32 m0, s28
	v_lshl_add_u64 v[114:115], v[172:173], 0, s[56:57]
	ds_read_b128 v[178:181], v176 offset:49152
	ds_read_b128 v[182:185], v176 offset:50176
	ds_read_b128 v[186:189], v176 offset:51200
	ds_read_b128 v[190:193], v176 offset:52224
	ds_read_b128 v[206:209], v176 offset:53248
	ds_read_b128 v[210:213], v176 offset:54272
	ds_read_b128 v[216:219], v176 offset:55296
	ds_read_b128 v[220:223], v176 offset:56320
	global_load_lds_dwordx4 v[114:115], off
	v_lshl_add_u64 v[114:115], v[194:195], 0, s[56:57]
	s_mov_b32 m0, s45
	s_nop 0
	global_load_lds_dwordx4 v[114:115], off
	v_lshl_add_u64 v[114:115], s[80:81], 0, v[166:167]
	s_mov_b32 m0, s69
	s_nop 0
	global_load_lds_dwordx4 v[114:115], off
	v_lshl_add_u64 v[114:115], s[80:81], 0, v[170:171]
	s_mov_b32 m0, s49
	s_nop 0
	global_load_lds_dwordx4 v[114:115], off
	v_lshl_add_u64 v[114:115], v[224:225], 0, s[56:57]
	s_mov_b32 m0, s54
	s_nop 0
	global_load_lds_dwordx4 v[114:115], off
	v_lshl_add_u64 v[114:115], v[226:227], 0, s[56:57]
	s_mov_b32 m0, s55
	s_nop 0
	global_load_lds_dwordx4 v[114:115], off
	s_waitcnt vmcnt(8)
	s_waitcnt lgkmcnt(0)
	s_barrier
	s_waitcnt lgkmcnt(0)
	v_mfma_f32_16x16x32_bf16 v[60:63], v[132:135], v[178:181], v[60:63]
	v_mfma_f32_16x16x32_bf16 v[56:59], v[140:143], v[178:181], v[56:59]
	v_mfma_f32_16x16x32_bf16 v[52:55], v[132:135], v[186:189], v[52:55]
	v_mfma_f32_16x16x32_bf16 v[48:51], v[140:143], v[186:189], v[48:51]
	v_mfma_f32_16x16x32_bf16 v[44:47], v[132:135], v[206:209], v[44:47]
	v_mfma_f32_16x16x32_bf16 v[40:43], v[140:143], v[206:209], v[40:43]
	v_mfma_f32_16x16x32_bf16 v[36:39], v[132:135], v[216:219], v[36:39]
	v_mfma_f32_16x16x32_bf16 v[32:35], v[140:143], v[216:219], v[32:35]
	v_mfma_f32_16x16x32_bf16 v[60:63], v[136:139], v[182:185], v[60:63]
	v_mfma_f32_16x16x32_bf16 v[56:59], v[144:147], v[182:185], v[56:59]
	v_mfma_f32_16x16x32_bf16 v[52:55], v[136:139], v[190:193], v[52:55]
	v_mfma_f32_16x16x32_bf16 v[48:51], v[144:147], v[190:193], v[48:51]
	v_mfma_f32_16x16x32_bf16 v[44:47], v[136:139], v[210:213], v[44:47]
	v_mfma_f32_16x16x32_bf16 v[40:43], v[144:147], v[210:213], v[40:43]
	v_mfma_f32_16x16x32_bf16 v[36:39], v[136:139], v[220:223], v[36:39]
	v_mfma_f32_16x16x32_bf16 v[32:35], v[144:147], v[220:223], v[32:35]
	v_mfma_f32_16x16x32_bf16 v[28:31], v[148:151], v[178:181], v[28:31]
	v_mfma_f32_16x16x32_bf16 v[24:27], v[156:159], v[178:181], v[24:27]
	v_mfma_f32_16x16x32_bf16 v[20:23], v[148:151], v[186:189], v[20:23]
	v_mfma_f32_16x16x32_bf16 v[16:19], v[156:159], v[186:189], v[16:19]
	v_mfma_f32_16x16x32_bf16 v[12:15], v[148:151], v[206:209], v[12:15]
	v_mfma_f32_16x16x32_bf16 v[8:11], v[156:159], v[206:209], v[8:11]
	v_mfma_f32_16x16x32_bf16 v[4:7], v[148:151], v[216:219], v[4:7]
	v_mfma_f32_16x16x32_bf16 v[0:3], v[156:159], v[216:219], v[0:3]
	v_mfma_f32_16x16x32_bf16 v[28:31], v[152:155], v[182:185], v[28:31]
	v_mfma_f32_16x16x32_bf16 v[24:27], v[160:163], v[182:185], v[24:27]
	v_mfma_f32_16x16x32_bf16 v[20:23], v[152:155], v[190:193], v[20:23]
	v_mfma_f32_16x16x32_bf16 v[16:19], v[160:163], v[190:193], v[16:19]
	v_mfma_f32_16x16x32_bf16 v[12:15], v[152:155], v[210:213], v[12:15]
	v_mfma_f32_16x16x32_bf16 v[8:11], v[160:163], v[210:213], v[8:11]
	v_mfma_f32_16x16x32_bf16 v[4:7], v[152:155], v[220:223], v[4:7]
	v_mfma_f32_16x16x32_bf16 v[0:3], v[160:163], v[220:223], v[0:3]
	s_barrier
	s_andn2_b64 vcc, exec, s[78:79]
	s_mov_b64 s[50:51], -1
	s_mov_b64 s[78:79], 0
	s_mov_b64 s[80:81], 0x100
	s_cbranch_vccz .LBB0_758
	s_and_b64 vcc, exec, s[46:47]
	s_cbranch_vccz .LBB0_761
	s_barrier

.Lpeel_wo:
	s_add_u32 s28, s78, 0xfffc0080
	s_addc_u32 s29, s79, -1
	s_add_i32 s30, 0, 0x10000
	s_cmp_eq_u32 s84, 12
	s_cselect_b32 s83, s37, s29
	s_cselect_b32 s82, s50, s28
	v_add_u32_e32 v112, s30, v183
	s_cselect_b32 s81, s51, s77
	s_cselect_b32 s80, s65, s71
	s_add_i32 s31, 0, 0x14000
	ds_read_b128 v[130:133], v112
	ds_read_b128 v[134:137], v112 offset:1024
	ds_read_b128 v[150:153], v112 offset:2048
	ds_read_b128 v[154:157], v112 offset:3072
	v_add_u32_e32 v112, s31, v183
	ds_read_b128 v[158:161], v112
	ds_read_b128 v[162:165], v112 offset:1024
	ds_read_b128 v[166:169], v112 offset:2048
	ds_read_b128 v[170:173], v112 offset:3072
	v_lshl_add_u64 v[194:195], s[78:79], 0, v[146:147]
	s_add_i32 m0, s34, 0xc000
	ds_read_b128 v[174:177], v184
	ds_read_b128 v[178:181], v184 offset:1024
	ds_read_b128 v[186:189], v184 offset:2048
	ds_read_b128 v[190:193], v184 offset:3072
	ds_read_b128 v[206:209], v184 offset:4096
	ds_read_b128 v[210:213], v184 offset:5120
	ds_read_b128 v[216:219], v184 offset:6144
	ds_read_b128 v[220:223], v184 offset:7168
	global_load_lds_dwordx4 v[194:195], off
	v_lshl_add_u64 v[194:195], s[78:79], 0, v[148:149]
	s_add_i32 m0, s34, 0xe000
	s_nop 0
	global_load_lds_dwordx4 v[194:195], off
	s_waitcnt vmcnt(8)
	s_waitcnt lgkmcnt(0)
	s_barrier
	s_waitcnt lgkmcnt(0)
	v_mfma_f32_16x16x32_bf16 v[126:129], v[130:133], v[174:177], 0
	v_mfma_f32_16x16x32_bf16 v[122:125], v[150:153], v[174:177], 0
	v_mfma_f32_16x16x32_bf16 v[118:121], v[130:133], v[186:189], 0
	v_mfma_f32_16x16x32_bf16 v[114:117], v[150:153], v[186:189], 0
	v_mfma_f32_16x16x32_bf16 v[108:111], v[130:133], v[206:209], 0
	v_mfma_f32_16x16x32_bf16 v[104:107], v[150:153], v[206:209], 0
	v_mfma_f32_16x16x32_bf16 v[100:103], v[130:133], v[216:219], 0
	v_mfma_f32_16x16x32_bf16 v[96:99], v[150:153], v[216:219], 0
	v_mfma_f32_16x16x32_bf16 v[126:129], v[134:137], v[178:181], v[126:129]
	v_mfma_f32_16x16x32_bf16 v[122:125], v[154:157], v[178:181], v[122:125]
	v_mfma_f32_16x16x32_bf16 v[118:121], v[134:137], v[190:193], v[118:121]
	v_mfma_f32_16x16x32_bf16 v[114:117], v[154:157], v[190:193], v[114:117]
	v_mfma_f32_16x16x32_bf16 v[108:111], v[134:137], v[210:213], v[108:111]
	v_mfma_f32_16x16x32_bf16 v[104:107], v[154:157], v[210:213], v[104:107]
	v_mfma_f32_16x16x32_bf16 v[100:103], v[134:137], v[220:223], v[100:103]
	v_mfma_f32_16x16x32_bf16 v[96:99], v[154:157], v[220:223], v[96:99]
	v_mfma_f32_16x16x32_bf16 v[60:63], v[158:161], v[174:177], 0
	v_mfma_f32_16x16x32_bf16 v[56:59], v[166:169], v[174:177], 0
	v_mfma_f32_16x16x32_bf16 v[52:55], v[158:161], v[186:189], 0
	v_mfma_f32_16x16x32_bf16 v[48:51], v[166:169], v[186:189], 0
	v_mfma_f32_16x16x32_bf16 v[44:47], v[158:161], v[206:209], 0
	v_mfma_f32_16x16x32_bf16 v[40:43], v[166:169], v[206:209], 0
	v_mfma_f32_16x16x32_bf16 v[36:39], v[158:161], v[216:219], 0
	v_mfma_f32_16x16x32_bf16 v[32:35], v[166:169], v[216:219], 0
	v_mfma_f32_16x16x32_bf16 v[60:63], v[162:165], v[178:181], v[60:63]
	v_mfma_f32_16x16x32_bf16 v[56:59], v[170:173], v[178:181], v[56:59]
	v_mfma_f32_16x16x32_bf16 v[52:55], v[162:165], v[190:193], v[52:55]
	v_mfma_f32_16x16x32_bf16 v[48:51], v[170:173], v[190:193], v[48:51]
	v_mfma_f32_16x16x32_bf16 v[44:47], v[162:165], v[210:213], v[44:47]
	v_mfma_f32_16x16x32_bf16 v[40:43], v[170:173], v[210:213], v[40:43]
	v_mfma_f32_16x16x32_bf16 v[36:39], v[162:165], v[220:223], v[36:39]
	v_mfma_f32_16x16x32_bf16 v[32:35], v[170:173], v[220:223], v[32:35]
	s_barrier
	s_add_i32 s28, s30, s33
	v_lshl_add_u64 v[194:195], s[80:81], 0, v[140:141]
	s_mov_b32 m0, s28
	ds_read_b128 v[174:177], v184 offset:16384
	ds_read_b128 v[178:181], v184 offset:17408
	ds_read_b128 v[186:189], v184 offset:18432
	ds_read_b128 v[190:193], v184 offset:19456
	ds_read_b128 v[206:209], v184 offset:20480
	ds_read_b128 v[210:213], v184 offset:21504
	ds_read_b128 v[216:219], v184 offset:22528
	ds_read_b128 v[220:223], v184 offset:23552
	global_load_lds_dwordx4 v[194:195], off
	s_add_i32 m0, s28, 0x2000
	s_add_u32 s28, s80, 0x40000
	v_lshl_add_u64 v[224:225], s[80:81], 0, v[144:145]
	s_addc_u32 s29, s81, 0
	s_add_i32 s30, s31, s33
	global_load_lds_dwordx4 v[224:225], off
	v_lshl_add_u64 v[226:227], s[28:29], 0, v[140:141]
	s_mov_b32 m0, s30
	v_lshl_add_u64 v[228:229], s[82:83], 0, v[142:143]
	global_load_lds_dwordx4 v[226:227], off
	v_lshl_add_u64 v[226:227], s[28:29], 0, v[144:145]
	s_add_i32 m0, s30, 0x2000
	s_nop 0
	global_load_lds_dwordx4 v[226:227], off
	v_lshl_add_u64 v[226:227], s[82:83], 0, v[138:139]
	s_mov_b32 m0, s34
	s_nop 0
	global_load_lds_dwordx4 v[226:227], off
	s_mov_b32 m0, s54
	s_nop 0
	global_load_lds_dwordx4 v[228:229], off
	s_waitcnt vmcnt(8)
	s_waitcnt lgkmcnt(0)
	s_barrier
	s_waitcnt lgkmcnt(0)
	v_mfma_f32_16x16x32_bf16 v[92:95], v[130:133], v[174:177], 0
	v_mfma_f32_16x16x32_bf16 v[88:91], v[150:153], v[174:177], 0
	v_mfma_f32_16x16x32_bf16 v[84:87], v[130:133], v[186:189], 0
	v_mfma_f32_16x16x32_bf16 v[80:83], v[150:153], v[186:189], 0
	v_mfma_f32_16x16x32_bf16 v[76:79], v[130:133], v[206:209], 0
	v_mfma_f32_16x16x32_bf16 v[72:75], v[150:153], v[206:209], 0
	v_mfma_f32_16x16x32_bf16 v[68:71], v[130:133], v[216:219], 0
	v_mfma_f32_16x16x32_bf16 v[64:67], v[150:153], v[216:219], 0
	v_mfma_f32_16x16x32_bf16 v[92:95], v[134:137], v[178:181], v[92:95]
	v_mfma_f32_16x16x32_bf16 v[88:91], v[154:157], v[178:181], v[88:91]
	v_mfma_f32_16x16x32_bf16 v[84:87], v[134:137], v[190:193], v[84:87]
	v_mfma_f32_16x16x32_bf16 v[80:83], v[154:157], v[190:193], v[80:83]
	v_mfma_f32_16x16x32_bf16 v[76:79], v[134:137], v[210:213], v[76:79]
	v_mfma_f32_16x16x32_bf16 v[72:75], v[154:157], v[210:213], v[72:75]
	v_mfma_f32_16x16x32_bf16 v[68:71], v[134:137], v[220:223], v[68:71]
	v_mfma_f32_16x16x32_bf16 v[64:67], v[154:157], v[220:223], v[64:67]
	v_mfma_f32_16x16x32_bf16 v[28:31], v[158:161], v[174:177], 0
	v_mfma_f32_16x16x32_bf16 v[24:27], v[166:169], v[174:177], 0
	v_mfma_f32_16x16x32_bf16 v[20:23], v[158:161], v[186:189], 0
	v_mfma_f32_16x16x32_bf16 v[16:19], v[166:169], v[186:189], 0
	v_mfma_f32_16x16x32_bf16 v[12:15], v[158:161], v[206:209], 0
	v_mfma_f32_16x16x32_bf16 v[8:11], v[166:169], v[206:209], 0
	v_mfma_f32_16x16x32_bf16 v[4:7], v[158:161], v[216:219], 0
	v_mfma_f32_16x16x32_bf16 v[0:3], v[166:169], v[216:219], 0
	v_mfma_f32_16x16x32_bf16 v[28:31], v[162:165], v[178:181], v[28:31]
	v_mfma_f32_16x16x32_bf16 v[24:27], v[170:173], v[178:181], v[24:27]
	v_mfma_f32_16x16x32_bf16 v[20:23], v[162:165], v[190:193], v[20:23]
	v_mfma_f32_16x16x32_bf16 v[16:19], v[170:173], v[190:193], v[16:19]
	v_mfma_f32_16x16x32_bf16 v[12:15], v[162:165], v[210:213], v[12:15]
	v_mfma_f32_16x16x32_bf16 v[8:11], v[170:173], v[210:213], v[8:11]
	v_mfma_f32_16x16x32_bf16 v[4:7], v[162:165], v[220:223], v[4:7]
	v_mfma_f32_16x16x32_bf16 v[0:3], v[170:173], v[220:223], v[0:3]
	s_barrier
	s_add_i32 s30, 0, 0x18000
	v_add_u32_e32 v112, s30, v183
	s_add_i32 s31, 0, 0x1c000
	ds_read_b128 v[130:133], v112
	ds_read_b128 v[134:137], v112 offset:1024
	ds_read_b128 v[150:153], v112 offset:2048
	ds_read_b128 v[154:157], v112 offset:3072
	v_add_u32_e32 v112, s31, v183
	ds_read_b128 v[158:161], v112
	ds_read_b128 v[162:165], v112 offset:1024
	ds_read_b128 v[166:169], v112 offset:2048
	ds_read_b128 v[170:173], v112 offset:3072
	s_add_u32 s28, s82, 0x40000
	s_addc_u32 s29, s83, 0
	s_mov_b32 m0, s55
	v_lshl_add_u64 v[230:231], s[28:29], 0, v[138:139]
	ds_read_b128 v[174:177], v184 offset:32768
	ds_read_b128 v[178:181], v184 offset:33792
	ds_read_b128 v[186:189], v184 offset:34816
	ds_read_b128 v[190:193], v184 offset:35840
	ds_read_b128 v[206:209], v184 offset:36864
	ds_read_b128 v[210:213], v184 offset:37888
	ds_read_b128 v[216:219], v184 offset:38912
	ds_read_b128 v[220:223], v184 offset:39936
	global_load_lds_dwordx4 v[230:231], off
	v_lshl_add_u64 v[230:231], s[28:29], 0, v[142:143]
	s_mov_b32 m0, s58
	s_nop 0
	global_load_lds_dwordx4 v[230:231], off
	s_waitcnt vmcnt(8)
	s_waitcnt lgkmcnt(0)
	s_barrier
	s_waitcnt lgkmcnt(0)
	v_mfma_f32_16x16x32_bf16 v[126:129], v[130:133], v[174:177], v[126:129]
	v_mfma_f32_16x16x32_bf16 v[122:125], v[150:153], v[174:177], v[122:125]
	v_mfma_f32_16x16x32_bf16 v[118:121], v[130:133], v[186:189], v[118:121]
	v_mfma_f32_16x16x32_bf16 v[114:117], v[150:153], v[186:189], v[114:117]
	v_mfma_f32_16x16x32_bf16 v[108:111], v[130:133], v[206:209], v[108:111]
	v_mfma_f32_16x16x32_bf16 v[104:107], v[150:153], v[206:209], v[104:107]
	v_mfma_f32_16x16x32_bf16 v[100:103], v[130:133], v[216:219], v[100:103]
	v_mfma_f32_16x16x32_bf16 v[96:99], v[150:153], v[216:219], v[96:99]
	v_mfma_f32_16x16x32_bf16 v[126:129], v[134:137], v[178:181], v[126:129]
	v_mfma_f32_16x16x32_bf16 v[122:125], v[154:157], v[178:181], v[122:125]
	v_mfma_f32_16x16x32_bf16 v[118:121], v[134:137], v[190:193], v[118:121]
	v_mfma_f32_16x16x32_bf16 v[114:117], v[154:157], v[190:193], v[114:117]
	v_mfma_f32_16x16x32_bf16 v[108:111], v[134:137], v[210:213], v[108:111]
	v_mfma_f32_16x16x32_bf16 v[104:107], v[154:157], v[210:213], v[104:107]
	v_mfma_f32_16x16x32_bf16 v[100:103], v[134:137], v[220:223], v[100:103]
	v_mfma_f32_16x16x32_bf16 v[96:99], v[154:157], v[220:223], v[96:99]
	v_mfma_f32_16x16x32_bf16 v[60:63], v[158:161], v[174:177], v[60:63]
	v_mfma_f32_16x16x32_bf16 v[56:59], v[166:169], v[174:177], v[56:59]
	v_mfma_f32_16x16x32_bf16 v[52:55], v[158:161], v[186:189], v[52:55]
	v_mfma_f32_16x16x32_bf16 v[48:51], v[166:169], v[186:189], v[48:51]
	v_mfma_f32_16x16x32_bf16 v[44:47], v[158:161], v[206:209], v[44:47]
	v_mfma_f32_16x16x32_bf16 v[40:43], v[166:169], v[206:209], v[40:43]
	v_mfma_f32_16x16x32_bf16 v[36:39], v[158:161], v[216:219], v[36:39]
	v_mfma_f32_16x16x32_bf16 v[32:35], v[166:169], v[216:219], v[32:35]
	v_mfma_f32_16x16x32_bf16 v[60:63], v[162:165], v[178:181], v[60:63]
	v_mfma_f32_16x16x32_bf16 v[56:59], v[170:173], v[178:181], v[56:59]
	v_mfma_f32_16x16x32_bf16 v[52:55], v[162:165], v[190:193], v[52:55]
	v_mfma_f32_16x16x32_bf16 v[48:51], v[170:173], v[190:193], v[48:51]
	v_mfma_f32_16x16x32_bf16 v[44:47], v[162:165], v[210:213], v[44:47]
	v_mfma_f32_16x16x32_bf16 v[40:43], v[170:173], v[210:213], v[40:43]
	v_mfma_f32_16x16x32_bf16 v[36:39], v[162:165], v[220:223], v[36:39]
	v_mfma_f32_16x16x32_bf16 v[32:35], v[170:173], v[220:223], v[32:35]
	s_barrier
	s_add_i32 s28, s30, s33
	v_lshl_add_u64 v[194:195], v[194:195], 0, s[56:57]
	s_mov_b32 m0, s28
	ds_read_b128 v[174:177], v184 offset:49152
	ds_read_b128 v[178:181], v184 offset:50176
	ds_read_b128 v[186:189], v184 offset:51200
	ds_read_b128 v[190:193], v184 offset:52224
	ds_read_b128 v[206:209], v184 offset:53248
	ds_read_b128 v[210:213], v184 offset:54272
	ds_read_b128 v[216:219], v184 offset:55296
	ds_read_b128 v[220:223], v184 offset:56320
	global_load_lds_dwordx4 v[194:195], off
	s_add_i32 m0, s28, 0x2000
	s_add_u32 s28, s80, 0x40080
	v_lshl_add_u64 v[194:195], v[224:225], 0, s[56:57]
	s_addc_u32 s29, s81, 0
	s_add_i32 s30, s31, s33
	global_load_lds_dwordx4 v[194:195], off
	v_lshl_add_u64 v[194:195], s[28:29], 0, v[140:141]
	s_mov_b32 m0, s30
	s_nop 0
	global_load_lds_dwordx4 v[194:195], off
	v_lshl_add_u64 v[194:195], s[28:29], 0, v[144:145]
	s_add_i32 m0, s30, 0x2000
	s_nop 0
	global_load_lds_dwordx4 v[194:195], off
	v_lshl_add_u64 v[194:195], v[226:227], 0, s[56:57]
	s_mov_b32 m0, s86
	s_nop 0
	global_load_lds_dwordx4 v[194:195], off
	v_lshl_add_u64 v[194:195], v[228:229], 0, s[56:57]
	s_mov_b32 m0, s96
	s_nop 0
	global_load_lds_dwordx4 v[194:195], off
	s_waitcnt vmcnt(8)
	s_waitcnt lgkmcnt(0)
	s_barrier
	s_waitcnt lgkmcnt(0)
	v_mfma_f32_16x16x32_bf16 v[92:95], v[130:133], v[174:177], v[92:95]
	v_mfma_f32_16x16x32_bf16 v[88:91], v[150:153], v[174:177], v[88:91]
	v_mfma_f32_16x16x32_bf16 v[84:87], v[130:133], v[186:189], v[84:87]
	v_mfma_f32_16x16x32_bf16 v[80:83], v[150:153], v[186:189], v[80:83]
	v_mfma_f32_16x16x32_bf16 v[76:79], v[130:133], v[206:209], v[76:79]
	v_mfma_f32_16x16x32_bf16 v[72:75], v[150:153], v[206:209], v[72:75]
	v_mfma_f32_16x16x32_bf16 v[68:71], v[130:133], v[216:219], v[68:71]
	v_mfma_f32_16x16x32_bf16 v[64:67], v[150:153], v[216:219], v[64:67]
	v_mfma_f32_16x16x32_bf16 v[92:95], v[134:137], v[178:181], v[92:95]
	v_mfma_f32_16x16x32_bf16 v[88:91], v[154:157], v[178:181], v[88:91]
	v_mfma_f32_16x16x32_bf16 v[84:87], v[134:137], v[190:193], v[84:87]
	v_mfma_f32_16x16x32_bf16 v[80:83], v[154:157], v[190:193], v[80:83]
	v_mfma_f32_16x16x32_bf16 v[76:79], v[134:137], v[210:213], v[76:79]
	v_mfma_f32_16x16x32_bf16 v[72:75], v[154:157], v[210:213], v[72:75]
	v_mfma_f32_16x16x32_bf16 v[68:71], v[134:137], v[220:223], v[68:71]
	v_mfma_f32_16x16x32_bf16 v[64:67], v[154:157], v[220:223], v[64:67]
	v_mfma_f32_16x16x32_bf16 v[28:31], v[158:161], v[174:177], v[28:31]
	v_mfma_f32_16x16x32_bf16 v[24:27], v[166:169], v[174:177], v[24:27]
	v_mfma_f32_16x16x32_bf16 v[20:23], v[158:161], v[186:189], v[20:23]
	v_mfma_f32_16x16x32_bf16 v[16:19], v[166:169], v[186:189], v[16:19]
	v_mfma_f32_16x16x32_bf16 v[12:15], v[158:161], v[206:209], v[12:15]
	v_mfma_f32_16x16x32_bf16 v[8:11], v[166:169], v[206:209], v[8:11]
	v_mfma_f32_16x16x32_bf16 v[4:7], v[158:161], v[216:219], v[4:7]
	v_mfma_f32_16x16x32_bf16 v[0:3], v[166:169], v[216:219], v[0:3]
	v_mfma_f32_16x16x32_bf16 v[28:31], v[162:165], v[178:181], v[28:31]
	v_mfma_f32_16x16x32_bf16 v[24:27], v[170:173], v[178:181], v[24:27]
	v_mfma_f32_16x16x32_bf16 v[20:23], v[162:165], v[190:193], v[20:23]
	v_mfma_f32_16x16x32_bf16 v[16:19], v[170:173], v[190:193], v[16:19]
	v_mfma_f32_16x16x32_bf16 v[12:15], v[162:165], v[210:213], v[12:15]
	v_mfma_f32_16x16x32_bf16 v[8:11], v[170:173], v[210:213], v[8:11]
	v_mfma_f32_16x16x32_bf16 v[4:7], v[162:165], v[220:223], v[4:7]
	v_mfma_f32_16x16x32_bf16 v[0:3], v[170:173], v[220:223], v[0:3]
	s_barrier
	s_add_i32 s84, s84, 2
	s_add_u32 s78, s78, 0x100
	s_addc_u32 s79, s79, 0
	s_add_u32 s71, s71, 0x100
	s_addc_u32 s77, s77, 0
	s_cmp_gt_u32 s84, 13
.LBB0_836:
	s_add_u32 s28, s78, 0xfffc0080
	s_addc_u32 s29, s79, -1
	s_add_i32 s30, 0, 0x10000
	s_cmp_eq_u32 s84, 12
	s_cselect_b32 s83, s37, s29
	s_cselect_b32 s82, s50, s28
	v_add_u32_e32 v112, s30, v183
	s_cselect_b32 s81, s51, s77
	s_cselect_b32 s80, s65, s71
	s_add_i32 s31, 0, 0x14000
	ds_read_b128 v[130:133], v112
	ds_read_b128 v[134:137], v112 offset:1024
	ds_read_b128 v[150:153], v112 offset:2048
	ds_read_b128 v[154:157], v112 offset:3072
	v_add_u32_e32 v112, s31, v183
	ds_read_b128 v[158:161], v112
	ds_read_b128 v[162:165], v112 offset:1024
	ds_read_b128 v[166:169], v112 offset:2048
	ds_read_b128 v[170:173], v112 offset:3072
	v_lshl_add_u64 v[194:195], s[78:79], 0, v[146:147]
	s_add_i32 m0, s34, 0xc000
	ds_read_b128 v[174:177], v184
	ds_read_b128 v[178:181], v184 offset:1024
	ds_read_b128 v[186:189], v184 offset:2048
	ds_read_b128 v[190:193], v184 offset:3072
	ds_read_b128 v[206:209], v184 offset:4096
	ds_read_b128 v[210:213], v184 offset:5120
	ds_read_b128 v[216:219], v184 offset:6144
	ds_read_b128 v[220:223], v184 offset:7168
	global_load_lds_dwordx4 v[194:195], off
	v_lshl_add_u64 v[194:195], s[78:79], 0, v[148:149]
	s_add_i32 m0, s34, 0xe000
	s_nop 0
	global_load_lds_dwordx4 v[194:195], off
	s_waitcnt vmcnt(8)
	s_waitcnt lgkmcnt(0)
	s_barrier
	s_waitcnt lgkmcnt(0)
	v_mfma_f32_16x16x32_bf16 v[126:129], v[130:133], v[174:177], v[126:129]
	v_mfma_f32_16x16x32_bf16 v[122:125], v[150:153], v[174:177], v[122:125]
	v_mfma_f32_16x16x32_bf16 v[118:121], v[130:133], v[186:189], v[118:121]
	v_mfma_f32_16x16x32_bf16 v[114:117], v[150:153], v[186:189], v[114:117]
	v_mfma_f32_16x16x32_bf16 v[108:111], v[130:133], v[206:209], v[108:111]
	v_mfma_f32_16x16x32_bf16 v[104:107], v[150:153], v[206:209], v[104:107]
	v_mfma_f32_16x16x32_bf16 v[100:103], v[130:133], v[216:219], v[100:103]
	v_mfma_f32_16x16x32_bf16 v[96:99], v[150:153], v[216:219], v[96:99]
	v_mfma_f32_16x16x32_bf16 v[126:129], v[134:137], v[178:181], v[126:129]
	v_mfma_f32_16x16x32_bf16 v[122:125], v[154:157], v[178:181], v[122:125]
	v_mfma_f32_16x16x32_bf16 v[118:121], v[134:137], v[190:193], v[118:121]
	v_mfma_f32_16x16x32_bf16 v[114:117], v[154:157], v[190:193], v[114:117]
	v_mfma_f32_16x16x32_bf16 v[108:111], v[134:137], v[210:213], v[108:111]
	v_mfma_f32_16x16x32_bf16 v[104:107], v[154:157], v[210:213], v[104:107]
	v_mfma_f32_16x16x32_bf16 v[100:103], v[134:137], v[220:223], v[100:103]
	v_mfma_f32_16x16x32_bf16 v[96:99], v[154:157], v[220:223], v[96:99]
	v_mfma_f32_16x16x32_bf16 v[60:63], v[158:161], v[174:177], v[60:63]
	v_mfma_f32_16x16x32_bf16 v[56:59], v[166:169], v[174:177], v[56:59]
	v_mfma_f32_16x16x32_bf16 v[52:55], v[158:161], v[186:189], v[52:55]
	v_mfma_f32_16x16x32_bf16 v[48:51], v[166:169], v[186:189], v[48:51]
	v_mfma_f32_16x16x32_bf16 v[44:47], v[158:161], v[206:209], v[44:47]
	v_mfma_f32_16x16x32_bf16 v[40:43], v[166:169], v[206:209], v[40:43]
	v_mfma_f32_16x16x32_bf16 v[36:39], v[158:161], v[216:219], v[36:39]
	v_mfma_f32_16x16x32_bf16 v[32:35], v[166:169], v[216:219], v[32:35]
	v_mfma_f32_16x16x32_bf16 v[60:63], v[162:165], v[178:181], v[60:63]
	v_mfma_f32_16x16x32_bf16 v[56:59], v[170:173], v[178:181], v[56:59]
	v_mfma_f32_16x16x32_bf16 v[52:55], v[162:165], v[190:193], v[52:55]
	v_mfma_f32_16x16x32_bf16 v[48:51], v[170:173], v[190:193], v[48:51]
	v_mfma_f32_16x16x32_bf16 v[44:47], v[162:165], v[210:213], v[44:47]
	v_mfma_f32_16x16x32_bf16 v[40:43], v[170:173], v[210:213], v[40:43]
	v_mfma_f32_16x16x32_bf16 v[36:39], v[162:165], v[220:223], v[36:39]
	v_mfma_f32_16x16x32_bf16 v[32:35], v[170:173], v[220:223], v[32:35]
	s_barrier
	s_add_i32 s28, s30, s33
	v_lshl_add_u64 v[194:195], s[80:81], 0, v[140:141]
	s_mov_b32 m0, s28
	ds_read_b128 v[174:177], v184 offset:16384
	ds_read_b128 v[178:181], v184 offset:17408
	ds_read_b128 v[186:189], v184 offset:18432
	ds_read_b128 v[190:193], v184 offset:19456
	ds_read_b128 v[206:209], v184 offset:20480
	ds_read_b128 v[210:213], v184 offset:21504
	ds_read_b128 v[216:219], v184 offset:22528
	ds_read_b128 v[220:223], v184 offset:23552
	global_load_lds_dwordx4 v[194:195], off
	s_add_i32 m0, s28, 0x2000
	s_add_u32 s28, s80, 0x40000
	v_lshl_add_u64 v[224:225], s[80:81], 0, v[144:145]
	s_addc_u32 s29, s81, 0
	s_add_i32 s30, s31, s33
	global_load_lds_dwordx4 v[224:225], off
	v_lshl_add_u64 v[226:227], s[28:29], 0, v[140:141]
	s_mov_b32 m0, s30
	v_lshl_add_u64 v[228:229], s[82:83], 0, v[142:143]
	global_load_lds_dwordx4 v[226:227], off
	v_lshl_add_u64 v[226:227], s[28:29], 0, v[144:145]
	s_add_i32 m0, s30, 0x2000
	s_nop 0
	global_load_lds_dwordx4 v[226:227], off
	v_lshl_add_u64 v[226:227], s[82:83], 0, v[138:139]
	s_mov_b32 m0, s34
	s_nop 0
	global_load_lds_dwordx4 v[226:227], off
	s_mov_b32 m0, s54
	s_nop 0
	global_load_lds_dwordx4 v[228:229], off
	s_waitcnt vmcnt(8)
	s_waitcnt lgkmcnt(0)
	s_barrier
	s_waitcnt lgkmcnt(0)
	v_mfma_f32_16x16x32_bf16 v[92:95], v[130:133], v[174:177], v[92:95]
	v_mfma_f32_16x16x32_bf16 v[88:91], v[150:153], v[174:177], v[88:91]
	v_mfma_f32_16x16x32_bf16 v[84:87], v[130:133], v[186:189], v[84:87]
	v_mfma_f32_16x16x32_bf16 v[80:83], v[150:153], v[186:189], v[80:83]
	v_mfma_f32_16x16x32_bf16 v[76:79], v[130:133], v[206:209], v[76:79]
	v_mfma_f32_16x16x32_bf16 v[72:75], v[150:153], v[206:209], v[72:75]
	v_mfma_f32_16x16x32_bf16 v[68:71], v[130:133], v[216:219], v[68:71]
	v_mfma_f32_16x16x32_bf16 v[64:67], v[150:153], v[216:219], v[64:67]
	v_mfma_f32_16x16x32_bf16 v[92:95], v[134:137], v[178:181], v[92:95]
	v_mfma_f32_16x16x32_bf16 v[88:91], v[154:157], v[178:181], v[88:91]
	v_mfma_f32_16x16x32_bf16 v[84:87], v[134:137], v[190:193], v[84:87]
	v_mfma_f32_16x16x32_bf16 v[80:83], v[154:157], v[190:193], v[80:83]
	v_mfma_f32_16x16x32_bf16 v[76:79], v[134:137], v[210:213], v[76:79]
	v_mfma_f32_16x16x32_bf16 v[72:75], v[154:157], v[210:213], v[72:75]
	v_mfma_f32_16x16x32_bf16 v[68:71], v[134:137], v[220:223], v[68:71]
	v_mfma_f32_16x16x32_bf16 v[64:67], v[154:157], v[220:223], v[64:67]
	v_mfma_f32_16x16x32_bf16 v[28:31], v[158:161], v[174:177], v[28:31]
	v_mfma_f32_16x16x32_bf16 v[24:27], v[166:169], v[174:177], v[24:27]
	v_mfma_f32_16x16x32_bf16 v[20:23], v[158:161], v[186:189], v[20:23]
	v_mfma_f32_16x16x32_bf16 v[16:19], v[166:169], v[186:189], v[16:19]
	v_mfma_f32_16x16x32_bf16 v[12:15], v[158:161], v[206:209], v[12:15]
	v_mfma_f32_16x16x32_bf16 v[8:11], v[166:169], v[206:209], v[8:11]
	v_mfma_f32_16x16x32_bf16 v[4:7], v[158:161], v[216:219], v[4:7]
	v_mfma_f32_16x16x32_bf16 v[0:3], v[166:169], v[216:219], v[0:3]
	v_mfma_f32_16x16x32_bf16 v[28:31], v[162:165], v[178:181], v[28:31]
	v_mfma_f32_16x16x32_bf16 v[24:27], v[170:173], v[178:181], v[24:27]
	v_mfma_f32_16x16x32_bf16 v[20:23], v[162:165], v[190:193], v[20:23]
	v_mfma_f32_16x16x32_bf16 v[16:19], v[170:173], v[190:193], v[16:19]
	v_mfma_f32_16x16x32_bf16 v[12:15], v[162:165], v[210:213], v[12:15]
	v_mfma_f32_16x16x32_bf16 v[8:11], v[170:173], v[210:213], v[8:11]
	v_mfma_f32_16x16x32_bf16 v[4:7], v[162:165], v[220:223], v[4:7]
	v_mfma_f32_16x16x32_bf16 v[0:3], v[170:173], v[220:223], v[0:3]
	s_barrier
	s_add_i32 s30, 0, 0x18000
	v_add_u32_e32 v112, s30, v183
	s_add_i32 s31, 0, 0x1c000
	ds_read_b128 v[130:133], v112
	ds_read_b128 v[134:137], v112 offset:1024
	ds_read_b128 v[150:153], v112 offset:2048
	ds_read_b128 v[154:157], v112 offset:3072
	v_add_u32_e32 v112, s31, v183
	ds_read_b128 v[158:161], v112
	ds_read_b128 v[162:165], v112 offset:1024
	ds_read_b128 v[166:169], v112 offset:2048
	ds_read_b128 v[170:173], v112 offset:3072
	s_add_u32 s28, s82, 0x40000
	s_addc_u32 s29, s83, 0
	s_mov_b32 m0, s55
	v_lshl_add_u64 v[230:231], s[28:29], 0, v[138:139]
	ds_read_b128 v[174:177], v184 offset:32768
	ds_read_b128 v[178:181], v184 offset:33792
	ds_read_b128 v[186:189], v184 offset:34816
	ds_read_b128 v[190:193], v184 offset:35840
	ds_read_b128 v[206:209], v184 offset:36864
	ds_read_b128 v[210:213], v184 offset:37888
	ds_read_b128 v[216:219], v184 offset:38912
	ds_read_b128 v[220:223], v184 offset:39936
	global_load_lds_dwordx4 v[230:231], off
	v_lshl_add_u64 v[230:231], s[28:29], 0, v[142:143]
	s_mov_b32 m0, s58
	s_nop 0
	global_load_lds_dwordx4 v[230:231], off
	s_waitcnt vmcnt(8)
	s_waitcnt lgkmcnt(0)
	s_barrier
	s_waitcnt lgkmcnt(0)
	v_mfma_f32_16x16x32_bf16 v[126:129], v[130:133], v[174:177], v[126:129]
	v_mfma_f32_16x16x32_bf16 v[122:125], v[150:153], v[174:177], v[122:125]
	v_mfma_f32_16x16x32_bf16 v[118:121], v[130:133], v[186:189], v[118:121]
	v_mfma_f32_16x16x32_bf16 v[114:117], v[150:153], v[186:189], v[114:117]
	v_mfma_f32_16x16x32_bf16 v[108:111], v[130:133], v[206:209], v[108:111]
	v_mfma_f32_16x16x32_bf16 v[104:107], v[150:153], v[206:209], v[104:107]
	v_mfma_f32_16x16x32_bf16 v[100:103], v[130:133], v[216:219], v[100:103]
	v_mfma_f32_16x16x32_bf16 v[96:99], v[150:153], v[216:219], v[96:99]
	v_mfma_f32_16x16x32_bf16 v[126:129], v[134:137], v[178:181], v[126:129]
	v_mfma_f32_16x16x32_bf16 v[122:125], v[154:157], v[178:181], v[122:125]
	v_mfma_f32_16x16x32_bf16 v[118:121], v[134:137], v[190:193], v[118:121]
	v_mfma_f32_16x16x32_bf16 v[114:117], v[154:157], v[190:193], v[114:117]
	v_mfma_f32_16x16x32_bf16 v[108:111], v[134:137], v[210:213], v[108:111]
	v_mfma_f32_16x16x32_bf16 v[104:107], v[154:157], v[210:213], v[104:107]
	v_mfma_f32_16x16x32_bf16 v[100:103], v[134:137], v[220:223], v[100:103]
	v_mfma_f32_16x16x32_bf16 v[96:99], v[154:157], v[220:223], v[96:99]
	v_mfma_f32_16x16x32_bf16 v[60:63], v[158:161], v[174:177], v[60:63]
	v_mfma_f32_16x16x32_bf16 v[56:59], v[166:169], v[174:177], v[56:59]
	v_mfma_f32_16x16x32_bf16 v[52:55], v[158:161], v[186:189], v[52:55]
	v_mfma_f32_16x16x32_bf16 v[48:51], v[166:169], v[186:189], v[48:51]
	v_mfma_f32_16x16x32_bf16 v[44:47], v[158:161], v[206:209], v[44:47]
	v_mfma_f32_16x16x32_bf16 v[40:43], v[166:169], v[206:209], v[40:43]
	v_mfma_f32_16x16x32_bf16 v[36:39], v[158:161], v[216:219], v[36:39]
	v_mfma_f32_16x16x32_bf16 v[32:35], v[166:169], v[216:219], v[32:35]
	v_mfma_f32_16x16x32_bf16 v[60:63], v[162:165], v[178:181], v[60:63]
	v_mfma_f32_16x16x32_bf16 v[56:59], v[170:173], v[178:181], v[56:59]
	v_mfma_f32_16x16x32_bf16 v[52:55], v[162:165], v[190:193], v[52:55]
	v_mfma_f32_16x16x32_bf16 v[48:51], v[170:173], v[190:193], v[48:51]
	v_mfma_f32_16x16x32_bf16 v[44:47], v[162:165], v[210:213], v[44:47]
	v_mfma_f32_16x16x32_bf16 v[40:43], v[170:173], v[210:213], v[40:43]
	v_mfma_f32_16x16x32_bf16 v[36:39], v[162:165], v[220:223], v[36:39]
	v_mfma_f32_16x16x32_bf16 v[32:35], v[170:173], v[220:223], v[32:35]
	s_barrier
	s_add_i32 s28, s30, s33
	v_lshl_add_u64 v[194:195], v[194:195], 0, s[56:57]
	s_mov_b32 m0, s28
	ds_read_b128 v[174:177], v184 offset:49152
	ds_read_b128 v[178:181], v184 offset:50176
	ds_read_b128 v[186:189], v184 offset:51200
	ds_read_b128 v[190:193], v184 offset:52224
	ds_read_b128 v[206:209], v184 offset:53248
	ds_read_b128 v[210:213], v184 offset:54272
	ds_read_b128 v[216:219], v184 offset:55296
	ds_read_b128 v[220:223], v184 offset:56320
	global_load_lds_dwordx4 v[194:195], off
	s_add_i32 m0, s28, 0x2000
	s_add_u32 s28, s80, 0x40080
	v_lshl_add_u64 v[194:195], v[224:225], 0, s[56:57]
	s_addc_u32 s29, s81, 0
	s_add_i32 s30, s31, s33
	global_load_lds_dwordx4 v[194:195], off
	v_lshl_add_u64 v[194:195], s[28:29], 0, v[140:141]
	s_mov_b32 m0, s30
	s_nop 0
	global_load_lds_dwordx4 v[194:195], off
	v_lshl_add_u64 v[194:195], s[28:29], 0, v[144:145]
	s_add_i32 m0, s30, 0x2000
	s_nop 0
	global_load_lds_dwordx4 v[194:195], off
	v_lshl_add_u64 v[194:195], v[226:227], 0, s[56:57]
	s_mov_b32 m0, s86
	s_nop 0
	global_load_lds_dwordx4 v[194:195], off
	v_lshl_add_u64 v[194:195], v[228:229], 0, s[56:57]
	s_mov_b32 m0, s96
	s_nop 0
	global_load_lds_dwordx4 v[194:195], off
	s_waitcnt vmcnt(8)
	s_waitcnt lgkmcnt(0)
	s_barrier
	s_waitcnt lgkmcnt(0)
	v_mfma_f32_16x16x32_bf16 v[92:95], v[130:133], v[174:177], v[92:95]
	v_mfma_f32_16x16x32_bf16 v[88:91], v[150:153], v[174:177], v[88:91]
	v_mfma_f32_16x16x32_bf16 v[84:87], v[130:133], v[186:189], v[84:87]
	v_mfma_f32_16x16x32_bf16 v[80:83], v[150:153], v[186:189], v[80:83]
	v_mfma_f32_16x16x32_bf16 v[76:79], v[130:133], v[206:209], v[76:79]
	v_mfma_f32_16x16x32_bf16 v[72:75], v[150:153], v[206:209], v[72:75]
	v_mfma_f32_16x16x32_bf16 v[68:71], v[130:133], v[216:219], v[68:71]
	v_mfma_f32_16x16x32_bf16 v[64:67], v[150:153], v[216:219], v[64:67]
	v_mfma_f32_16x16x32_bf16 v[92:95], v[134:137], v[178:181], v[92:95]
	v_mfma_f32_16x16x32_bf16 v[88:91], v[154:157], v[178:181], v[88:91]
	v_mfma_f32_16x16x32_bf16 v[84:87], v[134:137], v[190:193], v[84:87]
	v_mfma_f32_16x16x32_bf16 v[80:83], v[154:157], v[190:193], v[80:83]
	v_mfma_f32_16x16x32_bf16 v[76:79], v[134:137], v[210:213], v[76:79]
	v_mfma_f32_16x16x32_bf16 v[72:75], v[154:157], v[210:213], v[72:75]
	v_mfma_f32_16x16x32_bf16 v[68:71], v[134:137], v[220:223], v[68:71]
	v_mfma_f32_16x16x32_bf16 v[64:67], v[154:157], v[220:223], v[64:67]
	v_mfma_f32_16x16x32_bf16 v[28:31], v[158:161], v[174:177], v[28:31]
	v_mfma_f32_16x16x32_bf16 v[24:27], v[166:169], v[174:177], v[24:27]
	v_mfma_f32_16x16x32_bf16 v[20:23], v[158:161], v[186:189], v[20:23]
	v_mfma_f32_16x16x32_bf16 v[16:19], v[166:169], v[186:189], v[16:19]
	v_mfma_f32_16x16x32_bf16 v[12:15], v[158:161], v[206:209], v[12:15]
	v_mfma_f32_16x16x32_bf16 v[8:11], v[166:169], v[206:209], v[8:11]
	v_mfma_f32_16x16x32_bf16 v[4:7], v[158:161], v[216:219], v[4:7]
	v_mfma_f32_16x16x32_bf16 v[0:3], v[166:169], v[216:219], v[0:3]
	v_mfma_f32_16x16x32_bf16 v[28:31], v[162:165], v[178:181], v[28:31]
	v_mfma_f32_16x16x32_bf16 v[24:27], v[170:173], v[178:181], v[24:27]
	v_mfma_f32_16x16x32_bf16 v[20:23], v[162:165], v[190:193], v[20:23]
	v_mfma_f32_16x16x32_bf16 v[16:19], v[170:173], v[190:193], v[16:19]
	v_mfma_f32_16x16x32_bf16 v[12:15], v[162:165], v[210:213], v[12:15]
	v_mfma_f32_16x16x32_bf16 v[8:11], v[170:173], v[210:213], v[8:11]
	v_mfma_f32_16x16x32_bf16 v[4:7], v[162:165], v[220:223], v[4:7]
	v_mfma_f32_16x16x32_bf16 v[0:3], v[170:173], v[220:223], v[0:3]
	s_barrier
	s_add_i32 s84, s84, 2
	s_add_u32 s78, s78, 0x100
	s_addc_u32 s79, s79, 0
	s_add_u32 s71, s71, 0x100
	s_addc_u32 s77, s77, 0
	s_cmp_gt_u32 s84, 13
	s_cbranch_scc0 .LBB0_836
	s_and_b64 vcc, exec, s[46:47]
	s_cbranch_vccz .LBB0_839
	s_barrier

.Lpeel_up_body:
	s_add_u32 s30, s94, s72
	s_addc_u32 s31, s95, s73
	s_add_u32 s45, s30, 0x28dd9100
	s_addc_u32 s55, s31, 0
	s_and_b64 s[30:31], s[40:41], exec
	s_cselect_b32 s77, s91, s55
	s_cselect_b32 s76, s90, s45
	s_add_u32 s45, s37, s72
	s_addc_u32 s55, s47, s73
	s_and_b64 s[30:31], s[40:41], exec
	s_cselect_b32 s75, s65, s55
	s_cselect_b32 s74, s64, s45
	s_add_i32 s55, 0, 0x10000
	s_add_i32 s58, 0, 0x14000
	v_add_u32_e32 v0, s55, v193
	v_add_u32_e32 v12, s58, v193
	ds_read_b128 v[16:19], v0
	ds_read_b128 v[20:23], v0 offset:1024
	ds_read_b128 v[24:27], v0 offset:2048
	ds_read_b128 v[28:31], v0 offset:3072
	ds_read_b128 v[0:3], v12
	ds_read_b128 v[4:7], v12 offset:1024
	ds_read_b128 v[8:11], v12 offset:2048
	ds_read_b128 v[12:15], v12 offset:3072
	v_lshl_add_u64 v[206:207], v[178:179], 0, s[72:73]
	s_add_i32 m0, s7, 0xc000
	ds_read_b128 v[180:183], v169
	ds_read_b128 v[184:187], v169 offset:1024
	ds_read_b128 v[224:227], v169 offset:2048
	ds_read_b128 v[228:231], v169 offset:3072
	ds_read_b128 v[232:235], v169 offset:4096
	ds_read_b128 v[236:239], v169 offset:5120
	ds_read_b128 v[240:243], v169 offset:6144
	ds_read_b128 v[244:247], v169 offset:7168
	global_load_lds_dwordx4 v[206:207], off
	v_lshl_add_u64 v[206:207], v[176:177], 0, s[72:73]
	s_add_i32 m0, s7, 0xe000
	s_nop 0
	global_load_lds_dwordx4 v[206:207], off
	s_waitcnt vmcnt(8)
	s_waitcnt lgkmcnt(0)
	s_barrier
	s_waitcnt lgkmcnt(0)
	v_mfma_scale_f32_16x16x128_f8f6f4 v[158:161], v[16:23], v[180:187], 0, v200, v201 op_sel_hi:[0,0,0]
	v_mfma_scale_f32_16x16x128_f8f6f4 v[150:153], v[24:31], v[180:187], 0, v200, v201 op_sel_hi:[0,0,0]
	v_mfma_scale_f32_16x16x128_f8f6f4 v[142:145], v[16:23], v[224:231], 0, v200, v201 op_sel_hi:[0,0,0]
	v_mfma_scale_f32_16x16x128_f8f6f4 v[134:137], v[24:31], v[224:231], 0, v200, v201 op_sel_hi:[0,0,0]
	v_mfma_scale_f32_16x16x128_f8f6f4 v[126:129], v[16:23], v[232:239], 0, v200, v201 op_sel_hi:[0,0,0]
	v_mfma_scale_f32_16x16x128_f8f6f4 v[118:121], v[24:31], v[232:239], 0, v200, v201 op_sel_hi:[0,0,0]
	v_mfma_scale_f32_16x16x128_f8f6f4 v[108:111], v[16:23], v[240:247], 0, v200, v201 op_sel_hi:[0,0,0]
	v_mfma_scale_f32_16x16x128_f8f6f4 v[100:103], v[24:31], v[240:247], 0, v200, v201 op_sel_hi:[0,0,0]
	v_mfma_scale_f32_16x16x128_f8f6f4 v[154:157], v[0:7], v[180:187], 0, v200, v201 op_sel_hi:[0,0,0]
	v_mfma_scale_f32_16x16x128_f8f6f4 v[146:149], v[8:15], v[180:187], 0, v200, v201 op_sel_hi:[0,0,0]
	v_mfma_scale_f32_16x16x128_f8f6f4 v[138:141], v[0:7], v[224:231], 0, v200, v201 op_sel_hi:[0,0,0]
	v_mfma_scale_f32_16x16x128_f8f6f4 v[130:133], v[8:15], v[224:231], 0, v200, v201 op_sel_hi:[0,0,0]
	v_mfma_scale_f32_16x16x128_f8f6f4 v[122:125], v[0:7], v[232:239], 0, v200, v201 op_sel_hi:[0,0,0]
	v_mfma_scale_f32_16x16x128_f8f6f4 v[114:117], v[8:15], v[232:239], 0, v200, v201 op_sel_hi:[0,0,0]
	v_mfma_scale_f32_16x16x128_f8f6f4 v[104:107], v[0:7], v[240:247], 0, v200, v201 op_sel_hi:[0,0,0]
	v_mfma_scale_f32_16x16x128_f8f6f4 v[96:99], v[8:15], v[240:247], 0, v200, v201 op_sel_hi:[0,0,0]
	s_barrier
	s_add_i32 s30, s55, s14
	v_lshl_add_u64 v[180:181], s[74:75], 0, v[164:165]
	s_mov_b32 m0, s30
	ds_read_b128 v[224:227], v169 offset:16384
	ds_read_b128 v[228:231], v169 offset:17408
	ds_read_b128 v[232:235], v169 offset:18432
	ds_read_b128 v[236:239], v169 offset:19456
	ds_read_b128 v[240:243], v169 offset:20480
	ds_read_b128 v[244:247], v169 offset:21504
	ds_read_b128 v[206:209], v169 offset:22528
	ds_read_b128 v[210:213], v169 offset:23552
	global_load_lds_dwordx4 v[180:181], off
	s_add_i32 m0, s30, 0x2000
	s_add_u32 s30, s74, 0x20000
	v_lshl_add_u64 v[182:183], s[74:75], 0, v[162:163]
	s_addc_u32 s31, s75, 0
	s_add_i32 s45, s58, s14
	global_load_lds_dwordx4 v[182:183], off
	v_lshl_add_u64 v[184:185], s[30:31], 0, v[164:165]
	s_mov_b32 m0, s45
	v_cndmask_b32_e64 v112, v168, v173, s[40:41]
	global_load_lds_dwordx4 v[184:185], off
	v_lshl_add_u64 v[184:185], s[30:31], 0, v[162:163]
	s_add_i32 m0, s45, 0x2000
	s_nop 0
	global_load_lds_dwordx4 v[184:185], off
	s_mov_b32 m0, s7
	v_lshl_add_u64 v[184:185], s[76:77], 0, v[112:113]
	global_load_lds_dwordx4 v112, s[76:77]
	v_cndmask_b32_e64 v112, v170, v175, s[40:41]
	s_mov_b32 m0, s33
	v_lshl_add_u64 v[186:187], s[76:77], 0, v[112:113]
	global_load_lds_dwordx4 v112, s[76:77]
	s_waitcnt vmcnt(8)
	s_waitcnt lgkmcnt(0)
	s_barrier
	s_waitcnt lgkmcnt(0)
	v_mfma_scale_f32_16x16x128_f8f6f4 v[92:95], v[16:23], v[224:231], 0, v200, v201 op_sel_hi:[0,0,0]
	v_mfma_scale_f32_16x16x128_f8f6f4 v[84:87], v[24:31], v[224:231], 0, v200, v201 op_sel_hi:[0,0,0]
	v_mfma_scale_f32_16x16x128_f8f6f4 v[76:79], v[16:23], v[232:239], 0, v200, v201 op_sel_hi:[0,0,0]
	v_mfma_scale_f32_16x16x128_f8f6f4 v[68:71], v[24:31], v[232:239], 0, v200, v201 op_sel_hi:[0,0,0]
	v_mfma_scale_f32_16x16x128_f8f6f4 v[60:63], v[16:23], v[240:247], 0, v200, v201 op_sel_hi:[0,0,0]
	v_mfma_scale_f32_16x16x128_f8f6f4 v[52:55], v[24:31], v[240:247], 0, v200, v201 op_sel_hi:[0,0,0]
	v_mfma_scale_f32_16x16x128_f8f6f4 v[44:47], v[16:23], v[206:213], 0, v200, v201 op_sel_hi:[0,0,0]
	v_mfma_scale_f32_16x16x128_f8f6f4 v[36:39], v[24:31], v[206:213], 0, v200, v201 op_sel_hi:[0,0,0]
	v_mfma_scale_f32_16x16x128_f8f6f4 v[88:91], v[0:7], v[224:231], 0, v200, v201 op_sel_hi:[0,0,0]
	v_mfma_scale_f32_16x16x128_f8f6f4 v[80:83], v[8:15], v[224:231], 0, v200, v201 op_sel_hi:[0,0,0]
	v_mfma_scale_f32_16x16x128_f8f6f4 v[72:75], v[0:7], v[232:239], 0, v200, v201 op_sel_hi:[0,0,0]
	v_mfma_scale_f32_16x16x128_f8f6f4 v[64:67], v[8:15], v[232:239], 0, v200, v201 op_sel_hi:[0,0,0]
	v_mfma_scale_f32_16x16x128_f8f6f4 v[56:59], v[0:7], v[240:247], 0, v200, v201 op_sel_hi:[0,0,0]
	v_mfma_scale_f32_16x16x128_f8f6f4 v[48:51], v[8:15], v[240:247], 0, v200, v201 op_sel_hi:[0,0,0]
	v_mfma_scale_f32_16x16x128_f8f6f4 v[40:43], v[0:7], v[206:213], 0, v200, v201 op_sel_hi:[0,0,0]
	v_mfma_scale_f32_16x16x128_f8f6f4 v[32:35], v[8:15], v[206:213], 0, v200, v201 op_sel_hi:[0,0,0]
	s_barrier
	s_add_i32 s30, 0, 0x18000
	s_add_i32 s45, 0, 0x1c000
	v_add_u32_e32 v12, s30, v193
	v_add_u32_e32 v28, s45, v193
	ds_read_b128 v[0:3], v12
	ds_read_b128 v[4:7], v12 offset:1024
	ds_read_b128 v[8:11], v12 offset:2048
	ds_read_b128 v[12:15], v12 offset:3072
	ds_read_b128 v[16:19], v28
	ds_read_b128 v[20:23], v28 offset:1024
	ds_read_b128 v[24:27], v28 offset:2048
	ds_read_b128 v[28:31], v28 offset:3072
	s_mov_b32 m0, s34
	v_cndmask_b32_e64 v112, v172, v217, s[40:41]
	ds_read_b128 v[206:209], v169 offset:32768
	ds_read_b128 v[210:213], v169 offset:33792
	ds_read_b128 v[224:227], v169 offset:34816
	ds_read_b128 v[228:231], v169 offset:35840
	ds_read_b128 v[232:235], v169 offset:36864
	ds_read_b128 v[236:239], v169 offset:37888
	ds_read_b128 v[240:243], v169 offset:38912
	ds_read_b128 v[244:247], v169 offset:39936
	global_load_lds_dwordx4 v112, s[76:77]
	v_cndmask_b32_e64 v112, v174, v218, s[40:41]
	s_mov_b32 m0, s50
	s_nop 0
	global_load_lds_dwordx4 v112, s[76:77]
	s_waitcnt vmcnt(8)
	s_waitcnt lgkmcnt(0)
	s_barrier
	s_waitcnt lgkmcnt(0)
	v_mfma_scale_f32_16x16x128_f8f6f4 v[158:161], v[0:7], v[206:213], v[158:161], v200, v201 op_sel_hi:[0,0,0]
	v_mfma_scale_f32_16x16x128_f8f6f4 v[150:153], v[8:15], v[206:213], v[150:153], v200, v201 op_sel_hi:[0,0,0]
	v_mfma_scale_f32_16x16x128_f8f6f4 v[142:145], v[0:7], v[224:231], v[142:145], v200, v201 op_sel_hi:[0,0,0]
	v_mfma_scale_f32_16x16x128_f8f6f4 v[134:137], v[8:15], v[224:231], v[134:137], v200, v201 op_sel_hi:[0,0,0]
	v_mfma_scale_f32_16x16x128_f8f6f4 v[126:129], v[0:7], v[232:239], v[126:129], v200, v201 op_sel_hi:[0,0,0]
	v_mfma_scale_f32_16x16x128_f8f6f4 v[118:121], v[8:15], v[232:239], v[118:121], v200, v201 op_sel_hi:[0,0,0]
	v_mfma_scale_f32_16x16x128_f8f6f4 v[108:111], v[0:7], v[240:247], v[108:111], v200, v201 op_sel_hi:[0,0,0]
	v_mfma_scale_f32_16x16x128_f8f6f4 v[100:103], v[8:15], v[240:247], v[100:103], v200, v201 op_sel_hi:[0,0,0]
	v_mfma_scale_f32_16x16x128_f8f6f4 v[154:157], v[16:23], v[206:213], v[154:157], v200, v201 op_sel_hi:[0,0,0]
	v_mfma_scale_f32_16x16x128_f8f6f4 v[146:149], v[24:31], v[206:213], v[146:149], v200, v201 op_sel_hi:[0,0,0]
	v_mfma_scale_f32_16x16x128_f8f6f4 v[138:141], v[16:23], v[224:231], v[138:141], v200, v201 op_sel_hi:[0,0,0]
	v_mfma_scale_f32_16x16x128_f8f6f4 v[130:133], v[24:31], v[224:231], v[130:133], v200, v201 op_sel_hi:[0,0,0]
	v_mfma_scale_f32_16x16x128_f8f6f4 v[122:125], v[16:23], v[232:239], v[122:125], v200, v201 op_sel_hi:[0,0,0]
	v_mfma_scale_f32_16x16x128_f8f6f4 v[114:117], v[24:31], v[232:239], v[114:117], v200, v201 op_sel_hi:[0,0,0]
	v_mfma_scale_f32_16x16x128_f8f6f4 v[104:107], v[16:23], v[240:247], v[104:107], v200, v201 op_sel_hi:[0,0,0]
	v_mfma_scale_f32_16x16x128_f8f6f4 v[96:99], v[24:31], v[240:247], v[96:99], v200, v201 op_sel_hi:[0,0,0]
	s_barrier
	s_add_i32 s30, s30, s14
	v_lshl_add_u64 v[180:181], v[180:181], 0, s[56:57]
	s_mov_b32 m0, s30
	ds_read_b128 v[206:209], v169 offset:49152
	ds_read_b128 v[210:213], v169 offset:50176
	ds_read_b128 v[224:227], v169 offset:51200
	ds_read_b128 v[228:231], v169 offset:52224
	ds_read_b128 v[232:235], v169 offset:53248
	ds_read_b128 v[236:239], v169 offset:54272
	ds_read_b128 v[240:243], v169 offset:55296
	ds_read_b128 v[244:247], v169 offset:56320
	global_load_lds_dwordx4 v[180:181], off
	s_add_i32 m0, s30, 0x2000
	s_add_u32 s30, s74, 0x20080
	v_lshl_add_u64 v[180:181], v[182:183], 0, s[56:57]
	s_addc_u32 s31, s75, 0
	s_add_i32 s40, s45, s14
	global_load_lds_dwordx4 v[180:181], off
	v_lshl_add_u64 v[180:181], s[30:31], 0, v[164:165]
	s_mov_b32 m0, s40
	s_nop 0
	global_load_lds_dwordx4 v[180:181], off
	v_lshl_add_u64 v[180:181], s[30:31], 0, v[162:163]
	s_add_i32 m0, s40, 0x2000
	s_nop 0
	global_load_lds_dwordx4 v[180:181], off
	v_lshl_add_u64 v[180:181], v[184:185], 0, s[56:57]
	s_mov_b32 m0, s4
	s_nop 0
	global_load_lds_dwordx4 v[180:181], off
	v_lshl_add_u64 v[180:181], v[186:187], 0, s[56:57]
	s_mov_b32 m0, s51
	s_nop 0
	global_load_lds_dwordx4 v[180:181], off
	s_waitcnt vmcnt(8)
	s_waitcnt lgkmcnt(0)
	s_barrier
	s_waitcnt lgkmcnt(0)
	v_mfma_scale_f32_16x16x128_f8f6f4 v[92:95], v[0:7], v[206:213], v[92:95], v200, v201 op_sel_hi:[0,0,0]
	v_mfma_scale_f32_16x16x128_f8f6f4 v[84:87], v[8:15], v[206:213], v[84:87], v200, v201 op_sel_hi:[0,0,0]
	v_mfma_scale_f32_16x16x128_f8f6f4 v[76:79], v[0:7], v[224:231], v[76:79], v200, v201 op_sel_hi:[0,0,0]
	v_mfma_scale_f32_16x16x128_f8f6f4 v[68:71], v[8:15], v[224:231], v[68:71], v200, v201 op_sel_hi:[0,0,0]
	v_mfma_scale_f32_16x16x128_f8f6f4 v[60:63], v[0:7], v[232:239], v[60:63], v200, v201 op_sel_hi:[0,0,0]
	v_mfma_scale_f32_16x16x128_f8f6f4 v[52:55], v[8:15], v[232:239], v[52:55], v200, v201 op_sel_hi:[0,0,0]
	v_mfma_scale_f32_16x16x128_f8f6f4 v[44:47], v[0:7], v[240:247], v[44:47], v200, v201 op_sel_hi:[0,0,0]
	v_mfma_scale_f32_16x16x128_f8f6f4 v[36:39], v[8:15], v[240:247], v[36:39], v200, v201 op_sel_hi:[0,0,0]
	v_mfma_scale_f32_16x16x128_f8f6f4 v[88:91], v[16:23], v[206:213], v[88:91], v200, v201 op_sel_hi:[0,0,0]
	v_mfma_scale_f32_16x16x128_f8f6f4 v[80:83], v[24:31], v[206:213], v[80:83], v200, v201 op_sel_hi:[0,0,0]
	v_mfma_scale_f32_16x16x128_f8f6f4 v[72:75], v[16:23], v[224:231], v[72:75], v200, v201 op_sel_hi:[0,0,0]
	v_mfma_scale_f32_16x16x128_f8f6f4 v[64:67], v[24:31], v[224:231], v[64:67], v200, v201 op_sel_hi:[0,0,0]
	v_mfma_scale_f32_16x16x128_f8f6f4 v[56:59], v[16:23], v[232:239], v[56:59], v200, v201 op_sel_hi:[0,0,0]
	v_mfma_scale_f32_16x16x128_f8f6f4 v[48:51], v[24:31], v[232:239], v[48:51], v200, v201 op_sel_hi:[0,0,0]
	v_mfma_scale_f32_16x16x128_f8f6f4 v[40:43], v[16:23], v[240:247], v[40:43], v200, v201 op_sel_hi:[0,0,0]
	v_mfma_scale_f32_16x16x128_f8f6f4 v[32:35], v[24:31], v[240:247], v[32:35], v200, v201 op_sel_hi:[0,0,0]
	s_barrier
	s_add_i32 s49, s49, 2
	s_add_u32 s72, s72, 0x100
	s_addc_u32 s73, s73, 0
	s_cmp_gt_u32 s49, 5
	s_cbranch_scc1 .LBB0_1092
	s_branch .LBB0_1090
.LBB0_1089:
	s_add_u32 s30, s94, s72
	s_addc_u32 s31, s95, s73
	s_add_u32 s45, s30, 0x28dd9100
	s_addc_u32 s55, s31, 0
	s_and_b64 s[30:31], s[40:41], exec
	s_cselect_b32 s77, s91, s55
	s_cselect_b32 s76, s90, s45
	s_add_u32 s45, s37, s72
	s_addc_u32 s55, s47, s73
	s_and_b64 s[30:31], s[40:41], exec
	s_cselect_b32 s75, s65, s55
	s_cselect_b32 s74, s64, s45
	s_add_i32 s55, 0, 0x10000
	s_add_i32 s58, 0, 0x14000
	v_add_u32_e32 v0, s55, v193
	v_add_u32_e32 v12, s58, v193
	ds_read_b128 v[16:19], v0
	ds_read_b128 v[20:23], v0 offset:1024
	ds_read_b128 v[24:27], v0 offset:2048
	ds_read_b128 v[28:31], v0 offset:3072
	ds_read_b128 v[0:3], v12
	ds_read_b128 v[4:7], v12 offset:1024
	ds_read_b128 v[8:11], v12 offset:2048
	ds_read_b128 v[12:15], v12 offset:3072
	v_lshl_add_u64 v[206:207], v[178:179], 0, s[72:73]
	s_add_i32 m0, s7, 0xc000
	ds_read_b128 v[180:183], v169
	ds_read_b128 v[184:187], v169 offset:1024
	ds_read_b128 v[224:227], v169 offset:2048
	ds_read_b128 v[228:231], v169 offset:3072
	ds_read_b128 v[232:235], v169 offset:4096
	ds_read_b128 v[236:239], v169 offset:5120
	ds_read_b128 v[240:243], v169 offset:6144
	ds_read_b128 v[244:247], v169 offset:7168
	global_load_lds_dwordx4 v[206:207], off
	v_lshl_add_u64 v[206:207], v[176:177], 0, s[72:73]
	s_add_i32 m0, s7, 0xe000
	s_nop 0
	global_load_lds_dwordx4 v[206:207], off
	s_waitcnt vmcnt(8)
	s_waitcnt lgkmcnt(0)
	s_barrier
	s_waitcnt lgkmcnt(0)
	v_mfma_scale_f32_16x16x128_f8f6f4 v[158:161], v[16:23], v[180:187], v[158:161], v200, v201 op_sel_hi:[0,0,0]
	v_mfma_scale_f32_16x16x128_f8f6f4 v[150:153], v[24:31], v[180:187], v[150:153], v200, v201 op_sel_hi:[0,0,0]
	v_mfma_scale_f32_16x16x128_f8f6f4 v[142:145], v[16:23], v[224:231], v[142:145], v200, v201 op_sel_hi:[0,0,0]
	v_mfma_scale_f32_16x16x128_f8f6f4 v[134:137], v[24:31], v[224:231], v[134:137], v200, v201 op_sel_hi:[0,0,0]
	v_mfma_scale_f32_16x16x128_f8f6f4 v[126:129], v[16:23], v[232:239], v[126:129], v200, v201 op_sel_hi:[0,0,0]
	v_mfma_scale_f32_16x16x128_f8f6f4 v[118:121], v[24:31], v[232:239], v[118:121], v200, v201 op_sel_hi:[0,0,0]
	v_mfma_scale_f32_16x16x128_f8f6f4 v[108:111], v[16:23], v[240:247], v[108:111], v200, v201 op_sel_hi:[0,0,0]
	v_mfma_scale_f32_16x16x128_f8f6f4 v[100:103], v[24:31], v[240:247], v[100:103], v200, v201 op_sel_hi:[0,0,0]
	v_mfma_scale_f32_16x16x128_f8f6f4 v[154:157], v[0:7], v[180:187], v[154:157], v200, v201 op_sel_hi:[0,0,0]
	v_mfma_scale_f32_16x16x128_f8f6f4 v[146:149], v[8:15], v[180:187], v[146:149], v200, v201 op_sel_hi:[0,0,0]
	v_mfma_scale_f32_16x16x128_f8f6f4 v[138:141], v[0:7], v[224:231], v[138:141], v200, v201 op_sel_hi:[0,0,0]
	v_mfma_scale_f32_16x16x128_f8f6f4 v[130:133], v[8:15], v[224:231], v[130:133], v200, v201 op_sel_hi:[0,0,0]
	v_mfma_scale_f32_16x16x128_f8f6f4 v[122:125], v[0:7], v[232:239], v[122:125], v200, v201 op_sel_hi:[0,0,0]
	v_mfma_scale_f32_16x16x128_f8f6f4 v[114:117], v[8:15], v[232:239], v[114:117], v200, v201 op_sel_hi:[0,0,0]
	v_mfma_scale_f32_16x16x128_f8f6f4 v[104:107], v[0:7], v[240:247], v[104:107], v200, v201 op_sel_hi:[0,0,0]
	v_mfma_scale_f32_16x16x128_f8f6f4 v[96:99], v[8:15], v[240:247], v[96:99], v200, v201 op_sel_hi:[0,0,0]
	s_barrier
	s_add_i32 s30, s55, s14
	v_lshl_add_u64 v[180:181], s[74:75], 0, v[164:165]
	s_mov_b32 m0, s30
	ds_read_b128 v[224:227], v169 offset:16384
	ds_read_b128 v[228:231], v169 offset:17408
	ds_read_b128 v[232:235], v169 offset:18432
	ds_read_b128 v[236:239], v169 offset:19456
	ds_read_b128 v[240:243], v169 offset:20480
	ds_read_b128 v[244:247], v169 offset:21504
	ds_read_b128 v[206:209], v169 offset:22528
	ds_read_b128 v[210:213], v169 offset:23552
	global_load_lds_dwordx4 v[180:181], off
	s_add_i32 m0, s30, 0x2000
	s_add_u32 s30, s74, 0x20000
	v_lshl_add_u64 v[182:183], s[74:75], 0, v[162:163]
	s_addc_u32 s31, s75, 0
	s_add_i32 s45, s58, s14
	global_load_lds_dwordx4 v[182:183], off
	v_lshl_add_u64 v[184:185], s[30:31], 0, v[164:165]
	s_mov_b32 m0, s45
	v_cndmask_b32_e64 v112, v168, v173, s[40:41]
	global_load_lds_dwordx4 v[184:185], off
	v_lshl_add_u64 v[184:185], s[30:31], 0, v[162:163]
	s_add_i32 m0, s45, 0x2000
	s_nop 0
	global_load_lds_dwordx4 v[184:185], off
	s_mov_b32 m0, s7
	v_lshl_add_u64 v[184:185], s[76:77], 0, v[112:113]
	global_load_lds_dwordx4 v112, s[76:77]
	v_cndmask_b32_e64 v112, v170, v175, s[40:41]
	s_mov_b32 m0, s33
	v_lshl_add_u64 v[186:187], s[76:77], 0, v[112:113]
	global_load_lds_dwordx4 v112, s[76:77]
	s_waitcnt vmcnt(8)
	s_waitcnt lgkmcnt(0)
	s_barrier
	s_waitcnt lgkmcnt(0)
	v_mfma_scale_f32_16x16x128_f8f6f4 v[92:95], v[16:23], v[224:231], v[92:95], v200, v201 op_sel_hi:[0,0,0]
	v_mfma_scale_f32_16x16x128_f8f6f4 v[84:87], v[24:31], v[224:231], v[84:87], v200, v201 op_sel_hi:[0,0,0]
	v_mfma_scale_f32_16x16x128_f8f6f4 v[76:79], v[16:23], v[232:239], v[76:79], v200, v201 op_sel_hi:[0,0,0]
	v_mfma_scale_f32_16x16x128_f8f6f4 v[68:71], v[24:31], v[232:239], v[68:71], v200, v201 op_sel_hi:[0,0,0]
	v_mfma_scale_f32_16x16x128_f8f6f4 v[60:63], v[16:23], v[240:247], v[60:63], v200, v201 op_sel_hi:[0,0,0]
	v_mfma_scale_f32_16x16x128_f8f6f4 v[52:55], v[24:31], v[240:247], v[52:55], v200, v201 op_sel_hi:[0,0,0]
	v_mfma_scale_f32_16x16x128_f8f6f4 v[44:47], v[16:23], v[206:213], v[44:47], v200, v201 op_sel_hi:[0,0,0]
	v_mfma_scale_f32_16x16x128_f8f6f4 v[36:39], v[24:31], v[206:213], v[36:39], v200, v201 op_sel_hi:[0,0,0]
	v_mfma_scale_f32_16x16x128_f8f6f4 v[88:91], v[0:7], v[224:231], v[88:91], v200, v201 op_sel_hi:[0,0,0]
	v_mfma_scale_f32_16x16x128_f8f6f4 v[80:83], v[8:15], v[224:231], v[80:83], v200, v201 op_sel_hi:[0,0,0]
	v_mfma_scale_f32_16x16x128_f8f6f4 v[72:75], v[0:7], v[232:239], v[72:75], v200, v201 op_sel_hi:[0,0,0]
	v_mfma_scale_f32_16x16x128_f8f6f4 v[64:67], v[8:15], v[232:239], v[64:67], v200, v201 op_sel_hi:[0,0,0]
	v_mfma_scale_f32_16x16x128_f8f6f4 v[56:59], v[0:7], v[240:247], v[56:59], v200, v201 op_sel_hi:[0,0,0]
	v_mfma_scale_f32_16x16x128_f8f6f4 v[48:51], v[8:15], v[240:247], v[48:51], v200, v201 op_sel_hi:[0,0,0]
	v_mfma_scale_f32_16x16x128_f8f6f4 v[40:43], v[0:7], v[206:213], v[40:43], v200, v201 op_sel_hi:[0,0,0]
	v_mfma_scale_f32_16x16x128_f8f6f4 v[32:35], v[8:15], v[206:213], v[32:35], v200, v201 op_sel_hi:[0,0,0]
	s_barrier
	s_add_i32 s30, 0, 0x18000
	s_add_i32 s45, 0, 0x1c000
	v_add_u32_e32 v12, s30, v193
	v_add_u32_e32 v28, s45, v193
	ds_read_b128 v[0:3], v12
	ds_read_b128 v[4:7], v12 offset:1024
	ds_read_b128 v[8:11], v12 offset:2048
	ds_read_b128 v[12:15], v12 offset:3072
	ds_read_b128 v[16:19], v28
	ds_read_b128 v[20:23], v28 offset:1024
	ds_read_b128 v[24:27], v28 offset:2048
	ds_read_b128 v[28:31], v28 offset:3072
	s_mov_b32 m0, s34
	v_cndmask_b32_e64 v112, v172, v217, s[40:41]
	ds_read_b128 v[206:209], v169 offset:32768
	ds_read_b128 v[210:213], v169 offset:33792
	ds_read_b128 v[224:227], v169 offset:34816
	ds_read_b128 v[228:231], v169 offset:35840
	ds_read_b128 v[232:235], v169 offset:36864
	ds_read_b128 v[236:239], v169 offset:37888
	ds_read_b128 v[240:243], v169 offset:38912
	ds_read_b128 v[244:247], v169 offset:39936
	global_load_lds_dwordx4 v112, s[76:77]
	v_cndmask_b32_e64 v112, v174, v218, s[40:41]
	s_mov_b32 m0, s50
	s_nop 0
	global_load_lds_dwordx4 v112, s[76:77]
	s_waitcnt vmcnt(8)
	s_waitcnt lgkmcnt(0)
	s_barrier
	s_waitcnt lgkmcnt(0)
	v_mfma_scale_f32_16x16x128_f8f6f4 v[158:161], v[0:7], v[206:213], v[158:161], v200, v201 op_sel_hi:[0,0,0]
	v_mfma_scale_f32_16x16x128_f8f6f4 v[150:153], v[8:15], v[206:213], v[150:153], v200, v201 op_sel_hi:[0,0,0]
	v_mfma_scale_f32_16x16x128_f8f6f4 v[142:145], v[0:7], v[224:231], v[142:145], v200, v201 op_sel_hi:[0,0,0]
	v_mfma_scale_f32_16x16x128_f8f6f4 v[134:137], v[8:15], v[224:231], v[134:137], v200, v201 op_sel_hi:[0,0,0]
	v_mfma_scale_f32_16x16x128_f8f6f4 v[126:129], v[0:7], v[232:239], v[126:129], v200, v201 op_sel_hi:[0,0,0]
	v_mfma_scale_f32_16x16x128_f8f6f4 v[118:121], v[8:15], v[232:239], v[118:121], v200, v201 op_sel_hi:[0,0,0]
	v_mfma_scale_f32_16x16x128_f8f6f4 v[108:111], v[0:7], v[240:247], v[108:111], v200, v201 op_sel_hi:[0,0,0]
	v_mfma_scale_f32_16x16x128_f8f6f4 v[100:103], v[8:15], v[240:247], v[100:103], v200, v201 op_sel_hi:[0,0,0]
	v_mfma_scale_f32_16x16x128_f8f6f4 v[154:157], v[16:23], v[206:213], v[154:157], v200, v201 op_sel_hi:[0,0,0]
	v_mfma_scale_f32_16x16x128_f8f6f4 v[146:149], v[24:31], v[206:213], v[146:149], v200, v201 op_sel_hi:[0,0,0]
	v_mfma_scale_f32_16x16x128_f8f6f4 v[138:141], v[16:23], v[224:231], v[138:141], v200, v201 op_sel_hi:[0,0,0]
	v_mfma_scale_f32_16x16x128_f8f6f4 v[130:133], v[24:31], v[224:231], v[130:133], v200, v201 op_sel_hi:[0,0,0]
	v_mfma_scale_f32_16x16x128_f8f6f4 v[122:125], v[16:23], v[232:239], v[122:125], v200, v201 op_sel_hi:[0,0,0]
	v_mfma_scale_f32_16x16x128_f8f6f4 v[114:117], v[24:31], v[232:239], v[114:117], v200, v201 op_sel_hi:[0,0,0]
	v_mfma_scale_f32_16x16x128_f8f6f4 v[104:107], v[16:23], v[240:247], v[104:107], v200, v201 op_sel_hi:[0,0,0]
	v_mfma_scale_f32_16x16x128_f8f6f4 v[96:99], v[24:31], v[240:247], v[96:99], v200, v201 op_sel_hi:[0,0,0]
	s_barrier
	s_add_i32 s30, s30, s14
	v_lshl_add_u64 v[180:181], v[180:181], 0, s[56:57]
	s_mov_b32 m0, s30
	ds_read_b128 v[206:209], v169 offset:49152
	ds_read_b128 v[210:213], v169 offset:50176
	ds_read_b128 v[224:227], v169 offset:51200
	ds_read_b128 v[228:231], v169 offset:52224
	ds_read_b128 v[232:235], v169 offset:53248
	ds_read_b128 v[236:239], v169 offset:54272
	ds_read_b128 v[240:243], v169 offset:55296
	ds_read_b128 v[244:247], v169 offset:56320
	global_load_lds_dwordx4 v[180:181], off
	s_add_i32 m0, s30, 0x2000
	s_add_u32 s30, s74, 0x20080
	v_lshl_add_u64 v[180:181], v[182:183], 0, s[56:57]
	s_addc_u32 s31, s75, 0
	s_add_i32 s40, s45, s14
	global_load_lds_dwordx4 v[180:181], off
	v_lshl_add_u64 v[180:181], s[30:31], 0, v[164:165]
	s_mov_b32 m0, s40
	s_nop 0
	global_load_lds_dwordx4 v[180:181], off
	v_lshl_add_u64 v[180:181], s[30:31], 0, v[162:163]
	s_add_i32 m0, s40, 0x2000
	s_nop 0
	global_load_lds_dwordx4 v[180:181], off
	v_lshl_add_u64 v[180:181], v[184:185], 0, s[56:57]
	s_mov_b32 m0, s4
	s_nop 0
	global_load_lds_dwordx4 v[180:181], off
	v_lshl_add_u64 v[180:181], v[186:187], 0, s[56:57]
	s_mov_b32 m0, s51
	s_nop 0
	global_load_lds_dwordx4 v[180:181], off
	s_waitcnt vmcnt(8)
	s_waitcnt lgkmcnt(0)
	s_barrier
	s_waitcnt lgkmcnt(0)
	v_mfma_scale_f32_16x16x128_f8f6f4 v[92:95], v[0:7], v[206:213], v[92:95], v200, v201 op_sel_hi:[0,0,0]
	v_mfma_scale_f32_16x16x128_f8f6f4 v[84:87], v[8:15], v[206:213], v[84:87], v200, v201 op_sel_hi:[0,0,0]
	v_mfma_scale_f32_16x16x128_f8f6f4 v[76:79], v[0:7], v[224:231], v[76:79], v200, v201 op_sel_hi:[0,0,0]
	v_mfma_scale_f32_16x16x128_f8f6f4 v[68:71], v[8:15], v[224:231], v[68:71], v200, v201 op_sel_hi:[0,0,0]
	v_mfma_scale_f32_16x16x128_f8f6f4 v[60:63], v[0:7], v[232:239], v[60:63], v200, v201 op_sel_hi:[0,0,0]
	v_mfma_scale_f32_16x16x128_f8f6f4 v[52:55], v[8:15], v[232:239], v[52:55], v200, v201 op_sel_hi:[0,0,0]
	v_mfma_scale_f32_16x16x128_f8f6f4 v[44:47], v[0:7], v[240:247], v[44:47], v200, v201 op_sel_hi:[0,0,0]
	v_mfma_scale_f32_16x16x128_f8f6f4 v[36:39], v[8:15], v[240:247], v[36:39], v200, v201 op_sel_hi:[0,0,0]
	v_mfma_scale_f32_16x16x128_f8f6f4 v[88:91], v[16:23], v[206:213], v[88:91], v200, v201 op_sel_hi:[0,0,0]
	v_mfma_scale_f32_16x16x128_f8f6f4 v[80:83], v[24:31], v[206:213], v[80:83], v200, v201 op_sel_hi:[0,0,0]
	v_mfma_scale_f32_16x16x128_f8f6f4 v[72:75], v[16:23], v[224:231], v[72:75], v200, v201 op_sel_hi:[0,0,0]
	v_mfma_scale_f32_16x16x128_f8f6f4 v[64:67], v[24:31], v[224:231], v[64:67], v200, v201 op_sel_hi:[0,0,0]
	v_mfma_scale_f32_16x16x128_f8f6f4 v[56:59], v[16:23], v[232:239], v[56:59], v200, v201 op_sel_hi:[0,0,0]
	v_mfma_scale_f32_16x16x128_f8f6f4 v[48:51], v[24:31], v[232:239], v[48:51], v200, v201 op_sel_hi:[0,0,0]
	v_mfma_scale_f32_16x16x128_f8f6f4 v[40:43], v[16:23], v[240:247], v[40:43], v200, v201 op_sel_hi:[0,0,0]
	v_mfma_scale_f32_16x16x128_f8f6f4 v[32:35], v[24:31], v[240:247], v[32:35], v200, v201 op_sel_hi:[0,0,0]
	s_barrier
	s_add_i32 s49, s49, 2
	s_add_u32 s72, s72, 0x100
	s_addc_u32 s73, s73, 0
	s_cmp_gt_u32 s49, 5
	s_cbranch_scc1 .LBB0_1092

.Lpeel_down:
	s_add_u32 s30, s72, 0xfffe0080
	s_addc_u32 s31, s73, -1
	s_add_i32 s51, 0, 0x10000
	s_cmp_eq_u32 s50, 4
	s_cselect_b32 s77, s27, s31
	s_cselect_b32 s76, s37, s30
	s_cselect_b32 s75, s65, s49
	s_cselect_b32 s74, s64, s47
	s_add_i32 s58, 0, 0x14000
	v_add_u32_e32 v0, s51, v183
	v_add_u32_e32 v12, s58, v183
	ds_read_b128 v[16:19], v0
	ds_read_b128 v[20:23], v0 offset:1024
	ds_read_b128 v[24:27], v0 offset:2048
	ds_read_b128 v[28:31], v0 offset:3072
	ds_read_b128 v[0:3], v12
	ds_read_b128 v[4:7], v12 offset:1024
	ds_read_b128 v[8:11], v12 offset:2048
	ds_read_b128 v[12:15], v12 offset:3072
	v_lshl_add_u64 v[194:195], s[72:73], 0, v[168:169]
	s_add_i32 m0, s7, 0xc000
	ds_read_b128 v[174:177], v184
	ds_read_b128 v[178:181], v184 offset:1024
	ds_read_b128 v[186:189], v184 offset:2048
	ds_read_b128 v[190:193], v184 offset:3072
	ds_read_b128 v[206:209], v184 offset:4096
	ds_read_b128 v[210:213], v184 offset:5120
	ds_read_b128 v[216:219], v184 offset:6144
	ds_read_b128 v[220:223], v184 offset:7168
	global_load_lds_dwordx4 v[194:195], off
	v_lshl_add_u64 v[194:195], s[72:73], 0, v[170:171]
	s_add_i32 m0, s7, 0xe000
	s_nop 0
	global_load_lds_dwordx4 v[194:195], off
	s_waitcnt vmcnt(8)
	s_waitcnt lgkmcnt(0)
	s_barrier
	s_waitcnt lgkmcnt(0)
	v_mfma_scale_f32_16x16x128_f8f6f4 v[158:161], v[16:23], v[174:181], 0, v200, v201 op_sel_hi:[0,0,0]
	v_mfma_scale_f32_16x16x128_f8f6f4 v[154:157], v[24:31], v[174:181], 0, v200, v201 op_sel_hi:[0,0,0]
	v_mfma_scale_f32_16x16x128_f8f6f4 v[142:145], v[16:23], v[186:193], 0, v200, v201 op_sel_hi:[0,0,0]
	v_mfma_scale_f32_16x16x128_f8f6f4 v[138:141], v[24:31], v[186:193], 0, v200, v201 op_sel_hi:[0,0,0]
	v_mfma_scale_f32_16x16x128_f8f6f4 v[126:129], v[16:23], v[206:213], 0, v200, v201 op_sel_hi:[0,0,0]
	v_mfma_scale_f32_16x16x128_f8f6f4 v[122:125], v[24:31], v[206:213], 0, v200, v201 op_sel_hi:[0,0,0]
	v_mfma_scale_f32_16x16x128_f8f6f4 v[108:111], v[16:23], v[216:223], 0, v200, v201 op_sel_hi:[0,0,0]
	v_mfma_scale_f32_16x16x128_f8f6f4 v[104:107], v[24:31], v[216:223], 0, v200, v201 op_sel_hi:[0,0,0]
	v_mfma_scale_f32_16x16x128_f8f6f4 v[150:153], v[0:7], v[174:181], 0, v200, v201 op_sel_hi:[0,0,0]
	v_mfma_scale_f32_16x16x128_f8f6f4 v[146:149], v[8:15], v[174:181], 0, v200, v201 op_sel_hi:[0,0,0]
	v_mfma_scale_f32_16x16x128_f8f6f4 v[134:137], v[0:7], v[186:193], 0, v200, v201 op_sel_hi:[0,0,0]
	v_mfma_scale_f32_16x16x128_f8f6f4 v[130:133], v[8:15], v[186:193], 0, v200, v201 op_sel_hi:[0,0,0]
	v_mfma_scale_f32_16x16x128_f8f6f4 v[118:121], v[0:7], v[206:213], 0, v200, v201 op_sel_hi:[0,0,0]
	v_mfma_scale_f32_16x16x128_f8f6f4 v[114:117], v[8:15], v[206:213], 0, v200, v201 op_sel_hi:[0,0,0]
	v_mfma_scale_f32_16x16x128_f8f6f4 v[100:103], v[0:7], v[216:223], 0, v200, v201 op_sel_hi:[0,0,0]
	v_mfma_scale_f32_16x16x128_f8f6f4 v[96:99], v[8:15], v[216:223], 0, v200, v201 op_sel_hi:[0,0,0]
	s_barrier
	s_add_i32 s30, s51, s14
	v_lshl_add_u64 v[174:175], s[74:75], 0, v[112:113]
	s_mov_b32 m0, s30
	ds_read_b128 v[186:189], v184 offset:16384
	ds_read_b128 v[190:193], v184 offset:17408
	ds_read_b128 v[206:209], v184 offset:18432
	ds_read_b128 v[210:213], v184 offset:19456
	ds_read_b128 v[216:219], v184 offset:20480
	ds_read_b128 v[220:223], v184 offset:21504
	ds_read_b128 v[224:227], v184 offset:22528
	ds_read_b128 v[228:231], v184 offset:23552
	global_load_lds_dwordx4 v[174:175], off
	s_add_i32 m0, s30, 0x2000
	s_add_u32 s30, s74, 0x20000
	v_lshl_add_u64 v[176:177], s[74:75], 0, v[162:163]
	s_addc_u32 s31, s75, 0
	s_add_i32 s45, s58, s14
	global_load_lds_dwordx4 v[176:177], off
	v_lshl_add_u64 v[178:179], s[30:31], 0, v[112:113]
	s_mov_b32 m0, s45
	v_lshl_add_u64 v[180:181], s[76:77], 0, v[164:165]
	global_load_lds_dwordx4 v[178:179], off
	v_lshl_add_u64 v[178:179], s[30:31], 0, v[162:163]
	s_add_i32 m0, s45, 0x2000
	s_nop 0
	global_load_lds_dwordx4 v[178:179], off
	v_lshl_add_u64 v[178:179], s[76:77], 0, v[166:167]
	s_mov_b32 m0, s7
	s_nop 0
	global_load_lds_dwordx4 v[178:179], off
	s_mov_b32 m0, s25
	s_nop 0
	global_load_lds_dwordx4 v[180:181], off
	s_waitcnt vmcnt(8)
	s_waitcnt lgkmcnt(0)
	s_barrier
	s_waitcnt lgkmcnt(0)
	v_mfma_scale_f32_16x16x128_f8f6f4 v[92:95], v[16:23], v[186:193], 0, v200, v201 op_sel_hi:[0,0,0]
	v_mfma_scale_f32_16x16x128_f8f6f4 v[88:91], v[24:31], v[186:193], 0, v200, v201 op_sel_hi:[0,0,0]
	v_mfma_scale_f32_16x16x128_f8f6f4 v[76:79], v[16:23], v[206:213], 0, v200, v201 op_sel_hi:[0,0,0]
	v_mfma_scale_f32_16x16x128_f8f6f4 v[72:75], v[24:31], v[206:213], 0, v200, v201 op_sel_hi:[0,0,0]
	v_mfma_scale_f32_16x16x128_f8f6f4 v[60:63], v[16:23], v[216:223], 0, v200, v201 op_sel_hi:[0,0,0]
	v_mfma_scale_f32_16x16x128_f8f6f4 v[56:59], v[24:31], v[216:223], 0, v200, v201 op_sel_hi:[0,0,0]
	v_mfma_scale_f32_16x16x128_f8f6f4 v[44:47], v[16:23], v[224:231], 0, v200, v201 op_sel_hi:[0,0,0]
	v_mfma_scale_f32_16x16x128_f8f6f4 v[40:43], v[24:31], v[224:231], 0, v200, v201 op_sel_hi:[0,0,0]
	v_mfma_scale_f32_16x16x128_f8f6f4 v[84:87], v[0:7], v[186:193], 0, v200, v201 op_sel_hi:[0,0,0]
	v_mfma_scale_f32_16x16x128_f8f6f4 v[80:83], v[8:15], v[186:193], 0, v200, v201 op_sel_hi:[0,0,0]
	v_mfma_scale_f32_16x16x128_f8f6f4 v[68:71], v[0:7], v[206:213], 0, v200, v201 op_sel_hi:[0,0,0]
	v_mfma_scale_f32_16x16x128_f8f6f4 v[64:67], v[8:15], v[206:213], 0, v200, v201 op_sel_hi:[0,0,0]
	v_mfma_scale_f32_16x16x128_f8f6f4 v[52:55], v[0:7], v[216:223], 0, v200, v201 op_sel_hi:[0,0,0]
	v_mfma_scale_f32_16x16x128_f8f6f4 v[48:51], v[8:15], v[216:223], 0, v200, v201 op_sel_hi:[0,0,0]
	v_mfma_scale_f32_16x16x128_f8f6f4 v[36:39], v[0:7], v[224:231], 0, v200, v201 op_sel_hi:[0,0,0]
	v_mfma_scale_f32_16x16x128_f8f6f4 v[32:35], v[8:15], v[224:231], 0, v200, v201 op_sel_hi:[0,0,0]
	s_barrier
	s_add_i32 s45, 0, 0x18000
	s_add_i32 s51, 0, 0x1c000
	v_add_u32_e32 v12, s45, v183
	v_add_u32_e32 v28, s51, v183
	ds_read_b128 v[0:3], v12
	ds_read_b128 v[4:7], v12 offset:1024
	ds_read_b128 v[8:11], v12 offset:2048
	ds_read_b128 v[12:15], v12 offset:3072
	ds_read_b128 v[16:19], v28
	ds_read_b128 v[20:23], v28 offset:1024
	ds_read_b128 v[24:27], v28 offset:2048
	ds_read_b128 v[28:31], v28 offset:3072
	s_add_u32 s30, s76, 0x20000
	s_addc_u32 s31, s77, 0
	s_mov_b32 m0, s33
	v_lshl_add_u64 v[194:195], s[30:31], 0, v[166:167]
	ds_read_b128 v[186:189], v184 offset:32768
	ds_read_b128 v[190:193], v184 offset:33792
	ds_read_b128 v[206:209], v184 offset:34816
	ds_read_b128 v[210:213], v184 offset:35840
	ds_read_b128 v[216:219], v184 offset:36864
	ds_read_b128 v[220:223], v184 offset:37888
	ds_read_b128 v[224:227], v184 offset:38912
	ds_read_b128 v[228:231], v184 offset:39936
	global_load_lds_dwordx4 v[194:195], off
	v_lshl_add_u64 v[194:195], s[30:31], 0, v[164:165]
	s_mov_b32 m0, s34
	s_nop 0
	global_load_lds_dwordx4 v[194:195], off
	s_waitcnt vmcnt(8)
	s_waitcnt lgkmcnt(0)
	s_barrier
	s_waitcnt lgkmcnt(0)
	v_mfma_scale_f32_16x16x128_f8f6f4 v[158:161], v[0:7], v[186:193], v[158:161], v200, v201 op_sel_hi:[0,0,0]
	v_mfma_scale_f32_16x16x128_f8f6f4 v[154:157], v[8:15], v[186:193], v[154:157], v200, v201 op_sel_hi:[0,0,0]
	v_mfma_scale_f32_16x16x128_f8f6f4 v[142:145], v[0:7], v[206:213], v[142:145], v200, v201 op_sel_hi:[0,0,0]
	v_mfma_scale_f32_16x16x128_f8f6f4 v[138:141], v[8:15], v[206:213], v[138:141], v200, v201 op_sel_hi:[0,0,0]
	v_mfma_scale_f32_16x16x128_f8f6f4 v[126:129], v[0:7], v[216:223], v[126:129], v200, v201 op_sel_hi:[0,0,0]
	v_mfma_scale_f32_16x16x128_f8f6f4 v[122:125], v[8:15], v[216:223], v[122:125], v200, v201 op_sel_hi:[0,0,0]
	v_mfma_scale_f32_16x16x128_f8f6f4 v[108:111], v[0:7], v[224:231], v[108:111], v200, v201 op_sel_hi:[0,0,0]
	v_mfma_scale_f32_16x16x128_f8f6f4 v[104:107], v[8:15], v[224:231], v[104:107], v200, v201 op_sel_hi:[0,0,0]
	v_mfma_scale_f32_16x16x128_f8f6f4 v[150:153], v[16:23], v[186:193], v[150:153], v200, v201 op_sel_hi:[0,0,0]
	v_mfma_scale_f32_16x16x128_f8f6f4 v[146:149], v[24:31], v[186:193], v[146:149], v200, v201 op_sel_hi:[0,0,0]
	v_mfma_scale_f32_16x16x128_f8f6f4 v[134:137], v[16:23], v[206:213], v[134:137], v200, v201 op_sel_hi:[0,0,0]
	v_mfma_scale_f32_16x16x128_f8f6f4 v[130:133], v[24:31], v[206:213], v[130:133], v200, v201 op_sel_hi:[0,0,0]
	v_mfma_scale_f32_16x16x128_f8f6f4 v[118:121], v[16:23], v[216:223], v[118:121], v200, v201 op_sel_hi:[0,0,0]
	v_mfma_scale_f32_16x16x128_f8f6f4 v[114:117], v[24:31], v[216:223], v[114:117], v200, v201 op_sel_hi:[0,0,0]
	v_mfma_scale_f32_16x16x128_f8f6f4 v[100:103], v[16:23], v[224:231], v[100:103], v200, v201 op_sel_hi:[0,0,0]
	v_mfma_scale_f32_16x16x128_f8f6f4 v[96:99], v[24:31], v[224:231], v[96:99], v200, v201 op_sel_hi:[0,0,0]
	s_barrier
	s_add_i32 s30, s45, s14
	v_lshl_add_u64 v[174:175], v[174:175], 0, s[56:57]
	s_mov_b32 m0, s30
	ds_read_b128 v[186:189], v184 offset:49152
	ds_read_b128 v[190:193], v184 offset:50176
	ds_read_b128 v[206:209], v184 offset:51200
	ds_read_b128 v[210:213], v184 offset:52224
	ds_read_b128 v[216:219], v184 offset:53248
	ds_read_b128 v[220:223], v184 offset:54272
	ds_read_b128 v[224:227], v184 offset:55296
	ds_read_b128 v[228:231], v184 offset:56320
	global_load_lds_dwordx4 v[174:175], off
	s_add_i32 m0, s30, 0x2000
	s_add_u32 s30, s74, 0x20080
	v_lshl_add_u64 v[174:175], v[176:177], 0, s[56:57]
	s_addc_u32 s31, s75, 0
	s_add_i32 s45, s51, s14
	global_load_lds_dwordx4 v[174:175], off
	v_lshl_add_u64 v[174:175], s[30:31], 0, v[112:113]
	s_mov_b32 m0, s45
	s_nop 0
	global_load_lds_dwordx4 v[174:175], off
	v_lshl_add_u64 v[174:175], s[30:31], 0, v[162:163]
	s_add_i32 m0, s45, 0x2000
	s_nop 0
	global_load_lds_dwordx4 v[174:175], off
	v_lshl_add_u64 v[174:175], v[178:179], 0, s[56:57]
	s_mov_b32 m0, s4
	s_nop 0
	global_load_lds_dwordx4 v[174:175], off
	v_lshl_add_u64 v[174:175], v[180:181], 0, s[56:57]
	s_mov_b32 m0, s54
	s_nop 0
	global_load_lds_dwordx4 v[174:175], off
	s_waitcnt vmcnt(8)
	s_waitcnt lgkmcnt(0)
	s_barrier
	s_waitcnt lgkmcnt(0)
	v_mfma_scale_f32_16x16x128_f8f6f4 v[92:95], v[0:7], v[186:193], v[92:95], v200, v201 op_sel_hi:[0,0,0]
	v_mfma_scale_f32_16x16x128_f8f6f4 v[88:91], v[8:15], v[186:193], v[88:91], v200, v201 op_sel_hi:[0,0,0]
	v_mfma_scale_f32_16x16x128_f8f6f4 v[76:79], v[0:7], v[206:213], v[76:79], v200, v201 op_sel_hi:[0,0,0]
	v_mfma_scale_f32_16x16x128_f8f6f4 v[72:75], v[8:15], v[206:213], v[72:75], v200, v201 op_sel_hi:[0,0,0]
	v_mfma_scale_f32_16x16x128_f8f6f4 v[60:63], v[0:7], v[216:223], v[60:63], v200, v201 op_sel_hi:[0,0,0]
	v_mfma_scale_f32_16x16x128_f8f6f4 v[56:59], v[8:15], v[216:223], v[56:59], v200, v201 op_sel_hi:[0,0,0]
	v_mfma_scale_f32_16x16x128_f8f6f4 v[44:47], v[0:7], v[224:231], v[44:47], v200, v201 op_sel_hi:[0,0,0]
	v_mfma_scale_f32_16x16x128_f8f6f4 v[40:43], v[8:15], v[224:231], v[40:43], v200, v201 op_sel_hi:[0,0,0]
	v_mfma_scale_f32_16x16x128_f8f6f4 v[84:87], v[16:23], v[186:193], v[84:87], v200, v201 op_sel_hi:[0,0,0]
	v_mfma_scale_f32_16x16x128_f8f6f4 v[80:83], v[24:31], v[186:193], v[80:83], v200, v201 op_sel_hi:[0,0,0]
	v_mfma_scale_f32_16x16x128_f8f6f4 v[68:71], v[16:23], v[206:213], v[68:71], v200, v201 op_sel_hi:[0,0,0]
	v_mfma_scale_f32_16x16x128_f8f6f4 v[64:67], v[24:31], v[206:213], v[64:67], v200, v201 op_sel_hi:[0,0,0]
	v_mfma_scale_f32_16x16x128_f8f6f4 v[52:55], v[16:23], v[216:223], v[52:55], v200, v201 op_sel_hi:[0,0,0]
	v_mfma_scale_f32_16x16x128_f8f6f4 v[48:51], v[24:31], v[216:223], v[48:51], v200, v201 op_sel_hi:[0,0,0]
	v_mfma_scale_f32_16x16x128_f8f6f4 v[36:39], v[16:23], v[224:231], v[36:39], v200, v201 op_sel_hi:[0,0,0]
	v_mfma_scale_f32_16x16x128_f8f6f4 v[32:35], v[24:31], v[224:231], v[32:35], v200, v201 op_sel_hi:[0,0,0]
	s_barrier
	s_add_i32 s50, s50, 2
	s_add_u32 s72, s72, 0x100
	s_addc_u32 s73, s73, 0
	s_add_u32 s47, s47, 0x100
	s_addc_u32 s49, s49, 0
	s_cmp_gt_u32 s50, 5
.LBB0_1166:
	s_add_u32 s30, s72, 0xfffe0080
	s_addc_u32 s31, s73, -1
	s_add_i32 s51, 0, 0x10000
	s_cmp_eq_u32 s50, 4
	s_cselect_b32 s77, s27, s31
	s_cselect_b32 s76, s37, s30
	s_cselect_b32 s75, s65, s49
	s_cselect_b32 s74, s64, s47
	s_add_i32 s58, 0, 0x14000
	v_add_u32_e32 v0, s51, v183
	v_add_u32_e32 v12, s58, v183
	ds_read_b128 v[16:19], v0
	ds_read_b128 v[20:23], v0 offset:1024
	ds_read_b128 v[24:27], v0 offset:2048
	ds_read_b128 v[28:31], v0 offset:3072
	ds_read_b128 v[0:3], v12
	ds_read_b128 v[4:7], v12 offset:1024
	ds_read_b128 v[8:11], v12 offset:2048
	ds_read_b128 v[12:15], v12 offset:3072
	v_lshl_add_u64 v[194:195], s[72:73], 0, v[168:169]
	s_add_i32 m0, s7, 0xc000
	ds_read_b128 v[174:177], v184
	ds_read_b128 v[178:181], v184 offset:1024
	ds_read_b128 v[186:189], v184 offset:2048
	ds_read_b128 v[190:193], v184 offset:3072
	ds_read_b128 v[206:209], v184 offset:4096
	ds_read_b128 v[210:213], v184 offset:5120
	ds_read_b128 v[216:219], v184 offset:6144
	ds_read_b128 v[220:223], v184 offset:7168
	global_load_lds_dwordx4 v[194:195], off
	v_lshl_add_u64 v[194:195], s[72:73], 0, v[170:171]
	s_add_i32 m0, s7, 0xe000
	s_nop 0
	global_load_lds_dwordx4 v[194:195], off
	s_waitcnt vmcnt(8)
	s_waitcnt lgkmcnt(0)
	s_barrier
	s_waitcnt lgkmcnt(0)
	v_mfma_scale_f32_16x16x128_f8f6f4 v[158:161], v[16:23], v[174:181], v[158:161], v200, v201 op_sel_hi:[0,0,0]
	v_mfma_scale_f32_16x16x128_f8f6f4 v[154:157], v[24:31], v[174:181], v[154:157], v200, v201 op_sel_hi:[0,0,0]
	v_mfma_scale_f32_16x16x128_f8f6f4 v[142:145], v[16:23], v[186:193], v[142:145], v200, v201 op_sel_hi:[0,0,0]
	v_mfma_scale_f32_16x16x128_f8f6f4 v[138:141], v[24:31], v[186:193], v[138:141], v200, v201 op_sel_hi:[0,0,0]
	v_mfma_scale_f32_16x16x128_f8f6f4 v[126:129], v[16:23], v[206:213], v[126:129], v200, v201 op_sel_hi:[0,0,0]
	v_mfma_scale_f32_16x16x128_f8f6f4 v[122:125], v[24:31], v[206:213], v[122:125], v200, v201 op_sel_hi:[0,0,0]
	v_mfma_scale_f32_16x16x128_f8f6f4 v[108:111], v[16:23], v[216:223], v[108:111], v200, v201 op_sel_hi:[0,0,0]
	v_mfma_scale_f32_16x16x128_f8f6f4 v[104:107], v[24:31], v[216:223], v[104:107], v200, v201 op_sel_hi:[0,0,0]
	v_mfma_scale_f32_16x16x128_f8f6f4 v[150:153], v[0:7], v[174:181], v[150:153], v200, v201 op_sel_hi:[0,0,0]
	v_mfma_scale_f32_16x16x128_f8f6f4 v[146:149], v[8:15], v[174:181], v[146:149], v200, v201 op_sel_hi:[0,0,0]
	v_mfma_scale_f32_16x16x128_f8f6f4 v[134:137], v[0:7], v[186:193], v[134:137], v200, v201 op_sel_hi:[0,0,0]
	v_mfma_scale_f32_16x16x128_f8f6f4 v[130:133], v[8:15], v[186:193], v[130:133], v200, v201 op_sel_hi:[0,0,0]
	v_mfma_scale_f32_16x16x128_f8f6f4 v[118:121], v[0:7], v[206:213], v[118:121], v200, v201 op_sel_hi:[0,0,0]
	v_mfma_scale_f32_16x16x128_f8f6f4 v[114:117], v[8:15], v[206:213], v[114:117], v200, v201 op_sel_hi:[0,0,0]
	v_mfma_scale_f32_16x16x128_f8f6f4 v[100:103], v[0:7], v[216:223], v[100:103], v200, v201 op_sel_hi:[0,0,0]
	v_mfma_scale_f32_16x16x128_f8f6f4 v[96:99], v[8:15], v[216:223], v[96:99], v200, v201 op_sel_hi:[0,0,0]
	s_barrier
	s_add_i32 s30, s51, s14
	v_lshl_add_u64 v[174:175], s[74:75], 0, v[112:113]
	s_mov_b32 m0, s30
	ds_read_b128 v[186:189], v184 offset:16384
	ds_read_b128 v[190:193], v184 offset:17408
	ds_read_b128 v[206:209], v184 offset:18432
	ds_read_b128 v[210:213], v184 offset:19456
	ds_read_b128 v[216:219], v184 offset:20480
	ds_read_b128 v[220:223], v184 offset:21504
	ds_read_b128 v[224:227], v184 offset:22528
	ds_read_b128 v[228:231], v184 offset:23552
	global_load_lds_dwordx4 v[174:175], off
	s_add_i32 m0, s30, 0x2000
	s_add_u32 s30, s74, 0x20000
	v_lshl_add_u64 v[176:177], s[74:75], 0, v[162:163]
	s_addc_u32 s31, s75, 0
	s_add_i32 s45, s58, s14
	global_load_lds_dwordx4 v[176:177], off
	v_lshl_add_u64 v[178:179], s[30:31], 0, v[112:113]
	s_mov_b32 m0, s45
	v_lshl_add_u64 v[180:181], s[76:77], 0, v[164:165]
	global_load_lds_dwordx4 v[178:179], off
	v_lshl_add_u64 v[178:179], s[30:31], 0, v[162:163]
	s_add_i32 m0, s45, 0x2000
	s_nop 0
	global_load_lds_dwordx4 v[178:179], off
	v_lshl_add_u64 v[178:179], s[76:77], 0, v[166:167]
	s_mov_b32 m0, s7
	s_nop 0
	global_load_lds_dwordx4 v[178:179], off
	s_mov_b32 m0, s25
	s_nop 0
	global_load_lds_dwordx4 v[180:181], off
	s_waitcnt vmcnt(8)
	s_waitcnt lgkmcnt(0)
	s_barrier
	s_waitcnt lgkmcnt(0)
	v_mfma_scale_f32_16x16x128_f8f6f4 v[92:95], v[16:23], v[186:193], v[92:95], v200, v201 op_sel_hi:[0,0,0]
	v_mfma_scale_f32_16x16x128_f8f6f4 v[88:91], v[24:31], v[186:193], v[88:91], v200, v201 op_sel_hi:[0,0,0]
	v_mfma_scale_f32_16x16x128_f8f6f4 v[76:79], v[16:23], v[206:213], v[76:79], v200, v201 op_sel_hi:[0,0,0]
	v_mfma_scale_f32_16x16x128_f8f6f4 v[72:75], v[24:31], v[206:213], v[72:75], v200, v201 op_sel_hi:[0,0,0]
	v_mfma_scale_f32_16x16x128_f8f6f4 v[60:63], v[16:23], v[216:223], v[60:63], v200, v201 op_sel_hi:[0,0,0]
	v_mfma_scale_f32_16x16x128_f8f6f4 v[56:59], v[24:31], v[216:223], v[56:59], v200, v201 op_sel_hi:[0,0,0]
	v_mfma_scale_f32_16x16x128_f8f6f4 v[44:47], v[16:23], v[224:231], v[44:47], v200, v201 op_sel_hi:[0,0,0]
	v_mfma_scale_f32_16x16x128_f8f6f4 v[40:43], v[24:31], v[224:231], v[40:43], v200, v201 op_sel_hi:[0,0,0]
	v_mfma_scale_f32_16x16x128_f8f6f4 v[84:87], v[0:7], v[186:193], v[84:87], v200, v201 op_sel_hi:[0,0,0]
	v_mfma_scale_f32_16x16x128_f8f6f4 v[80:83], v[8:15], v[186:193], v[80:83], v200, v201 op_sel_hi:[0,0,0]
	v_mfma_scale_f32_16x16x128_f8f6f4 v[68:71], v[0:7], v[206:213], v[68:71], v200, v201 op_sel_hi:[0,0,0]
	v_mfma_scale_f32_16x16x128_f8f6f4 v[64:67], v[8:15], v[206:213], v[64:67], v200, v201 op_sel_hi:[0,0,0]
	v_mfma_scale_f32_16x16x128_f8f6f4 v[52:55], v[0:7], v[216:223], v[52:55], v200, v201 op_sel_hi:[0,0,0]
	v_mfma_scale_f32_16x16x128_f8f6f4 v[48:51], v[8:15], v[216:223], v[48:51], v200, v201 op_sel_hi:[0,0,0]
	v_mfma_scale_f32_16x16x128_f8f6f4 v[36:39], v[0:7], v[224:231], v[36:39], v200, v201 op_sel_hi:[0,0,0]
	v_mfma_scale_f32_16x16x128_f8f6f4 v[32:35], v[8:15], v[224:231], v[32:35], v200, v201 op_sel_hi:[0,0,0]
	s_barrier
	s_add_i32 s45, 0, 0x18000
	s_add_i32 s51, 0, 0x1c000
	v_add_u32_e32 v12, s45, v183
	v_add_u32_e32 v28, s51, v183
	ds_read_b128 v[0:3], v12
	ds_read_b128 v[4:7], v12 offset:1024
	ds_read_b128 v[8:11], v12 offset:2048
	ds_read_b128 v[12:15], v12 offset:3072
	ds_read_b128 v[16:19], v28
	ds_read_b128 v[20:23], v28 offset:1024
	ds_read_b128 v[24:27], v28 offset:2048
	ds_read_b128 v[28:31], v28 offset:3072
	s_add_u32 s30, s76, 0x20000
	s_addc_u32 s31, s77, 0
	s_mov_b32 m0, s33
	v_lshl_add_u64 v[194:195], s[30:31], 0, v[166:167]
	ds_read_b128 v[186:189], v184 offset:32768
	ds_read_b128 v[190:193], v184 offset:33792
	ds_read_b128 v[206:209], v184 offset:34816
	ds_read_b128 v[210:213], v184 offset:35840
	ds_read_b128 v[216:219], v184 offset:36864
	ds_read_b128 v[220:223], v184 offset:37888
	ds_read_b128 v[224:227], v184 offset:38912
	ds_read_b128 v[228:231], v184 offset:39936
	global_load_lds_dwordx4 v[194:195], off
	v_lshl_add_u64 v[194:195], s[30:31], 0, v[164:165]
	s_mov_b32 m0, s34
	s_nop 0
	global_load_lds_dwordx4 v[194:195], off
	s_waitcnt vmcnt(8)
	s_waitcnt lgkmcnt(0)
	s_barrier
	s_waitcnt lgkmcnt(0)
	v_mfma_scale_f32_16x16x128_f8f6f4 v[158:161], v[0:7], v[186:193], v[158:161], v200, v201 op_sel_hi:[0,0,0]
	v_mfma_scale_f32_16x16x128_f8f6f4 v[154:157], v[8:15], v[186:193], v[154:157], v200, v201 op_sel_hi:[0,0,0]
	v_mfma_scale_f32_16x16x128_f8f6f4 v[142:145], v[0:7], v[206:213], v[142:145], v200, v201 op_sel_hi:[0,0,0]
	v_mfma_scale_f32_16x16x128_f8f6f4 v[138:141], v[8:15], v[206:213], v[138:141], v200, v201 op_sel_hi:[0,0,0]
	v_mfma_scale_f32_16x16x128_f8f6f4 v[126:129], v[0:7], v[216:223], v[126:129], v200, v201 op_sel_hi:[0,0,0]
	v_mfma_scale_f32_16x16x128_f8f6f4 v[122:125], v[8:15], v[216:223], v[122:125], v200, v201 op_sel_hi:[0,0,0]
	v_mfma_scale_f32_16x16x128_f8f6f4 v[108:111], v[0:7], v[224:231], v[108:111], v200, v201 op_sel_hi:[0,0,0]
	v_mfma_scale_f32_16x16x128_f8f6f4 v[104:107], v[8:15], v[224:231], v[104:107], v200, v201 op_sel_hi:[0,0,0]
	v_mfma_scale_f32_16x16x128_f8f6f4 v[150:153], v[16:23], v[186:193], v[150:153], v200, v201 op_sel_hi:[0,0,0]
	v_mfma_scale_f32_16x16x128_f8f6f4 v[146:149], v[24:31], v[186:193], v[146:149], v200, v201 op_sel_hi:[0,0,0]
	v_mfma_scale_f32_16x16x128_f8f6f4 v[134:137], v[16:23], v[206:213], v[134:137], v200, v201 op_sel_hi:[0,0,0]
	v_mfma_scale_f32_16x16x128_f8f6f4 v[130:133], v[24:31], v[206:213], v[130:133], v200, v201 op_sel_hi:[0,0,0]
	v_mfma_scale_f32_16x16x128_f8f6f4 v[118:121], v[16:23], v[216:223], v[118:121], v200, v201 op_sel_hi:[0,0,0]
	v_mfma_scale_f32_16x16x128_f8f6f4 v[114:117], v[24:31], v[216:223], v[114:117], v200, v201 op_sel_hi:[0,0,0]
	v_mfma_scale_f32_16x16x128_f8f6f4 v[100:103], v[16:23], v[224:231], v[100:103], v200, v201 op_sel_hi:[0,0,0]
	v_mfma_scale_f32_16x16x128_f8f6f4 v[96:99], v[24:31], v[224:231], v[96:99], v200, v201 op_sel_hi:[0,0,0]
	s_barrier
	s_add_i32 s30, s45, s14
	v_lshl_add_u64 v[174:175], v[174:175], 0, s[56:57]
	s_mov_b32 m0, s30
	ds_read_b128 v[186:189], v184 offset:49152
	ds_read_b128 v[190:193], v184 offset:50176
	ds_read_b128 v[206:209], v184 offset:51200
	ds_read_b128 v[210:213], v184 offset:52224
	ds_read_b128 v[216:219], v184 offset:53248
	ds_read_b128 v[220:223], v184 offset:54272
	ds_read_b128 v[224:227], v184 offset:55296
	ds_read_b128 v[228:231], v184 offset:56320
	global_load_lds_dwordx4 v[174:175], off
	s_add_i32 m0, s30, 0x2000
	s_add_u32 s30, s74, 0x20080
	v_lshl_add_u64 v[174:175], v[176:177], 0, s[56:57]
	s_addc_u32 s31, s75, 0
	s_add_i32 s45, s51, s14
	global_load_lds_dwordx4 v[174:175], off
	v_lshl_add_u64 v[174:175], s[30:31], 0, v[112:113]
	s_mov_b32 m0, s45
	s_nop 0
	global_load_lds_dwordx4 v[174:175], off
	v_lshl_add_u64 v[174:175], s[30:31], 0, v[162:163]
	s_add_i32 m0, s45, 0x2000
	s_nop 0
	global_load_lds_dwordx4 v[174:175], off
	v_lshl_add_u64 v[174:175], v[178:179], 0, s[56:57]
	s_mov_b32 m0, s4
	s_nop 0
	global_load_lds_dwordx4 v[174:175], off
	v_lshl_add_u64 v[174:175], v[180:181], 0, s[56:57]
	s_mov_b32 m0, s54
	s_nop 0
	global_load_lds_dwordx4 v[174:175], off
	s_waitcnt vmcnt(8)
	s_waitcnt lgkmcnt(0)
	s_barrier
	s_waitcnt lgkmcnt(0)
	v_mfma_scale_f32_16x16x128_f8f6f4 v[92:95], v[0:7], v[186:193], v[92:95], v200, v201 op_sel_hi:[0,0,0]
	v_mfma_scale_f32_16x16x128_f8f6f4 v[88:91], v[8:15], v[186:193], v[88:91], v200, v201 op_sel_hi:[0,0,0]
	v_mfma_scale_f32_16x16x128_f8f6f4 v[76:79], v[0:7], v[206:213], v[76:79], v200, v201 op_sel_hi:[0,0,0]
	v_mfma_scale_f32_16x16x128_f8f6f4 v[72:75], v[8:15], v[206:213], v[72:75], v200, v201 op_sel_hi:[0,0,0]
	v_mfma_scale_f32_16x16x128_f8f6f4 v[60:63], v[0:7], v[216:223], v[60:63], v200, v201 op_sel_hi:[0,0,0]
	v_mfma_scale_f32_16x16x128_f8f6f4 v[56:59], v[8:15], v[216:223], v[56:59], v200, v201 op_sel_hi:[0,0,0]
	v_mfma_scale_f32_16x16x128_f8f6f4 v[44:47], v[0:7], v[224:231], v[44:47], v200, v201 op_sel_hi:[0,0,0]
	v_mfma_scale_f32_16x16x128_f8f6f4 v[40:43], v[8:15], v[224:231], v[40:43], v200, v201 op_sel_hi:[0,0,0]
	v_mfma_scale_f32_16x16x128_f8f6f4 v[84:87], v[16:23], v[186:193], v[84:87], v200, v201 op_sel_hi:[0,0,0]
	v_mfma_scale_f32_16x16x128_f8f6f4 v[80:83], v[24:31], v[186:193], v[80:83], v200, v201 op_sel_hi:[0,0,0]
	v_mfma_scale_f32_16x16x128_f8f6f4 v[68:71], v[16:23], v[206:213], v[68:71], v200, v201 op_sel_hi:[0,0,0]
	v_mfma_scale_f32_16x16x128_f8f6f4 v[64:67], v[24:31], v[206:213], v[64:67], v200, v201 op_sel_hi:[0,0,0]
	v_mfma_scale_f32_16x16x128_f8f6f4 v[52:55], v[16:23], v[216:223], v[52:55], v200, v201 op_sel_hi:[0,0,0]
	v_mfma_scale_f32_16x16x128_f8f6f4 v[48:51], v[24:31], v[216:223], v[48:51], v200, v201 op_sel_hi:[0,0,0]
	v_mfma_scale_f32_16x16x128_f8f6f4 v[36:39], v[16:23], v[224:231], v[36:39], v200, v201 op_sel_hi:[0,0,0]
	v_mfma_scale_f32_16x16x128_f8f6f4 v[32:35], v[24:31], v[224:231], v[32:35], v200, v201 op_sel_hi:[0,0,0]
	s_barrier
	s_add_i32 s50, s50, 2
	s_add_u32 s72, s72, 0x100
	s_addc_u32 s73, s73, 0
	s_add_u32 s47, s47, 0x100
	s_addc_u32 s49, s49, 0
	s_cmp_gt_u32 s50, 5
	s_cbranch_scc0 .LBB0_1166
	s_and_b64 vcc, exec, s[42:43]
	s_movk_i32 s44, 0xff
	v_readlane_b32 s45, v255, 19
	s_cbranch_vccz .LBB0_1169
	s_barrier
